# RG-LRU: waves 4-7 run the next chunk's MFMAs right after the exchange barrier (ahead of the chunk tail) so that the two waves of a SIMD alternate MFMA and VALU work; one barrier per chunk
# speedup vs baseline: 1.0094x; 1.0094x over previous
.LBB0_1451:
	s_load_dwordx4 s[0:3], s[8:9], 0x138
	s_waitcnt lgkmcnt(0)
	s_mov_b64 s[4:5], s[0:1]
	s_cmp_lt_i32 s4, 12
	s_cselect_b64 s[0:1], -1, 0
	s_cmp_gt_i32 s5, 11
	s_cselect_b64 s[2:3], -1, 0
	s_and_b64 s[0:1], s[0:1], s[2:3]
	s_andn2_b64 vcc, exec, s[0:1]
	s_cbranch_vccnz .LBB0_1535
	s_mov_b64 s[24:25], s[8:9]
	v_mbcnt_lo_u32_b32 v202, -1, 0
	v_mbcnt_hi_u32_b32 v202, -1, v202
	s_load_dword s0, s[8:9], 0x148
	s_waitcnt lgkmcnt(0)
	v_writelane_b32 v241, s0, 18
	s_nop 1
	v_writelane_b32 v241, s1, 19
	s_add_u32 s0, s8, 0x148
	s_addc_u32 s1, s9, 0
	v_writelane_b32 v241, s0, 34
	s_nop 1
	v_writelane_b32 v241, s1, 35
	v_readlane_b32 s0, v243, 0
	s_cmpk_gt_i32 s0, 0xff
	v_readlane_b32 s1, v243, 1
	s_cbranch_scc1 .LBB0_1482
	v_readlane_b32 s0, v243, 7
	v_readlane_b32 s1, v243, 8
	v_readlane_b32 s4, v243, 0
	v_readlane_b32 s6, v243, 12
	s_load_dwordx2 s[2:3], s[0:1], 0x130
	s_lshr_b32 s7, s6, 2
	s_and_b32 s8, s6, 3
	s_bfe_u32 s11, s4, 0x20003
	s_lshr_b32 s50, s4, 5
	s_lshl_b32 s50, s50, 3
	s_and_b32 s51, s4, 7
	s_or_b32 s50, s50, s51
	s_lshr_b32 s9, s50, 2
	s_and_b32 s10, s50, 3
	v_and_b32_e32 v160, 15, v202
	v_lshrrev_b32_e32 v161, 4, v202
	v_lshlrev_b32_e32 v209, 2, v202
	s_lshl_b32 s50, s7, 15
	v_xor_b32_e32 v178, v161, v160
	v_lshlrev_b32_e32 v178, 4, v178
	v_lshl_add_u32 v162, v160, 9, v178
	v_add_u32_e32 v162, s50, v162
	s_lshl_b32 s51, s11, 6
	s_lshl_b32 s52, s8, 4
	s_add_i32 s51, s51, s52
	v_add_u32_e32 v179, s51, v160
	v_lshrrev_b32_e32 v180, 3, v179
	v_and_b32_e32 v181, 7, v179
	v_lshlrev_b32_e32 v181, 1, v181
	v_lshlrev_b32_e32 v182, 2, v161
	v_add_u32_e32 v183, 0, v182
	v_xor_b32_e32 v184, v180, v183
	v_lshlrev_b32_e32 v184, 4, v184
	v_lshl_add_u32 v184, v183, 9, v184
	v_add3_u32 v165, v184, v181, s50
	v_add_u32_e32 v183, 1, v182
	v_xor_b32_e32 v184, v180, v183
	v_lshlrev_b32_e32 v184, 4, v184
	v_lshl_add_u32 v184, v183, 9, v184
	v_add3_u32 v166, v184, v181, s50
	v_add_u32_e32 v183, 2, v182
	v_xor_b32_e32 v184, v180, v183
	v_lshlrev_b32_e32 v184, 4, v184
	v_lshl_add_u32 v184, v183, 9, v184
	v_add3_u32 v167, v184, v181, s50
	v_add_u32_e32 v183, 3, v182
	v_xor_b32_e32 v184, v180, v183
	v_lshlrev_b32_e32 v184, 4, v184
	v_lshl_add_u32 v184, v183, 9, v184
	v_add3_u32 v168, v184, v181, s50
	v_lshrrev_b32_e32 v185, 5, v202
	v_and_b32_e32 v186, 31, v202
	s_lshl_b32 s51, s6, 4
	v_add_u32_e32 v187, 0, v185
	v_xor_b32_e32 v188, v186, v187
	v_lshlrev_b32_e32 v188, 4, v188
	v_add_u32_e32 v187, s51, v187
	v_lshl_add_u32 v211, v187, 11, v188
	v_add_u32_e32 v187, 2, v185
	v_xor_b32_e32 v188, v186, v187
	v_lshlrev_b32_e32 v188, 4, v188
	v_add_u32_e32 v187, s51, v187
	v_lshl_add_u32 v212, v187, 11, v188
	v_add_u32_e32 v187, 4, v185
	v_xor_b32_e32 v188, v186, v187
	v_lshlrev_b32_e32 v188, 4, v188
	v_add_u32_e32 v187, s51, v187
	v_lshl_add_u32 v213, v187, 11, v188
	v_add_u32_e32 v187, 6, v185
	v_xor_b32_e32 v188, v186, v187
	v_lshlrev_b32_e32 v188, 4, v188
	v_add_u32_e32 v187, s51, v187
	v_lshl_add_u32 v214, v187, 11, v188
	v_add_u32_e32 v187, 8, v185
	v_xor_b32_e32 v188, v186, v187
	v_lshlrev_b32_e32 v188, 4, v188
	v_add_u32_e32 v187, s51, v187
	v_lshl_add_u32 v215, v187, 11, v188
	v_add_u32_e32 v187, 10, v185
	v_xor_b32_e32 v188, v186, v187
	v_lshlrev_b32_e32 v188, 4, v188
	v_add_u32_e32 v187, s51, v187
	v_lshl_add_u32 v216, v187, 11, v188
	v_add_u32_e32 v187, 12, v185
	v_xor_b32_e32 v188, v186, v187
	v_lshlrev_b32_e32 v188, 4, v188
	v_add_u32_e32 v187, s51, v187
	v_lshl_add_u32 v217, v187, 11, v188
	v_add_u32_e32 v187, 14, v185
	v_xor_b32_e32 v188, v186, v187
	v_lshlrev_b32_e32 v188, 4, v188
	v_add_u32_e32 v187, s51, v187
	v_lshl_add_u32 v218, v187, 11, v188
	s_lshl_b32 s51, s6, 7
	s_add_i32 s51, s51, 0x20000
	v_lshl_add_u32 v207, v160, 3, s51
	s_lshl_b32 s51, s8, 7
	s_add_i32 s51, s51, 0x20000
	v_lshl_add_u32 v208, v160, 3, s51
	s_lshl_b32 s51, s7, 6
	v_add_u32_e32 v189, s51, v182
	s_lshl_b32 s51, s8, 4
	v_add_u32_e32 v190, s51, v160
	v_lshlrev_b32_e32 v190, 1, v190
	v_lshl_add_u32 v210, v189, 11, v190
	s_waitcnt lgkmcnt(0)
	s_lshl_b32 s50, s10, 9
	s_add_u32 s16, s2, s50
	s_addc_u32 s17, s3, 0
	s_add_u32 s16, s16, 0x1b900000
	s_addc_u32 s17, s17, 0
	s_lshl_b32 s50, s10, 9
	s_lshl_b32 s51, s11, 7
	s_add_i32 s50, s50, s51
	s_add_u32 s18, s2, s50
	s_addc_u32 s19, s3, 0
	s_add_u32 s18, s18, 0x13100000
	s_addc_u32 s19, s19, 0
	s_add_u32 s20, s2, s50
	s_addc_u32 s21, s3, 0
	s_add_u32 s20, s20, 0x29100000
	s_addc_u32 s21, s21, 0
	s_lshl_b32 s50, s4, 18
	s_add_u32 s22, s2, s50
	s_addc_u32 s23, s3, 0
	s_add_u32 s22, s22, 0x20100000
	s_addc_u32 s23, s23, 0
	s_lshl_b32 s50, s10, 10
	s_lshl_b32 s51, s11, 6
	s_add_i32 s50, s50, s51
	s_lshl_b32 s51, s8, 4
	s_add_i32 s50, s50, s51
	s_add_i32 s50, s50, 0
	s_lshl_b32 s50, s50, 9
	s_add_u32 s46, s2, s50
	s_addc_u32 s47, s3, 0
	s_add_u32 s46, s46, 0x1000000
	s_addc_u32 s47, s47, 0
	s_add_u32 s48, s46, 0x20000
	s_addc_u32 s49, s47, 0
	v_lshlrev_b32_e32 v178, 9, v160
	v_lshl_add_u32 v178, v161, 4, v178
	global_load_dwordx4 v[0:3], v178, s[46:47]
	global_load_dwordx4 v[4:7], v178, s[46:47] offset:64
	global_load_dwordx4 v[8:11], v178, s[46:47] offset:128
	global_load_dwordx4 v[12:15], v178, s[46:47] offset:192
	global_load_dwordx4 v[16:19], v178, s[46:47] offset:256
	global_load_dwordx4 v[20:23], v178, s[46:47] offset:320
	global_load_dwordx4 v[24:27], v178, s[46:47] offset:384
	global_load_dwordx4 v[28:31], v178, s[46:47] offset:448
	global_load_dwordx4 v[32:35], v178, s[48:49]
	global_load_dwordx4 v[36:39], v178, s[48:49] offset:64
	global_load_dwordx4 v[40:43], v178, s[48:49] offset:128
	global_load_dwordx4 v[44:47], v178, s[48:49] offset:192
	global_load_dwordx4 v[48:51], v178, s[48:49] offset:256
	global_load_dwordx4 v[52:55], v178, s[48:49] offset:320
	global_load_dwordx4 v[56:59], v178, s[48:49] offset:384
	global_load_dwordx4 v[60:63], v178, s[48:49] offset:448
	s_load_dwordx2 s[46:47], s[0:1], 0xa0
	s_load_dwordx2 s[48:49], s[0:1], 0xb0
	s_load_dwordx2 s[40:41], s[0:1], 0xb8
	s_lshl_b32 s50, s10, 8
	s_lshl_b32 s51, s11, 6
	s_add_i32 s50, s50, s51
	s_lshl_b32 s51, s8, 4
	s_add_i32 s50, s50, s51
	v_add_u32_e32 v179, s50, v160
	v_lshlrev_b32_e32 v179, 2, v179
	s_waitcnt lgkmcnt(0)
	global_load_dword v173, v179, s[46:47]
	global_load_dword v174, v179, s[48:49]
	global_load_dword v175, v179, s[40:41]
	v_cmp_le_u32_e64 s[34:35], 16, v202
	v_cmp_le_u32_e64 s[36:37], 32, v202
	v_add_u32_e32 v204, -16, v202
	v_add_u32_e32 v205, -32, v202
	v_add_u32_e32 v206, 48, v160
	s_cmp_eq_u32 s7, 1
	s_cselect_b64 s[38:39], -1, 0
	v_and_b32_e32 v204, 63, v204
	v_lshlrev_b32_e32 v204, 2, v204
	v_and_b32_e32 v205, 63, v205
	v_lshlrev_b32_e32 v205, 2, v205
	v_and_b32_e32 v206, 63, v206
	v_lshlrev_b32_e32 v206, 2, v206
	v_mov_b32_e32 v176, 0
	s_mov_b32 s53, 0xbfb8aa3b
	s_waitcnt vmcnt(0)
	v_mul_f32_e32 v173, s53, v173
	v_mul_f32_e32 v174, s53, v174
	v_mul_f32_e32 v175, s53, v175
	v_exp_f32_e32 v175, v175
	s_nop 0
	v_add_f32_e32 v180, 1.0, v175
	v_log_f32_e32 v180, v180
	v_mov_b32_e32 v181, 0x3eaaaaab
	v_fma_f32 v181, v175, v181, -0.5
	v_fma_f32 v181, v175, v181, 1.0
	v_mul_f32_e32 v181, v175, v181
	v_mul_f32_e32 v181, 0x3fb8aa3b, v181
	v_cmp_gt_f32_e32 vcc, 0x3cf5c28f, v175
	s_nop 1
	v_cndmask_b32_e32 v175, v180, v181, vcc
	v_mul_f32_e32 v175, 0xc1000000, v175
	s_mov_b32 s13, 0
	s_barrier
	s_cmp_lt_u32 s13, 2
	s_lshl_b32 s50, s13, 7
	s_lshl_b32 s51, s9, 8
	s_add_i32 s51, s51, 0x8000
	s_add_i32 s51, s51, s50
	s_lshl_b32 s59, s9, 11
	s_add_i32 s59, s59, s50
	s_addk_i32 s59, 0xff00
	s_cmp_lt_u32 s13, 2
	s_cselect_b32 s59, s51, s59
	s_lshl_b32 s52, s59, 11
	s_add_u32 s46, s16, s52
	s_addc_u32 s47, s17, 0
	s_lshl_b32 s52, s6, 13
	s_mov_b32 m0, s52
	s_add_i32 s52, s52, 0x400
	global_load_lds_dwordx4 v211, s[46:47]
	s_mov_b32 m0, s52
	s_add_i32 s52, s52, 0x400
	global_load_lds_dwordx4 v212, s[46:47]
	s_mov_b32 m0, s52
	s_add_i32 s52, s52, 0x400
	global_load_lds_dwordx4 v213, s[46:47]
	s_mov_b32 m0, s52
	s_add_i32 s52, s52, 0x400
	global_load_lds_dwordx4 v214, s[46:47]
	s_mov_b32 m0, s52
	s_add_i32 s52, s52, 0x400
	global_load_lds_dwordx4 v215, s[46:47]
	s_mov_b32 m0, s52
	s_add_i32 s52, s52, 0x400
	global_load_lds_dwordx4 v216, s[46:47]
	s_mov_b32 m0, s52
	s_add_i32 s52, s52, 0x400
	global_load_lds_dwordx4 v217, s[46:47]
	s_mov_b32 m0, s52
	s_nop 0
	global_load_lds_dwordx4 v218, s[46:47]
	s_mov_b32 s58, 1
	s_cmp_lt_u32 s58, 2
	s_lshl_b32 s50, s58, 7
	s_lshl_b32 s51, s9, 8
	s_add_i32 s51, s51, 0x8000
	s_add_i32 s51, s51, s50
	s_lshl_b32 s59, s9, 11
	s_add_i32 s59, s59, s50
	s_addk_i32 s59, 0xff00
	s_cmp_lt_u32 s58, 2
	s_cselect_b32 s59, s51, s59
	s_lshl_b32 s52, s59, 11
	s_add_u32 s46, s16, s52
	s_addc_u32 s47, s17, 0
	s_lshl_b32 s52, s6, 13
	s_add_i32 s52, s52, 0x10000
	s_mov_b32 m0, s52
	s_add_i32 s52, s52, 0x400
	global_load_lds_dwordx4 v211, s[46:47]
	s_mov_b32 m0, s52
	s_add_i32 s52, s52, 0x400
	global_load_lds_dwordx4 v212, s[46:47]
	s_mov_b32 m0, s52
	s_add_i32 s52, s52, 0x400
	global_load_lds_dwordx4 v213, s[46:47]
	s_mov_b32 m0, s52
	s_add_i32 s52, s52, 0x400
	global_load_lds_dwordx4 v214, s[46:47]
	s_mov_b32 m0, s52
	s_add_i32 s52, s52, 0x400
	global_load_lds_dwordx4 v215, s[46:47]
	s_mov_b32 m0, s52
	s_add_i32 s52, s52, 0x400
	global_load_lds_dwordx4 v216, s[46:47]
	s_mov_b32 m0, s52
	s_add_i32 s52, s52, 0x400
	global_load_lds_dwordx4 v217, s[46:47]
	s_mov_b32 m0, s52
	s_nop 0
	global_load_lds_dwordx4 v218, s[46:47]
	s_waitcnt vmcnt(8)
	s_barrier
	s_cmp_eq_u32 s7, 0
	s_cbranch_scc1 .Lmylru_p0_0
	v_mov_b32_e32 v163, v162
	ds_read_b128 v[112:115], v163
	ds_read_b128 v[116:119], v163 offset:8192
	ds_read_b128 v[120:123], v163 offset:16384
	ds_read_b128 v[124:127], v163 offset:24576
	s_waitcnt lgkmcnt(3)
	v_mfma_f32_16x16x32_bf16 v[64:67], v[112:115], v[0:3], 0
	v_mfma_f32_16x16x32_bf16 v[68:71], v[112:115], v[32:35], 0
	v_xor_b32_e32 v164, 0x40, v163
	ds_read_b128 v[112:115], v164
	s_waitcnt lgkmcnt(3)
	v_mfma_f32_16x16x32_bf16 v[72:75], v[116:119], v[0:3], 0
	v_mfma_f32_16x16x32_bf16 v[76:79], v[116:119], v[32:35], 0
	ds_read_b128 v[116:119], v164 offset:8192
	s_waitcnt lgkmcnt(3)
	v_mfma_f32_16x16x32_bf16 v[80:83], v[120:123], v[0:3], 0
	v_mfma_f32_16x16x32_bf16 v[84:87], v[120:123], v[32:35], 0
	ds_read_b128 v[120:123], v164 offset:16384
	s_waitcnt lgkmcnt(3)
	v_mfma_f32_16x16x32_bf16 v[88:91], v[124:127], v[0:3], 0
	v_mfma_f32_16x16x32_bf16 v[92:95], v[124:127], v[32:35], 0
	ds_read_b128 v[124:127], v164 offset:24576
	s_waitcnt lgkmcnt(3)
	v_mfma_f32_16x16x32_bf16 v[64:67], v[112:115], v[4:7], v[64:67]
	v_mfma_f32_16x16x32_bf16 v[68:71], v[112:115], v[36:39], v[68:71]
	v_xor_b32_e32 v164, 0x80, v163
	ds_read_b128 v[112:115], v164
	s_waitcnt lgkmcnt(3)
	v_mfma_f32_16x16x32_bf16 v[72:75], v[116:119], v[4:7], v[72:75]
	v_mfma_f32_16x16x32_bf16 v[76:79], v[116:119], v[36:39], v[76:79]
	ds_read_b128 v[116:119], v164 offset:8192
	s_waitcnt lgkmcnt(3)
	v_mfma_f32_16x16x32_bf16 v[80:83], v[120:123], v[4:7], v[80:83]
	v_mfma_f32_16x16x32_bf16 v[84:87], v[120:123], v[36:39], v[84:87]
	ds_read_b128 v[120:123], v164 offset:16384
	s_waitcnt lgkmcnt(3)
	v_mfma_f32_16x16x32_bf16 v[88:91], v[124:127], v[4:7], v[88:91]
	v_mfma_f32_16x16x32_bf16 v[92:95], v[124:127], v[36:39], v[92:95]
	ds_read_b128 v[124:127], v164 offset:24576
	s_waitcnt lgkmcnt(3)
	v_mfma_f32_16x16x32_bf16 v[64:67], v[112:115], v[8:11], v[64:67]
	v_mfma_f32_16x16x32_bf16 v[68:71], v[112:115], v[40:43], v[68:71]
	v_xor_b32_e32 v164, 0xc0, v163
	ds_read_b128 v[112:115], v164
	s_waitcnt lgkmcnt(3)
	v_mfma_f32_16x16x32_bf16 v[72:75], v[116:119], v[8:11], v[72:75]
	v_mfma_f32_16x16x32_bf16 v[76:79], v[116:119], v[40:43], v[76:79]
	ds_read_b128 v[116:119], v164 offset:8192
	s_waitcnt lgkmcnt(3)
	v_mfma_f32_16x16x32_bf16 v[80:83], v[120:123], v[8:11], v[80:83]
	v_mfma_f32_16x16x32_bf16 v[84:87], v[120:123], v[40:43], v[84:87]
	ds_read_b128 v[120:123], v164 offset:16384
	s_waitcnt lgkmcnt(3)
	v_mfma_f32_16x16x32_bf16 v[88:91], v[124:127], v[8:11], v[88:91]
	v_mfma_f32_16x16x32_bf16 v[92:95], v[124:127], v[40:43], v[92:95]
	ds_read_b128 v[124:127], v164 offset:24576
	s_waitcnt lgkmcnt(3)
	v_mfma_f32_16x16x32_bf16 v[64:67], v[112:115], v[12:15], v[64:67]
	v_mfma_f32_16x16x32_bf16 v[68:71], v[112:115], v[44:47], v[68:71]
	v_xor_b32_e32 v164, 0x100, v163
	ds_read_b128 v[112:115], v164
	s_waitcnt lgkmcnt(3)
	v_mfma_f32_16x16x32_bf16 v[72:75], v[116:119], v[12:15], v[72:75]
	v_mfma_f32_16x16x32_bf16 v[76:79], v[116:119], v[44:47], v[76:79]
	ds_read_b128 v[116:119], v164 offset:8192
	s_waitcnt lgkmcnt(3)
	v_mfma_f32_16x16x32_bf16 v[80:83], v[120:123], v[12:15], v[80:83]
	v_mfma_f32_16x16x32_bf16 v[84:87], v[120:123], v[44:47], v[84:87]
	ds_read_b128 v[120:123], v164 offset:16384
	s_waitcnt lgkmcnt(3)
	v_mfma_f32_16x16x32_bf16 v[88:91], v[124:127], v[12:15], v[88:91]
	v_mfma_f32_16x16x32_bf16 v[92:95], v[124:127], v[44:47], v[92:95]
	ds_read_b128 v[124:127], v164 offset:24576
	s_waitcnt lgkmcnt(3)
	v_mfma_f32_16x16x32_bf16 v[64:67], v[112:115], v[16:19], v[64:67]
	v_mfma_f32_16x16x32_bf16 v[68:71], v[112:115], v[48:51], v[68:71]
	v_xor_b32_e32 v164, 0x140, v163
	ds_read_b128 v[112:115], v164
	s_waitcnt lgkmcnt(3)
	v_mfma_f32_16x16x32_bf16 v[72:75], v[116:119], v[16:19], v[72:75]
	v_mfma_f32_16x16x32_bf16 v[76:79], v[116:119], v[48:51], v[76:79]
	ds_read_b128 v[116:119], v164 offset:8192
	s_waitcnt lgkmcnt(3)
	v_mfma_f32_16x16x32_bf16 v[80:83], v[120:123], v[16:19], v[80:83]
	v_mfma_f32_16x16x32_bf16 v[84:87], v[120:123], v[48:51], v[84:87]
	ds_read_b128 v[120:123], v164 offset:16384
	s_waitcnt lgkmcnt(3)
	v_mfma_f32_16x16x32_bf16 v[88:91], v[124:127], v[16:19], v[88:91]
	v_mfma_f32_16x16x32_bf16 v[92:95], v[124:127], v[48:51], v[92:95]
	ds_read_b128 v[124:127], v164 offset:24576
	s_waitcnt lgkmcnt(3)
	v_mfma_f32_16x16x32_bf16 v[64:67], v[112:115], v[20:23], v[64:67]
	v_mfma_f32_16x16x32_bf16 v[68:71], v[112:115], v[52:55], v[68:71]
	v_xor_b32_e32 v164, 0x180, v163
	ds_read_b128 v[112:115], v164
	s_waitcnt lgkmcnt(3)
	v_mfma_f32_16x16x32_bf16 v[72:75], v[116:119], v[20:23], v[72:75]
	v_mfma_f32_16x16x32_bf16 v[76:79], v[116:119], v[52:55], v[76:79]
	ds_read_b128 v[116:119], v164 offset:8192
	s_waitcnt lgkmcnt(3)
	v_mfma_f32_16x16x32_bf16 v[80:83], v[120:123], v[20:23], v[80:83]
	v_mfma_f32_16x16x32_bf16 v[84:87], v[120:123], v[52:55], v[84:87]
	ds_read_b128 v[120:123], v164 offset:16384
	s_waitcnt lgkmcnt(3)
	v_mfma_f32_16x16x32_bf16 v[88:91], v[124:127], v[20:23], v[88:91]
	v_mfma_f32_16x16x32_bf16 v[92:95], v[124:127], v[52:55], v[92:95]
	ds_read_b128 v[124:127], v164 offset:24576
	s_waitcnt lgkmcnt(3)
	v_mfma_f32_16x16x32_bf16 v[64:67], v[112:115], v[24:27], v[64:67]
	v_mfma_f32_16x16x32_bf16 v[68:71], v[112:115], v[56:59], v[68:71]
	v_xor_b32_e32 v164, 0x1c0, v163
	ds_read_b128 v[112:115], v164
	s_waitcnt lgkmcnt(3)
	v_mfma_f32_16x16x32_bf16 v[72:75], v[116:119], v[24:27], v[72:75]
	v_mfma_f32_16x16x32_bf16 v[76:79], v[116:119], v[56:59], v[76:79]
	ds_read_b128 v[116:119], v164 offset:8192
	s_waitcnt lgkmcnt(3)
	v_mfma_f32_16x16x32_bf16 v[80:83], v[120:123], v[24:27], v[80:83]
	v_mfma_f32_16x16x32_bf16 v[84:87], v[120:123], v[56:59], v[84:87]
	ds_read_b128 v[120:123], v164 offset:16384
	s_waitcnt lgkmcnt(3)
	v_mfma_f32_16x16x32_bf16 v[88:91], v[124:127], v[24:27], v[88:91]
	v_mfma_f32_16x16x32_bf16 v[92:95], v[124:127], v[56:59], v[92:95]
	ds_read_b128 v[124:127], v164 offset:24576
	s_waitcnt lgkmcnt(3)
	v_mfma_f32_16x16x32_bf16 v[64:67], v[112:115], v[28:31], v[64:67]
	v_mfma_f32_16x16x32_bf16 v[68:71], v[112:115], v[60:63], v[68:71]
	s_waitcnt lgkmcnt(2)
	v_mfma_f32_16x16x32_bf16 v[72:75], v[116:119], v[28:31], v[72:75]
	v_mfma_f32_16x16x32_bf16 v[76:79], v[116:119], v[60:63], v[76:79]
	s_waitcnt lgkmcnt(1)
	v_mfma_f32_16x16x32_bf16 v[80:83], v[120:123], v[28:31], v[80:83]
	v_mfma_f32_16x16x32_bf16 v[84:87], v[120:123], v[60:63], v[84:87]
	s_waitcnt lgkmcnt(0)
	v_mfma_f32_16x16x32_bf16 v[88:91], v[124:127], v[28:31], v[88:91]
	v_mfma_f32_16x16x32_bf16 v[92:95], v[124:127], v[60:63], v[92:95]
.Lmylru_p0_0:
	s_cmp_eq_u32 s7, 0
	s_cbranch_scc0 .Lmylru_nm_1
	v_mov_b32_e32 v163, v162
	ds_read_b128 v[96:99], v163
	ds_read_b128 v[100:103], v163 offset:8192
	ds_read_b128 v[104:107], v163 offset:16384
	ds_read_b128 v[108:111], v163 offset:24576
	v_xor_b32_e32 v164, 0x40, v163
	ds_read_b128 v[112:115], v164
	ds_read_b128 v[116:119], v164 offset:8192
	ds_read_b128 v[120:123], v164 offset:16384
	ds_read_b128 v[124:127], v164 offset:24576
	s_waitcnt lgkmcnt(7)
	v_mfma_f32_16x16x32_bf16 v[64:67], v[96:99], v[0:3], 0
	v_mfma_f32_16x16x32_bf16 v[68:71], v[96:99], v[32:35], 0
	v_xor_b32_e32 v164, 0x80, v163
	ds_read_b128 v[96:99], v164
	s_waitcnt lgkmcnt(7)
	v_mfma_f32_16x16x32_bf16 v[72:75], v[100:103], v[0:3], 0
	v_mfma_f32_16x16x32_bf16 v[76:79], v[100:103], v[32:35], 0
	ds_read_b128 v[100:103], v164 offset:8192
	s_waitcnt lgkmcnt(7)
	v_mfma_f32_16x16x32_bf16 v[80:83], v[104:107], v[0:3], 0
	v_mfma_f32_16x16x32_bf16 v[84:87], v[104:107], v[32:35], 0
	ds_read_b128 v[104:107], v164 offset:16384
	s_waitcnt lgkmcnt(7)
	v_mfma_f32_16x16x32_bf16 v[88:91], v[108:111], v[0:3], 0
	v_mfma_f32_16x16x32_bf16 v[92:95], v[108:111], v[32:35], 0
	ds_read_b128 v[108:111], v164 offset:24576
	s_waitcnt lgkmcnt(7)
	v_mfma_f32_16x16x32_bf16 v[64:67], v[112:115], v[4:7], v[64:67]
	v_mfma_f32_16x16x32_bf16 v[68:71], v[112:115], v[36:39], v[68:71]
	v_xor_b32_e32 v164, 0xc0, v163
	ds_read_b128 v[112:115], v164
	s_waitcnt lgkmcnt(7)
	v_mfma_f32_16x16x32_bf16 v[72:75], v[116:119], v[4:7], v[72:75]
	v_mfma_f32_16x16x32_bf16 v[76:79], v[116:119], v[36:39], v[76:79]
	ds_read_b128 v[116:119], v164 offset:8192
	s_waitcnt lgkmcnt(7)
	v_mfma_f32_16x16x32_bf16 v[80:83], v[120:123], v[4:7], v[80:83]
	v_mfma_f32_16x16x32_bf16 v[84:87], v[120:123], v[36:39], v[84:87]
	ds_read_b128 v[120:123], v164 offset:16384
	s_waitcnt lgkmcnt(7)
	v_mfma_f32_16x16x32_bf16 v[88:91], v[124:127], v[4:7], v[88:91]
	v_mfma_f32_16x16x32_bf16 v[92:95], v[124:127], v[36:39], v[92:95]
	ds_read_b128 v[124:127], v164 offset:24576
	s_waitcnt lgkmcnt(7)
	v_mfma_f32_16x16x32_bf16 v[64:67], v[96:99], v[8:11], v[64:67]
	v_mfma_f32_16x16x32_bf16 v[68:71], v[96:99], v[40:43], v[68:71]
	v_xor_b32_e32 v164, 0x100, v163
	ds_read_b128 v[96:99], v164
	s_waitcnt lgkmcnt(7)
	v_mfma_f32_16x16x32_bf16 v[72:75], v[100:103], v[8:11], v[72:75]
	v_mfma_f32_16x16x32_bf16 v[76:79], v[100:103], v[40:43], v[76:79]
	ds_read_b128 v[100:103], v164 offset:8192
	s_waitcnt lgkmcnt(7)
	v_mfma_f32_16x16x32_bf16 v[80:83], v[104:107], v[8:11], v[80:83]
	v_mfma_f32_16x16x32_bf16 v[84:87], v[104:107], v[40:43], v[84:87]
	ds_read_b128 v[104:107], v164 offset:16384
	s_waitcnt lgkmcnt(7)
	v_mfma_f32_16x16x32_bf16 v[88:91], v[108:111], v[8:11], v[88:91]
	v_mfma_f32_16x16x32_bf16 v[92:95], v[108:111], v[40:43], v[92:95]
	ds_read_b128 v[108:111], v164 offset:24576
	s_waitcnt lgkmcnt(7)
	v_mfma_f32_16x16x32_bf16 v[64:67], v[112:115], v[12:15], v[64:67]
	v_mfma_f32_16x16x32_bf16 v[68:71], v[112:115], v[44:47], v[68:71]
	v_xor_b32_e32 v164, 0x140, v163
	ds_read_b128 v[112:115], v164
	s_waitcnt lgkmcnt(7)
	v_mfma_f32_16x16x32_bf16 v[72:75], v[116:119], v[12:15], v[72:75]
	v_mfma_f32_16x16x32_bf16 v[76:79], v[116:119], v[44:47], v[76:79]
	ds_read_b128 v[116:119], v164 offset:8192
	s_waitcnt lgkmcnt(7)
	v_mfma_f32_16x16x32_bf16 v[80:83], v[120:123], v[12:15], v[80:83]
	v_mfma_f32_16x16x32_bf16 v[84:87], v[120:123], v[44:47], v[84:87]
	ds_read_b128 v[120:123], v164 offset:16384
	s_waitcnt lgkmcnt(7)
	v_mfma_f32_16x16x32_bf16 v[88:91], v[124:127], v[12:15], v[88:91]
	v_mfma_f32_16x16x32_bf16 v[92:95], v[124:127], v[44:47], v[92:95]
	ds_read_b128 v[124:127], v164 offset:24576
	s_waitcnt lgkmcnt(7)
	v_mfma_f32_16x16x32_bf16 v[64:67], v[96:99], v[16:19], v[64:67]
	v_mfma_f32_16x16x32_bf16 v[68:71], v[96:99], v[48:51], v[68:71]
	v_xor_b32_e32 v164, 0x180, v163
	ds_read_b128 v[96:99], v164
	s_waitcnt lgkmcnt(7)
	v_mfma_f32_16x16x32_bf16 v[72:75], v[100:103], v[16:19], v[72:75]
	v_mfma_f32_16x16x32_bf16 v[76:79], v[100:103], v[48:51], v[76:79]
	ds_read_b128 v[100:103], v164 offset:8192
	s_waitcnt lgkmcnt(7)
	v_mfma_f32_16x16x32_bf16 v[80:83], v[104:107], v[16:19], v[80:83]
	v_mfma_f32_16x16x32_bf16 v[84:87], v[104:107], v[48:51], v[84:87]
	ds_read_b128 v[104:107], v164 offset:16384
	s_waitcnt lgkmcnt(7)
	v_mfma_f32_16x16x32_bf16 v[88:91], v[108:111], v[16:19], v[88:91]
	v_mfma_f32_16x16x32_bf16 v[92:95], v[108:111], v[48:51], v[92:95]
	ds_read_b128 v[108:111], v164 offset:24576
	s_waitcnt lgkmcnt(7)
	v_mfma_f32_16x16x32_bf16 v[64:67], v[112:115], v[20:23], v[64:67]
	v_mfma_f32_16x16x32_bf16 v[68:71], v[112:115], v[52:55], v[68:71]
	v_xor_b32_e32 v164, 0x1c0, v163
	ds_read_b128 v[112:115], v164
	s_waitcnt lgkmcnt(7)
	v_mfma_f32_16x16x32_bf16 v[72:75], v[116:119], v[20:23], v[72:75]
	v_mfma_f32_16x16x32_bf16 v[76:79], v[116:119], v[52:55], v[76:79]
	ds_read_b128 v[116:119], v164 offset:8192
	s_waitcnt lgkmcnt(7)
	v_mfma_f32_16x16x32_bf16 v[80:83], v[120:123], v[20:23], v[80:83]
	v_mfma_f32_16x16x32_bf16 v[84:87], v[120:123], v[52:55], v[84:87]
	ds_read_b128 v[120:123], v164 offset:16384
	s_waitcnt lgkmcnt(7)
	v_mfma_f32_16x16x32_bf16 v[88:91], v[124:127], v[20:23], v[88:91]
	v_mfma_f32_16x16x32_bf16 v[92:95], v[124:127], v[52:55], v[92:95]
	ds_read_b128 v[124:127], v164 offset:24576
	s_waitcnt lgkmcnt(7)
	v_mfma_f32_16x16x32_bf16 v[64:67], v[96:99], v[24:27], v[64:67]
	v_mfma_f32_16x16x32_bf16 v[68:71], v[96:99], v[56:59], v[68:71]
	s_waitcnt lgkmcnt(6)
	v_mfma_f32_16x16x32_bf16 v[72:75], v[100:103], v[24:27], v[72:75]
	v_mfma_f32_16x16x32_bf16 v[76:79], v[100:103], v[56:59], v[76:79]
	s_waitcnt lgkmcnt(5)
	v_mfma_f32_16x16x32_bf16 v[80:83], v[104:107], v[24:27], v[80:83]
	v_mfma_f32_16x16x32_bf16 v[84:87], v[104:107], v[56:59], v[84:87]
	s_waitcnt lgkmcnt(4)
	v_mfma_f32_16x16x32_bf16 v[88:91], v[108:111], v[24:27], v[88:91]
	v_mfma_f32_16x16x32_bf16 v[92:95], v[108:111], v[56:59], v[92:95]
	s_waitcnt lgkmcnt(3)
	v_mfma_f32_16x16x32_bf16 v[64:67], v[112:115], v[28:31], v[64:67]
	v_mfma_f32_16x16x32_bf16 v[68:71], v[112:115], v[60:63], v[68:71]
	s_waitcnt lgkmcnt(2)
	v_mfma_f32_16x16x32_bf16 v[72:75], v[116:119], v[28:31], v[72:75]
	v_mfma_f32_16x16x32_bf16 v[76:79], v[116:119], v[60:63], v[76:79]
	s_waitcnt lgkmcnt(1)
	v_mfma_f32_16x16x32_bf16 v[80:83], v[120:123], v[28:31], v[80:83]
	v_mfma_f32_16x16x32_bf16 v[84:87], v[120:123], v[60:63], v[84:87]
	s_waitcnt lgkmcnt(0)
	v_mfma_f32_16x16x32_bf16 v[88:91], v[124:127], v[28:31], v[88:91]
	v_mfma_f32_16x16x32_bf16 v[92:95], v[124:127], v[60:63], v[92:95]
.Lmylru_nm_1:
	v_mov_b32_e32 v169, v165
	v_mov_b32_e32 v170, v166
	v_mov_b32_e32 v171, v167
	v_mov_b32_e32 v172, v168
	ds_read_u16 v144, v169
	ds_read_u16 v145, v170
	ds_read_u16 v146, v171
	ds_read_u16 v147, v172
	ds_read_u16 v148, v169 offset:8192
	ds_read_u16 v149, v170 offset:8192
	ds_read_u16 v150, v171 offset:8192
	ds_read_u16 v151, v172 offset:8192
	ds_read_u16 v152, v169 offset:16384
	ds_read_u16 v153, v170 offset:16384
	ds_read_u16 v154, v171 offset:16384
	ds_read_u16 v155, v172 offset:16384
	ds_read_u16 v156, v169 offset:24576
	ds_read_u16 v157, v170 offset:24576
	ds_read_u16 v158, v171 offset:24576
	ds_read_u16 v159, v172 offset:24576
	s_nop 7
	v_fma_f32 v178, v64, s53, v173
	v_fma_f32 v179, v65, s53, v173
	v_fma_f32 v180, v66, s53, v173
	v_fma_f32 v181, v67, s53, v173
	v_fma_f32 v182, v72, s53, v173
	v_fma_f32 v183, v73, s53, v173
	v_fma_f32 v184, v74, s53, v173
	v_fma_f32 v185, v75, s53, v173
	v_fma_f32 v186, v68, s53, v174
	v_fma_f32 v187, v69, s53, v174
	v_fma_f32 v188, v70, s53, v174
	v_fma_f32 v189, v71, s53, v174
	v_fma_f32 v190, v76, s53, v174
	v_fma_f32 v191, v77, s53, v174
	v_fma_f32 v192, v78, s53, v174
	v_fma_f32 v193, v79, s53, v174
	v_exp_f32_e32 v178, v178
	v_exp_f32_e32 v179, v179
	v_exp_f32_e32 v180, v180
	v_exp_f32_e32 v181, v181
	v_exp_f32_e32 v182, v182
	v_exp_f32_e32 v183, v183
	v_exp_f32_e32 v184, v184
	v_exp_f32_e32 v185, v185
	v_exp_f32_e32 v186, v186
	v_exp_f32_e32 v187, v187
	v_exp_f32_e32 v188, v188
	v_exp_f32_e32 v189, v189
	v_exp_f32_e32 v190, v190
	v_exp_f32_e32 v191, v191
	v_exp_f32_e32 v192, v192
	v_exp_f32_e32 v193, v193
	v_add_f32_e32 v178, 1.0, v178
	v_add_f32_e32 v179, 1.0, v179
	v_add_f32_e32 v180, 1.0, v180
	v_add_f32_e32 v181, 1.0, v181
	v_add_f32_e32 v182, 1.0, v182
	v_add_f32_e32 v183, 1.0, v183
	v_add_f32_e32 v184, 1.0, v184
	v_add_f32_e32 v185, 1.0, v185
	v_add_f32_e32 v186, 1.0, v186
	v_add_f32_e32 v187, 1.0, v187
	v_add_f32_e32 v188, 1.0, v188
	v_add_f32_e32 v189, 1.0, v189
	v_add_f32_e32 v190, 1.0, v190
	v_add_f32_e32 v191, 1.0, v191
	v_add_f32_e32 v192, 1.0, v192
	v_add_f32_e32 v193, 1.0, v193
	v_rcp_f32_e32 v178, v178
	v_rcp_f32_e32 v179, v179
	v_rcp_f32_e32 v180, v180
	v_rcp_f32_e32 v181, v181
	v_rcp_f32_e32 v182, v182
	v_rcp_f32_e32 v183, v183
	v_rcp_f32_e32 v184, v184
	v_rcp_f32_e32 v185, v185
	v_rcp_f32_e32 v186, v186
	v_rcp_f32_e32 v187, v187
	v_rcp_f32_e32 v188, v188
	v_rcp_f32_e32 v189, v189
	v_rcp_f32_e32 v190, v190
	v_rcp_f32_e32 v191, v191
	v_rcp_f32_e32 v192, v192
	v_rcp_f32_e32 v193, v193
	v_mul_f32_e32 v178, v175, v178
	v_mul_f32_e32 v179, v175, v179
	v_mul_f32_e32 v180, v175, v180
	v_mul_f32_e32 v181, v175, v181
	v_mul_f32_e32 v182, v175, v182
	v_mul_f32_e32 v183, v175, v183
	v_mul_f32_e32 v184, v175, v184
	v_mul_f32_e32 v185, v175, v185
	v_exp_f32_e32 v96, v178
	v_exp_f32_e32 v97, v179
	v_exp_f32_e32 v98, v180
	v_exp_f32_e32 v99, v181
	v_exp_f32_e32 v100, v182
	v_exp_f32_e32 v101, v183
	v_exp_f32_e32 v102, v184
	v_exp_f32_e32 v103, v185
	s_nop 0
	v_fma_f32 v194, -v96, v96, 1.0
	v_fma_f32 v195, -v97, v97, 1.0
	v_fma_f32 v196, -v98, v98, 1.0
	v_fma_f32 v197, -v99, v99, 1.0
	v_fma_f32 v198, -v100, v100, 1.0
	v_fma_f32 v199, -v101, v101, 1.0
	v_fma_f32 v200, -v102, v102, 1.0
	v_fma_f32 v201, -v103, v103, 1.0
	v_max_f32_e32 v194, 0, v194
	v_max_f32_e32 v195, 0, v195
	v_max_f32_e32 v196, 0, v196
	v_max_f32_e32 v197, 0, v197
	v_max_f32_e32 v198, 0, v198
	v_max_f32_e32 v199, 0, v199
	v_max_f32_e32 v200, 0, v200
	v_max_f32_e32 v201, 0, v201
	v_sqrt_f32_e32 v194, v194
	v_sqrt_f32_e32 v195, v195
	v_sqrt_f32_e32 v196, v196
	v_sqrt_f32_e32 v197, v197
	v_sqrt_f32_e32 v198, v198
	v_sqrt_f32_e32 v199, v199
	v_sqrt_f32_e32 v200, v200
	v_sqrt_f32_e32 v201, v201
	s_waitcnt lgkmcnt(8)
	v_lshlrev_b32_e32 v144, 16, v144
	v_lshlrev_b32_e32 v145, 16, v145
	v_lshlrev_b32_e32 v146, 16, v146
	v_lshlrev_b32_e32 v147, 16, v147
	v_lshlrev_b32_e32 v148, 16, v148
	v_lshlrev_b32_e32 v149, 16, v149
	v_lshlrev_b32_e32 v150, 16, v150
	v_lshlrev_b32_e32 v151, 16, v151
	v_mul_f32_e32 v194, v194, v186
	v_mul_f32_e32 v195, v195, v187
	v_mul_f32_e32 v196, v196, v188
	v_mul_f32_e32 v197, v197, v189
	v_mul_f32_e32 v198, v198, v190
	v_mul_f32_e32 v199, v199, v191
	v_mul_f32_e32 v200, v200, v192
	v_mul_f32_e32 v201, v201, v193
	v_mul_f32_e32 v144, v194, v144
	v_mul_f32_e32 v145, v195, v145
	v_mul_f32_e32 v146, v196, v146
	v_mul_f32_e32 v147, v197, v147
	v_mul_f32_e32 v148, v198, v148
	v_mul_f32_e32 v149, v199, v149
	v_mul_f32_e32 v150, v200, v150
	v_mul_f32_e32 v151, v201, v151
	v_fma_f32 v178, v80, s53, v173
	v_fma_f32 v179, v81, s53, v173
	v_fma_f32 v180, v82, s53, v173
	v_fma_f32 v181, v83, s53, v173
	v_fma_f32 v182, v88, s53, v173
	v_fma_f32 v183, v89, s53, v173
	v_fma_f32 v184, v90, s53, v173
	v_fma_f32 v185, v91, s53, v173
	v_fma_f32 v186, v84, s53, v174
	v_fma_f32 v187, v85, s53, v174
	v_fma_f32 v188, v86, s53, v174
	v_fma_f32 v189, v87, s53, v174
	v_fma_f32 v190, v92, s53, v174
	v_fma_f32 v191, v93, s53, v174
	v_fma_f32 v192, v94, s53, v174
	v_fma_f32 v193, v95, s53, v174
	v_exp_f32_e32 v178, v178
	v_exp_f32_e32 v179, v179
	v_exp_f32_e32 v180, v180
	v_exp_f32_e32 v181, v181
	v_exp_f32_e32 v182, v182
	v_exp_f32_e32 v183, v183
	v_exp_f32_e32 v184, v184
	v_exp_f32_e32 v185, v185
	v_exp_f32_e32 v186, v186
	v_exp_f32_e32 v187, v187
	v_exp_f32_e32 v188, v188
	v_exp_f32_e32 v189, v189
	v_exp_f32_e32 v190, v190
	v_exp_f32_e32 v191, v191
	v_exp_f32_e32 v192, v192
	v_exp_f32_e32 v193, v193
	v_add_f32_e32 v178, 1.0, v178
	v_add_f32_e32 v179, 1.0, v179
	v_add_f32_e32 v180, 1.0, v180
	v_add_f32_e32 v181, 1.0, v181
	v_add_f32_e32 v182, 1.0, v182
	v_add_f32_e32 v183, 1.0, v183
	v_add_f32_e32 v184, 1.0, v184
	v_add_f32_e32 v185, 1.0, v185
	v_add_f32_e32 v186, 1.0, v186
	v_add_f32_e32 v187, 1.0, v187
	v_add_f32_e32 v188, 1.0, v188
	v_add_f32_e32 v189, 1.0, v189
	v_add_f32_e32 v190, 1.0, v190
	v_add_f32_e32 v191, 1.0, v191
	v_add_f32_e32 v192, 1.0, v192
	v_add_f32_e32 v193, 1.0, v193
	v_rcp_f32_e32 v178, v178
	v_rcp_f32_e32 v179, v179
	v_rcp_f32_e32 v180, v180
	v_rcp_f32_e32 v181, v181
	v_rcp_f32_e32 v182, v182
	v_rcp_f32_e32 v183, v183
	v_rcp_f32_e32 v184, v184
	v_rcp_f32_e32 v185, v185
	v_rcp_f32_e32 v186, v186
	v_rcp_f32_e32 v187, v187
	v_rcp_f32_e32 v188, v188
	v_rcp_f32_e32 v189, v189
	v_rcp_f32_e32 v190, v190
	v_rcp_f32_e32 v191, v191
	v_rcp_f32_e32 v192, v192
	v_rcp_f32_e32 v193, v193
	v_mul_f32_e32 v178, v175, v178
	v_mul_f32_e32 v179, v175, v179
	v_mul_f32_e32 v180, v175, v180
	v_mul_f32_e32 v181, v175, v181
	v_mul_f32_e32 v182, v175, v182
	v_mul_f32_e32 v183, v175, v183
	v_mul_f32_e32 v184, v175, v184
	v_mul_f32_e32 v185, v175, v185
	v_exp_f32_e32 v104, v178
	v_exp_f32_e32 v105, v179
	v_exp_f32_e32 v106, v180
	v_exp_f32_e32 v107, v181
	v_exp_f32_e32 v108, v182
	v_exp_f32_e32 v109, v183
	v_exp_f32_e32 v110, v184
	v_exp_f32_e32 v111, v185
	s_nop 0
	v_fma_f32 v194, -v104, v104, 1.0
	v_fma_f32 v195, -v105, v105, 1.0
	v_fma_f32 v196, -v106, v106, 1.0
	v_fma_f32 v197, -v107, v107, 1.0
	v_fma_f32 v198, -v108, v108, 1.0
	v_fma_f32 v199, -v109, v109, 1.0
	v_fma_f32 v200, -v110, v110, 1.0
	v_fma_f32 v201, -v111, v111, 1.0
	v_max_f32_e32 v194, 0, v194
	v_max_f32_e32 v195, 0, v195
	v_max_f32_e32 v196, 0, v196
	v_max_f32_e32 v197, 0, v197
	v_max_f32_e32 v198, 0, v198
	v_max_f32_e32 v199, 0, v199
	v_max_f32_e32 v200, 0, v200
	v_max_f32_e32 v201, 0, v201
	v_sqrt_f32_e32 v194, v194
	v_sqrt_f32_e32 v195, v195
	v_sqrt_f32_e32 v196, v196
	v_sqrt_f32_e32 v197, v197
	v_sqrt_f32_e32 v198, v198
	v_sqrt_f32_e32 v199, v199
	v_sqrt_f32_e32 v200, v200
	v_sqrt_f32_e32 v201, v201
	s_waitcnt lgkmcnt(0)
	v_lshlrev_b32_e32 v152, 16, v152
	v_lshlrev_b32_e32 v153, 16, v153
	v_lshlrev_b32_e32 v154, 16, v154
	v_lshlrev_b32_e32 v155, 16, v155
	v_lshlrev_b32_e32 v156, 16, v156
	v_lshlrev_b32_e32 v157, 16, v157
	v_lshlrev_b32_e32 v158, 16, v158
	v_lshlrev_b32_e32 v159, 16, v159
	v_mul_f32_e32 v194, v194, v186
	v_mul_f32_e32 v195, v195, v187
	v_mul_f32_e32 v196, v196, v188
	v_mul_f32_e32 v197, v197, v189
	v_mul_f32_e32 v198, v198, v190
	v_mul_f32_e32 v199, v199, v191
	v_mul_f32_e32 v200, v200, v192
	v_mul_f32_e32 v201, v201, v193
	v_mul_f32_e32 v152, v194, v152
	v_mul_f32_e32 v153, v195, v153
	v_mul_f32_e32 v154, v196, v154
	v_mul_f32_e32 v155, v197, v155
	v_mul_f32_e32 v156, v198, v156
	v_mul_f32_e32 v157, v199, v157
	v_mul_f32_e32 v158, v200, v158
	v_mul_f32_e32 v159, v201, v159
	v_fma_f32 v145, v97, v144, v145
	v_fma_f32 v149, v101, v148, v149
	v_fma_f32 v153, v105, v152, v153
	v_fma_f32 v157, v109, v156, v157
	v_mul_f32_e32 v97, v97, v96
	v_mul_f32_e32 v101, v101, v100
	v_mul_f32_e32 v105, v105, v104
	v_mul_f32_e32 v109, v109, v108
	v_fma_f32 v146, v98, v145, v146
	v_fma_f32 v150, v102, v149, v150
	v_fma_f32 v154, v106, v153, v154
	v_fma_f32 v158, v110, v157, v158
	v_mul_f32_e32 v98, v98, v97
	v_mul_f32_e32 v102, v102, v101
	v_mul_f32_e32 v106, v106, v105
	v_mul_f32_e32 v110, v110, v109
	v_fma_f32 v147, v99, v146, v147
	v_fma_f32 v151, v103, v150, v151
	v_fma_f32 v155, v107, v154, v155
	v_fma_f32 v159, v111, v158, v159
	v_mul_f32_e32 v99, v99, v98
	v_mul_f32_e32 v103, v103, v102
	v_mul_f32_e32 v107, v107, v106
	v_mul_f32_e32 v111, v111, v110
	ds_bpermute_b32 v178, v204, v99
	ds_bpermute_b32 v182, v204, v147
	ds_bpermute_b32 v179, v204, v103
	ds_bpermute_b32 v183, v204, v151
	ds_bpermute_b32 v180, v204, v107
	ds_bpermute_b32 v184, v204, v155
	ds_bpermute_b32 v181, v204, v111
	ds_bpermute_b32 v185, v204, v159
	s_waitcnt lgkmcnt(0)
	v_fma_f32 v186, v182, v99, v147
	v_cndmask_b32_e64 v178, 1.0, v178, s[34:35]
	v_fma_f32 v187, v183, v103, v151
	v_cndmask_b32_e64 v179, 1.0, v179, s[34:35]
	v_fma_f32 v188, v184, v107, v155
	v_cndmask_b32_e64 v180, 1.0, v180, s[34:35]
	v_fma_f32 v189, v185, v111, v159
	v_cndmask_b32_e64 v181, 1.0, v181, s[34:35]
	v_cndmask_b32_e64 v223, v147, v186, s[34:35]
	v_mul_f32_e32 v219, v99, v178
	v_cndmask_b32_e64 v224, v151, v187, s[34:35]
	v_mul_f32_e32 v220, v103, v179
	v_cndmask_b32_e64 v225, v155, v188, s[34:35]
	v_mul_f32_e32 v221, v107, v180
	v_cndmask_b32_e64 v226, v159, v189, s[34:35]
	v_mul_f32_e32 v222, v111, v181
	ds_bpermute_b32 v178, v205, v219
	ds_bpermute_b32 v182, v205, v223
	ds_bpermute_b32 v179, v205, v220
	ds_bpermute_b32 v183, v205, v224
	ds_bpermute_b32 v180, v205, v221
	ds_bpermute_b32 v184, v205, v225
	ds_bpermute_b32 v181, v205, v222
	ds_bpermute_b32 v185, v205, v226
	s_waitcnt lgkmcnt(0)
	v_fma_f32 v186, v182, v219, v223
	v_cndmask_b32_e64 v178, 1.0, v178, s[36:37]
	v_fma_f32 v187, v183, v220, v224
	v_cndmask_b32_e64 v179, 1.0, v179, s[36:37]
	v_fma_f32 v188, v184, v221, v225
	v_cndmask_b32_e64 v180, 1.0, v180, s[36:37]
	v_fma_f32 v189, v185, v222, v226
	v_cndmask_b32_e64 v181, 1.0, v181, s[36:37]
	v_cndmask_b32_e64 v223, v223, v186, s[36:37]
	v_mul_f32_e32 v219, v219, v178
	v_cndmask_b32_e64 v224, v224, v187, s[36:37]
	v_mul_f32_e32 v220, v220, v179
	v_cndmask_b32_e64 v225, v225, v188, s[36:37]
	v_mul_f32_e32 v221, v221, v180
	v_cndmask_b32_e64 v226, v226, v189, s[36:37]
	v_mul_f32_e32 v222, v222, v181
	ds_bpermute_b32 v227, v204, v219
	ds_bpermute_b32 v231, v204, v223
	ds_bpermute_b32 v235, v206, v219
	ds_bpermute_b32 v239, v206, v223
	ds_bpermute_b32 v228, v204, v220
	ds_bpermute_b32 v232, v204, v224
	ds_bpermute_b32 v236, v206, v220
	ds_bpermute_b32 v244, v206, v224
	ds_bpermute_b32 v229, v204, v221
	ds_bpermute_b32 v233, v204, v225
	ds_bpermute_b32 v237, v206, v221
	ds_bpermute_b32 v245, v206, v225
	ds_bpermute_b32 v230, v204, v222
	ds_bpermute_b32 v234, v204, v226
	ds_bpermute_b32 v238, v206, v222
	ds_bpermute_b32 v246, v206, v226
	s_waitcnt lgkmcnt(0)
	v_cndmask_b32_e64 v227, 1.0, v227, s[34:35]
	v_cndmask_b32_e64 v231, 0, v231, s[34:35]
	v_cndmask_b32_e64 v228, 1.0, v228, s[34:35]
	v_cndmask_b32_e64 v232, 0, v232, s[34:35]
	v_cndmask_b32_e64 v229, 1.0, v229, s[34:35]
	v_cndmask_b32_e64 v233, 0, v233, s[34:35]
	v_cndmask_b32_e64 v230, 1.0, v230, s[34:35]
	v_cndmask_b32_e64 v234, 0, v234, s[34:35]
	v_mov_b32_e32 v190, v235
	v_mov_b32_e32 v194, v239
	v_mov_b32_e32 v198, v190
	v_mov_b32_e32 v201, v194
	v_fma_f32 v194, v194, v236, v244
	v_mul_f32_e32 v190, v190, v236
	v_mov_b32_e32 v199, v190
	v_mov_b32_e32 v177, v194
	v_fma_f32 v194, v194, v237, v245
	v_mul_f32_e32 v190, v190, v237
	v_mov_b32_e32 v200, v190
	v_mov_b32_e32 v203, v194
	v_fma_f32 v194, v194, v238, v246
	v_mul_f32_e32 v190, v190, v238
	v_mov_b32_e32 v191, v194
	ds_write_b64 v207, v[190:191]
	s_waitcnt vmcnt(0)
	s_waitcnt lgkmcnt(0)
	s_barrier
	s_cmp_gt_u32 s13, 15
	s_cbranch_scc1 .Lmylru_nodma_1
	s_add_i32 s58, s13, 2
	s_cmp_lt_u32 s58, 2
	s_lshl_b32 s50, s58, 7
	s_lshl_b32 s51, s9, 8
	s_add_i32 s51, s51, 0x8000
	s_add_i32 s51, s51, s50
	s_lshl_b32 s59, s9, 11
	s_add_i32 s59, s59, s50
	s_addk_i32 s59, 0xff00
	s_cmp_lt_u32 s58, 2
	s_cselect_b32 s59, s51, s59
	s_lshl_b32 s52, s59, 11
	s_add_u32 s46, s16, s52
	s_addc_u32 s47, s17, 0
	s_lshl_b32 s52, s6, 13
	s_mov_b32 m0, s52
	s_add_i32 s52, s52, 0x400
	global_load_lds_dwordx4 v211, s[46:47]
	s_mov_b32 m0, s52
	s_add_i32 s52, s52, 0x400
	global_load_lds_dwordx4 v212, s[46:47]
	s_mov_b32 m0, s52
	s_add_i32 s52, s52, 0x400
	global_load_lds_dwordx4 v213, s[46:47]
	s_mov_b32 m0, s52
	s_add_i32 s52, s52, 0x400
	global_load_lds_dwordx4 v214, s[46:47]
	s_mov_b32 m0, s52
	s_add_i32 s52, s52, 0x400
	global_load_lds_dwordx4 v215, s[46:47]
	s_mov_b32 m0, s52
	s_add_i32 s52, s52, 0x400
	global_load_lds_dwordx4 v216, s[46:47]
	s_mov_b32 m0, s52
	s_add_i32 s52, s52, 0x400
	global_load_lds_dwordx4 v217, s[46:47]
	s_mov_b32 m0, s52
	s_nop 0
	global_load_lds_dwordx4 v218, s[46:47]
.Lmylru_nodma_1:
	s_cmp_eq_u32 s7, 0
	s_cbranch_scc1 .Lmylru_ne_1
	s_cmp_eq_u32 s13, 17
	s_cbranch_scc1 .Lmylru_ne_1
	v_or_b32_e32 v163, 0x10000, v162
	ds_read_b128 v[112:115], v163
	ds_read_b128 v[116:119], v163 offset:8192
	ds_read_b128 v[120:123], v163 offset:16384
	ds_read_b128 v[124:127], v163 offset:24576
	s_waitcnt lgkmcnt(3)
	v_mfma_f32_16x16x32_bf16 v[64:67], v[112:115], v[0:3], 0
	v_mfma_f32_16x16x32_bf16 v[68:71], v[112:115], v[32:35], 0
	v_xor_b32_e32 v164, 0x40, v163
	ds_read_b128 v[112:115], v164
	s_waitcnt lgkmcnt(3)
	v_mfma_f32_16x16x32_bf16 v[72:75], v[116:119], v[0:3], 0
	v_mfma_f32_16x16x32_bf16 v[76:79], v[116:119], v[32:35], 0
	ds_read_b128 v[116:119], v164 offset:8192
	s_waitcnt lgkmcnt(3)
	v_mfma_f32_16x16x32_bf16 v[80:83], v[120:123], v[0:3], 0
	v_mfma_f32_16x16x32_bf16 v[84:87], v[120:123], v[32:35], 0
	ds_read_b128 v[120:123], v164 offset:16384
	s_waitcnt lgkmcnt(3)
	v_mfma_f32_16x16x32_bf16 v[88:91], v[124:127], v[0:3], 0
	v_mfma_f32_16x16x32_bf16 v[92:95], v[124:127], v[32:35], 0
	ds_read_b128 v[124:127], v164 offset:24576
	s_waitcnt lgkmcnt(3)
	v_mfma_f32_16x16x32_bf16 v[64:67], v[112:115], v[4:7], v[64:67]
	v_mfma_f32_16x16x32_bf16 v[68:71], v[112:115], v[36:39], v[68:71]
	v_xor_b32_e32 v164, 0x80, v163
	ds_read_b128 v[112:115], v164
	s_waitcnt lgkmcnt(3)
	v_mfma_f32_16x16x32_bf16 v[72:75], v[116:119], v[4:7], v[72:75]
	v_mfma_f32_16x16x32_bf16 v[76:79], v[116:119], v[36:39], v[76:79]
	ds_read_b128 v[116:119], v164 offset:8192
	s_waitcnt lgkmcnt(3)
	v_mfma_f32_16x16x32_bf16 v[80:83], v[120:123], v[4:7], v[80:83]
	v_mfma_f32_16x16x32_bf16 v[84:87], v[120:123], v[36:39], v[84:87]
	ds_read_b128 v[120:123], v164 offset:16384
	s_waitcnt lgkmcnt(3)
	v_mfma_f32_16x16x32_bf16 v[88:91], v[124:127], v[4:7], v[88:91]
	v_mfma_f32_16x16x32_bf16 v[92:95], v[124:127], v[36:39], v[92:95]
	ds_read_b128 v[124:127], v164 offset:24576
	s_waitcnt lgkmcnt(3)
	v_mfma_f32_16x16x32_bf16 v[64:67], v[112:115], v[8:11], v[64:67]
	v_mfma_f32_16x16x32_bf16 v[68:71], v[112:115], v[40:43], v[68:71]
	v_xor_b32_e32 v164, 0xc0, v163
	ds_read_b128 v[112:115], v164
	s_waitcnt lgkmcnt(3)
	v_mfma_f32_16x16x32_bf16 v[72:75], v[116:119], v[8:11], v[72:75]
	v_mfma_f32_16x16x32_bf16 v[76:79], v[116:119], v[40:43], v[76:79]
	ds_read_b128 v[116:119], v164 offset:8192
	s_waitcnt lgkmcnt(3)
	v_mfma_f32_16x16x32_bf16 v[80:83], v[120:123], v[8:11], v[80:83]
	v_mfma_f32_16x16x32_bf16 v[84:87], v[120:123], v[40:43], v[84:87]
	ds_read_b128 v[120:123], v164 offset:16384
	s_waitcnt lgkmcnt(3)
	v_mfma_f32_16x16x32_bf16 v[88:91], v[124:127], v[8:11], v[88:91]
	v_mfma_f32_16x16x32_bf16 v[92:95], v[124:127], v[40:43], v[92:95]
	ds_read_b128 v[124:127], v164 offset:24576
	s_waitcnt lgkmcnt(3)
	v_mfma_f32_16x16x32_bf16 v[64:67], v[112:115], v[12:15], v[64:67]
	v_mfma_f32_16x16x32_bf16 v[68:71], v[112:115], v[44:47], v[68:71]
	v_xor_b32_e32 v164, 0x100, v163
	ds_read_b128 v[112:115], v164
	s_waitcnt lgkmcnt(3)
	v_mfma_f32_16x16x32_bf16 v[72:75], v[116:119], v[12:15], v[72:75]
	v_mfma_f32_16x16x32_bf16 v[76:79], v[116:119], v[44:47], v[76:79]
	ds_read_b128 v[116:119], v164 offset:8192
	s_waitcnt lgkmcnt(3)
	v_mfma_f32_16x16x32_bf16 v[80:83], v[120:123], v[12:15], v[80:83]
	v_mfma_f32_16x16x32_bf16 v[84:87], v[120:123], v[44:47], v[84:87]
	ds_read_b128 v[120:123], v164 offset:16384
	s_waitcnt lgkmcnt(3)
	v_mfma_f32_16x16x32_bf16 v[88:91], v[124:127], v[12:15], v[88:91]
	v_mfma_f32_16x16x32_bf16 v[92:95], v[124:127], v[44:47], v[92:95]
	ds_read_b128 v[124:127], v164 offset:24576
	s_waitcnt lgkmcnt(3)
	v_mfma_f32_16x16x32_bf16 v[64:67], v[112:115], v[16:19], v[64:67]
	v_mfma_f32_16x16x32_bf16 v[68:71], v[112:115], v[48:51], v[68:71]
	v_xor_b32_e32 v164, 0x140, v163
	ds_read_b128 v[112:115], v164
	s_waitcnt lgkmcnt(3)
	v_mfma_f32_16x16x32_bf16 v[72:75], v[116:119], v[16:19], v[72:75]
	v_mfma_f32_16x16x32_bf16 v[76:79], v[116:119], v[48:51], v[76:79]
	ds_read_b128 v[116:119], v164 offset:8192
	s_waitcnt lgkmcnt(3)
	v_mfma_f32_16x16x32_bf16 v[80:83], v[120:123], v[16:19], v[80:83]
	v_mfma_f32_16x16x32_bf16 v[84:87], v[120:123], v[48:51], v[84:87]
	ds_read_b128 v[120:123], v164 offset:16384
	s_waitcnt lgkmcnt(3)
	v_mfma_f32_16x16x32_bf16 v[88:91], v[124:127], v[16:19], v[88:91]
	v_mfma_f32_16x16x32_bf16 v[92:95], v[124:127], v[48:51], v[92:95]
	ds_read_b128 v[124:127], v164 offset:24576
	s_waitcnt lgkmcnt(3)
	v_mfma_f32_16x16x32_bf16 v[64:67], v[112:115], v[20:23], v[64:67]
	v_mfma_f32_16x16x32_bf16 v[68:71], v[112:115], v[52:55], v[68:71]
	v_xor_b32_e32 v164, 0x180, v163
	ds_read_b128 v[112:115], v164
	s_waitcnt lgkmcnt(3)
	v_mfma_f32_16x16x32_bf16 v[72:75], v[116:119], v[20:23], v[72:75]
	v_mfma_f32_16x16x32_bf16 v[76:79], v[116:119], v[52:55], v[76:79]
	ds_read_b128 v[116:119], v164 offset:8192
	s_waitcnt lgkmcnt(3)
	v_mfma_f32_16x16x32_bf16 v[80:83], v[120:123], v[20:23], v[80:83]
	v_mfma_f32_16x16x32_bf16 v[84:87], v[120:123], v[52:55], v[84:87]
	ds_read_b128 v[120:123], v164 offset:16384
	s_waitcnt lgkmcnt(3)
	v_mfma_f32_16x16x32_bf16 v[88:91], v[124:127], v[20:23], v[88:91]
	v_mfma_f32_16x16x32_bf16 v[92:95], v[124:127], v[52:55], v[92:95]
	ds_read_b128 v[124:127], v164 offset:24576
	s_waitcnt lgkmcnt(3)
	v_mfma_f32_16x16x32_bf16 v[64:67], v[112:115], v[24:27], v[64:67]
	v_mfma_f32_16x16x32_bf16 v[68:71], v[112:115], v[56:59], v[68:71]
	v_xor_b32_e32 v164, 0x1c0, v163
	ds_read_b128 v[112:115], v164
	s_waitcnt lgkmcnt(3)
	v_mfma_f32_16x16x32_bf16 v[72:75], v[116:119], v[24:27], v[72:75]
	v_mfma_f32_16x16x32_bf16 v[76:79], v[116:119], v[56:59], v[76:79]
	ds_read_b128 v[116:119], v164 offset:8192
	s_waitcnt lgkmcnt(3)
	v_mfma_f32_16x16x32_bf16 v[80:83], v[120:123], v[24:27], v[80:83]
	v_mfma_f32_16x16x32_bf16 v[84:87], v[120:123], v[56:59], v[84:87]
	ds_read_b128 v[120:123], v164 offset:16384
	s_waitcnt lgkmcnt(3)
	v_mfma_f32_16x16x32_bf16 v[88:91], v[124:127], v[24:27], v[88:91]
	v_mfma_f32_16x16x32_bf16 v[92:95], v[124:127], v[56:59], v[92:95]
	ds_read_b128 v[124:127], v164 offset:24576
	s_waitcnt lgkmcnt(3)
	v_mfma_f32_16x16x32_bf16 v[64:67], v[112:115], v[28:31], v[64:67]
	v_mfma_f32_16x16x32_bf16 v[68:71], v[112:115], v[60:63], v[68:71]
	s_waitcnt lgkmcnt(2)
	v_mfma_f32_16x16x32_bf16 v[72:75], v[116:119], v[28:31], v[72:75]
	v_mfma_f32_16x16x32_bf16 v[76:79], v[116:119], v[60:63], v[76:79]
	s_waitcnt lgkmcnt(1)
	v_mfma_f32_16x16x32_bf16 v[80:83], v[120:123], v[28:31], v[80:83]
	v_mfma_f32_16x16x32_bf16 v[84:87], v[120:123], v[60:63], v[84:87]
	s_waitcnt lgkmcnt(0)
	v_mfma_f32_16x16x32_bf16 v[88:91], v[124:127], v[28:31], v[88:91]
	v_mfma_f32_16x16x32_bf16 v[92:95], v[124:127], v[60:63], v[92:95]
.Lmylru_ne_1:
	ds_read_b64 v[178:179], v208
	ds_read_b64 v[180:181], v208 offset:512
	s_waitcnt lgkmcnt(0)
	v_fma_f32 v182, v176, v178, v179
	v_cndmask_b32_e64 v183, v176, v182, s[38:39]
	v_fma_f32 v176, v182, v180, v181
	s_add_i32 s13, s13, 1
	s_cmp_eq_u32 s7, 0
	s_cbranch_scc0 .Lmylru_nm_2
	v_or_b32_e32 v163, 0x10000, v162
	ds_read_b128 v[96:99], v163
	ds_read_b128 v[100:103], v163 offset:8192
	ds_read_b128 v[104:107], v163 offset:16384
	ds_read_b128 v[108:111], v163 offset:24576
	v_xor_b32_e32 v164, 0x40, v163
	ds_read_b128 v[112:115], v164
	ds_read_b128 v[116:119], v164 offset:8192
	ds_read_b128 v[120:123], v164 offset:16384
	ds_read_b128 v[124:127], v164 offset:24576
	s_waitcnt lgkmcnt(7)
	v_mfma_f32_16x16x32_bf16 v[64:67], v[96:99], v[0:3], 0
	v_mfma_f32_16x16x32_bf16 v[68:71], v[96:99], v[32:35], 0
	v_xor_b32_e32 v164, 0x80, v163
	ds_read_b128 v[96:99], v164
	s_waitcnt lgkmcnt(7)
	v_mfma_f32_16x16x32_bf16 v[72:75], v[100:103], v[0:3], 0
	v_mfma_f32_16x16x32_bf16 v[76:79], v[100:103], v[32:35], 0
	ds_read_b128 v[100:103], v164 offset:8192
	s_waitcnt lgkmcnt(7)
	v_mfma_f32_16x16x32_bf16 v[80:83], v[104:107], v[0:3], 0
	v_mfma_f32_16x16x32_bf16 v[84:87], v[104:107], v[32:35], 0
	ds_read_b128 v[104:107], v164 offset:16384
	s_waitcnt lgkmcnt(7)
	v_mfma_f32_16x16x32_bf16 v[88:91], v[108:111], v[0:3], 0
	v_mfma_f32_16x16x32_bf16 v[92:95], v[108:111], v[32:35], 0
	ds_read_b128 v[108:111], v164 offset:24576
	s_waitcnt lgkmcnt(7)
	v_mfma_f32_16x16x32_bf16 v[64:67], v[112:115], v[4:7], v[64:67]
	v_mfma_f32_16x16x32_bf16 v[68:71], v[112:115], v[36:39], v[68:71]
	v_xor_b32_e32 v164, 0xc0, v163
	ds_read_b128 v[112:115], v164
	s_waitcnt lgkmcnt(7)
	v_mfma_f32_16x16x32_bf16 v[72:75], v[116:119], v[4:7], v[72:75]
	v_mfma_f32_16x16x32_bf16 v[76:79], v[116:119], v[36:39], v[76:79]
	ds_read_b128 v[116:119], v164 offset:8192
	s_waitcnt lgkmcnt(7)
	v_mfma_f32_16x16x32_bf16 v[80:83], v[120:123], v[4:7], v[80:83]
	v_mfma_f32_16x16x32_bf16 v[84:87], v[120:123], v[36:39], v[84:87]
	ds_read_b128 v[120:123], v164 offset:16384
	s_waitcnt lgkmcnt(7)
	v_mfma_f32_16x16x32_bf16 v[88:91], v[124:127], v[4:7], v[88:91]
	v_mfma_f32_16x16x32_bf16 v[92:95], v[124:127], v[36:39], v[92:95]
	ds_read_b128 v[124:127], v164 offset:24576
	s_waitcnt lgkmcnt(7)
	v_mfma_f32_16x16x32_bf16 v[64:67], v[96:99], v[8:11], v[64:67]
	v_mfma_f32_16x16x32_bf16 v[68:71], v[96:99], v[40:43], v[68:71]
	v_xor_b32_e32 v164, 0x100, v163
	ds_read_b128 v[96:99], v164
	s_waitcnt lgkmcnt(7)
	v_mfma_f32_16x16x32_bf16 v[72:75], v[100:103], v[8:11], v[72:75]
	v_mfma_f32_16x16x32_bf16 v[76:79], v[100:103], v[40:43], v[76:79]
	ds_read_b128 v[100:103], v164 offset:8192
	s_waitcnt lgkmcnt(7)
	v_mfma_f32_16x16x32_bf16 v[80:83], v[104:107], v[8:11], v[80:83]
	v_mfma_f32_16x16x32_bf16 v[84:87], v[104:107], v[40:43], v[84:87]
	ds_read_b128 v[104:107], v164 offset:16384
	s_waitcnt lgkmcnt(7)
	v_mfma_f32_16x16x32_bf16 v[88:91], v[108:111], v[8:11], v[88:91]
	v_mfma_f32_16x16x32_bf16 v[92:95], v[108:111], v[40:43], v[92:95]
	ds_read_b128 v[108:111], v164 offset:24576
	s_waitcnt lgkmcnt(7)
	v_mfma_f32_16x16x32_bf16 v[64:67], v[112:115], v[12:15], v[64:67]
	v_mfma_f32_16x16x32_bf16 v[68:71], v[112:115], v[44:47], v[68:71]
	v_xor_b32_e32 v164, 0x140, v163
	ds_read_b128 v[112:115], v164
	s_waitcnt lgkmcnt(7)
	v_mfma_f32_16x16x32_bf16 v[72:75], v[116:119], v[12:15], v[72:75]
	v_mfma_f32_16x16x32_bf16 v[76:79], v[116:119], v[44:47], v[76:79]
	ds_read_b128 v[116:119], v164 offset:8192
	s_waitcnt lgkmcnt(7)
	v_mfma_f32_16x16x32_bf16 v[80:83], v[120:123], v[12:15], v[80:83]
	v_mfma_f32_16x16x32_bf16 v[84:87], v[120:123], v[44:47], v[84:87]
	ds_read_b128 v[120:123], v164 offset:16384
	s_waitcnt lgkmcnt(7)
	v_mfma_f32_16x16x32_bf16 v[88:91], v[124:127], v[12:15], v[88:91]
	v_mfma_f32_16x16x32_bf16 v[92:95], v[124:127], v[44:47], v[92:95]
	ds_read_b128 v[124:127], v164 offset:24576
	s_waitcnt lgkmcnt(7)
	v_mfma_f32_16x16x32_bf16 v[64:67], v[96:99], v[16:19], v[64:67]
	v_mfma_f32_16x16x32_bf16 v[68:71], v[96:99], v[48:51], v[68:71]
	v_xor_b32_e32 v164, 0x180, v163
	ds_read_b128 v[96:99], v164
	s_waitcnt lgkmcnt(7)
	v_mfma_f32_16x16x32_bf16 v[72:75], v[100:103], v[16:19], v[72:75]
	v_mfma_f32_16x16x32_bf16 v[76:79], v[100:103], v[48:51], v[76:79]
	ds_read_b128 v[100:103], v164 offset:8192
	s_waitcnt lgkmcnt(7)
	v_mfma_f32_16x16x32_bf16 v[80:83], v[104:107], v[16:19], v[80:83]
	v_mfma_f32_16x16x32_bf16 v[84:87], v[104:107], v[48:51], v[84:87]
	ds_read_b128 v[104:107], v164 offset:16384
	s_waitcnt lgkmcnt(7)
	v_mfma_f32_16x16x32_bf16 v[88:91], v[108:111], v[16:19], v[88:91]
	v_mfma_f32_16x16x32_bf16 v[92:95], v[108:111], v[48:51], v[92:95]
	ds_read_b128 v[108:111], v164 offset:24576
	s_waitcnt lgkmcnt(7)
	v_mfma_f32_16x16x32_bf16 v[64:67], v[112:115], v[20:23], v[64:67]
	v_mfma_f32_16x16x32_bf16 v[68:71], v[112:115], v[52:55], v[68:71]
	v_xor_b32_e32 v164, 0x1c0, v163
	ds_read_b128 v[112:115], v164
	s_waitcnt lgkmcnt(7)
	v_mfma_f32_16x16x32_bf16 v[72:75], v[116:119], v[20:23], v[72:75]
	v_mfma_f32_16x16x32_bf16 v[76:79], v[116:119], v[52:55], v[76:79]
	ds_read_b128 v[116:119], v164 offset:8192
	s_waitcnt lgkmcnt(7)
	v_mfma_f32_16x16x32_bf16 v[80:83], v[120:123], v[20:23], v[80:83]
	v_mfma_f32_16x16x32_bf16 v[84:87], v[120:123], v[52:55], v[84:87]
	ds_read_b128 v[120:123], v164 offset:16384
	s_waitcnt lgkmcnt(7)
	v_mfma_f32_16x16x32_bf16 v[88:91], v[124:127], v[20:23], v[88:91]
	v_mfma_f32_16x16x32_bf16 v[92:95], v[124:127], v[52:55], v[92:95]
	ds_read_b128 v[124:127], v164 offset:24576
	s_waitcnt lgkmcnt(7)
	v_mfma_f32_16x16x32_bf16 v[64:67], v[96:99], v[24:27], v[64:67]
	v_mfma_f32_16x16x32_bf16 v[68:71], v[96:99], v[56:59], v[68:71]
	s_waitcnt lgkmcnt(6)
	v_mfma_f32_16x16x32_bf16 v[72:75], v[100:103], v[24:27], v[72:75]
	v_mfma_f32_16x16x32_bf16 v[76:79], v[100:103], v[56:59], v[76:79]
	s_waitcnt lgkmcnt(5)
	v_mfma_f32_16x16x32_bf16 v[80:83], v[104:107], v[24:27], v[80:83]
	v_mfma_f32_16x16x32_bf16 v[84:87], v[104:107], v[56:59], v[84:87]
	s_waitcnt lgkmcnt(4)
	v_mfma_f32_16x16x32_bf16 v[88:91], v[108:111], v[24:27], v[88:91]
	v_mfma_f32_16x16x32_bf16 v[92:95], v[108:111], v[56:59], v[92:95]
	s_waitcnt lgkmcnt(3)
	v_mfma_f32_16x16x32_bf16 v[64:67], v[112:115], v[28:31], v[64:67]
	v_mfma_f32_16x16x32_bf16 v[68:71], v[112:115], v[60:63], v[68:71]
	s_waitcnt lgkmcnt(2)
	v_mfma_f32_16x16x32_bf16 v[72:75], v[116:119], v[28:31], v[72:75]
	v_mfma_f32_16x16x32_bf16 v[76:79], v[116:119], v[60:63], v[76:79]
	s_waitcnt lgkmcnt(1)
	v_mfma_f32_16x16x32_bf16 v[80:83], v[120:123], v[28:31], v[80:83]
	v_mfma_f32_16x16x32_bf16 v[84:87], v[120:123], v[60:63], v[84:87]
	s_waitcnt lgkmcnt(0)
	v_mfma_f32_16x16x32_bf16 v[88:91], v[124:127], v[28:31], v[88:91]
	v_mfma_f32_16x16x32_bf16 v[92:95], v[124:127], v[60:63], v[92:95]
.Lmylru_nm_2:
	v_or_b32_e32 v169, 0x10000, v165
	v_or_b32_e32 v170, 0x10000, v166
	v_or_b32_e32 v171, 0x10000, v167
	v_or_b32_e32 v172, 0x10000, v168
	ds_read_u16 v144, v169
	ds_read_u16 v145, v170
	ds_read_u16 v146, v171
	ds_read_u16 v147, v172
	ds_read_u16 v148, v169 offset:8192
	ds_read_u16 v149, v170 offset:8192
	ds_read_u16 v150, v171 offset:8192
	ds_read_u16 v151, v172 offset:8192
	ds_read_u16 v152, v169 offset:16384
	ds_read_u16 v153, v170 offset:16384
	ds_read_u16 v154, v171 offset:16384
	ds_read_u16 v155, v172 offset:16384
	ds_read_u16 v156, v169 offset:24576
	ds_read_u16 v157, v170 offset:24576
	ds_read_u16 v158, v171 offset:24576
	ds_read_u16 v159, v172 offset:24576
	s_nop 7
	v_fma_f32 v178, v64, s53, v173
	v_fma_f32 v179, v65, s53, v173
	v_fma_f32 v180, v66, s53, v173
	v_fma_f32 v181, v67, s53, v173
	v_fma_f32 v182, v72, s53, v173
	v_fma_f32 v183, v73, s53, v173
	v_fma_f32 v184, v74, s53, v173
	v_fma_f32 v185, v75, s53, v173
	v_fma_f32 v186, v68, s53, v174
	v_fma_f32 v187, v69, s53, v174
	v_fma_f32 v188, v70, s53, v174
	v_fma_f32 v189, v71, s53, v174
	v_fma_f32 v190, v76, s53, v174
	v_fma_f32 v191, v77, s53, v174
	v_fma_f32 v192, v78, s53, v174
	v_fma_f32 v193, v79, s53, v174
	v_exp_f32_e32 v178, v178
	v_exp_f32_e32 v179, v179
	v_exp_f32_e32 v180, v180
	v_exp_f32_e32 v181, v181
	v_exp_f32_e32 v182, v182
	v_exp_f32_e32 v183, v183
	v_exp_f32_e32 v184, v184
	v_exp_f32_e32 v185, v185
	v_exp_f32_e32 v186, v186
	v_exp_f32_e32 v187, v187
	v_exp_f32_e32 v188, v188
	v_exp_f32_e32 v189, v189
	v_exp_f32_e32 v190, v190
	v_exp_f32_e32 v191, v191
	v_exp_f32_e32 v192, v192
	v_exp_f32_e32 v193, v193
	v_add_f32_e32 v178, 1.0, v178
	v_add_f32_e32 v179, 1.0, v179
	v_add_f32_e32 v180, 1.0, v180
	v_add_f32_e32 v181, 1.0, v181
	v_add_f32_e32 v182, 1.0, v182
	v_add_f32_e32 v183, 1.0, v183
	v_add_f32_e32 v184, 1.0, v184
	v_add_f32_e32 v185, 1.0, v185
	v_add_f32_e32 v186, 1.0, v186
	v_add_f32_e32 v187, 1.0, v187
	v_add_f32_e32 v188, 1.0, v188
	v_add_f32_e32 v189, 1.0, v189
	v_add_f32_e32 v190, 1.0, v190
	v_add_f32_e32 v191, 1.0, v191
	v_add_f32_e32 v192, 1.0, v192
	v_add_f32_e32 v193, 1.0, v193
	v_rcp_f32_e32 v178, v178
	v_rcp_f32_e32 v179, v179
	v_rcp_f32_e32 v180, v180
	v_rcp_f32_e32 v181, v181
	v_rcp_f32_e32 v182, v182
	v_rcp_f32_e32 v183, v183
	v_rcp_f32_e32 v184, v184
	v_rcp_f32_e32 v185, v185
	v_rcp_f32_e32 v186, v186
	v_rcp_f32_e32 v187, v187
	v_rcp_f32_e32 v188, v188
	v_rcp_f32_e32 v189, v189
	v_rcp_f32_e32 v190, v190
	v_rcp_f32_e32 v191, v191
	v_rcp_f32_e32 v192, v192
	v_rcp_f32_e32 v193, v193
	v_mul_f32_e32 v178, v175, v178
	v_mul_f32_e32 v179, v175, v179
	v_mul_f32_e32 v180, v175, v180
	v_mul_f32_e32 v181, v175, v181
	v_mul_f32_e32 v182, v175, v182
	v_mul_f32_e32 v183, v175, v183
	v_mul_f32_e32 v184, v175, v184
	v_mul_f32_e32 v185, v175, v185
	v_exp_f32_e32 v96, v178
	v_exp_f32_e32 v97, v179
	v_exp_f32_e32 v98, v180
	v_exp_f32_e32 v99, v181
	v_exp_f32_e32 v100, v182
	v_exp_f32_e32 v101, v183
	v_exp_f32_e32 v102, v184
	v_exp_f32_e32 v103, v185
	s_nop 0
	v_fma_f32 v194, -v96, v96, 1.0
	v_fma_f32 v195, -v97, v97, 1.0
	v_fma_f32 v196, -v98, v98, 1.0
	v_fma_f32 v197, -v99, v99, 1.0
	v_fma_f32 v198, -v100, v100, 1.0
	v_fma_f32 v199, -v101, v101, 1.0
	v_fma_f32 v200, -v102, v102, 1.0
	v_fma_f32 v201, -v103, v103, 1.0
	v_max_f32_e32 v194, 0, v194
	v_max_f32_e32 v195, 0, v195
	v_max_f32_e32 v196, 0, v196
	v_max_f32_e32 v197, 0, v197
	v_max_f32_e32 v198, 0, v198
	v_max_f32_e32 v199, 0, v199
	v_max_f32_e32 v200, 0, v200
	v_max_f32_e32 v201, 0, v201
	v_sqrt_f32_e32 v194, v194
	v_sqrt_f32_e32 v195, v195
	v_sqrt_f32_e32 v196, v196
	v_sqrt_f32_e32 v197, v197
	v_sqrt_f32_e32 v198, v198
	v_sqrt_f32_e32 v199, v199
	v_sqrt_f32_e32 v200, v200
	v_sqrt_f32_e32 v201, v201
	s_waitcnt lgkmcnt(8)
	v_lshlrev_b32_e32 v144, 16, v144
	v_lshlrev_b32_e32 v145, 16, v145
	v_lshlrev_b32_e32 v146, 16, v146
	v_lshlrev_b32_e32 v147, 16, v147
	v_lshlrev_b32_e32 v148, 16, v148
	v_lshlrev_b32_e32 v149, 16, v149
	v_lshlrev_b32_e32 v150, 16, v150
	v_lshlrev_b32_e32 v151, 16, v151
	v_mul_f32_e32 v194, v194, v186
	v_mul_f32_e32 v195, v195, v187
	v_mul_f32_e32 v196, v196, v188
	v_mul_f32_e32 v197, v197, v189
	v_mul_f32_e32 v198, v198, v190
	v_mul_f32_e32 v199, v199, v191
	v_mul_f32_e32 v200, v200, v192
	v_mul_f32_e32 v201, v201, v193
	v_mul_f32_e32 v144, v194, v144
	v_mul_f32_e32 v145, v195, v145
	v_mul_f32_e32 v146, v196, v146
	v_mul_f32_e32 v147, v197, v147
	v_mul_f32_e32 v148, v198, v148
	v_mul_f32_e32 v149, v199, v149
	v_mul_f32_e32 v150, v200, v150
	v_mul_f32_e32 v151, v201, v151
	v_fma_f32 v178, v80, s53, v173
	v_fma_f32 v179, v81, s53, v173
	v_fma_f32 v180, v82, s53, v173
	v_fma_f32 v181, v83, s53, v173
	v_fma_f32 v182, v88, s53, v173
	v_fma_f32 v183, v89, s53, v173
	v_fma_f32 v184, v90, s53, v173
	v_fma_f32 v185, v91, s53, v173
	v_fma_f32 v186, v84, s53, v174
	v_fma_f32 v187, v85, s53, v174
	v_fma_f32 v188, v86, s53, v174
	v_fma_f32 v189, v87, s53, v174
	v_fma_f32 v190, v92, s53, v174
	v_fma_f32 v191, v93, s53, v174
	v_fma_f32 v192, v94, s53, v174
	v_fma_f32 v193, v95, s53, v174
	v_exp_f32_e32 v178, v178
	v_exp_f32_e32 v179, v179
	v_exp_f32_e32 v180, v180
	v_exp_f32_e32 v181, v181
	v_exp_f32_e32 v182, v182
	v_exp_f32_e32 v183, v183
	v_exp_f32_e32 v184, v184
	v_exp_f32_e32 v185, v185
	v_exp_f32_e32 v186, v186
	v_exp_f32_e32 v187, v187
	v_exp_f32_e32 v188, v188
	v_exp_f32_e32 v189, v189
	v_exp_f32_e32 v190, v190
	v_exp_f32_e32 v191, v191
	v_exp_f32_e32 v192, v192
	v_exp_f32_e32 v193, v193
	v_add_f32_e32 v178, 1.0, v178
	v_add_f32_e32 v179, 1.0, v179
	v_add_f32_e32 v180, 1.0, v180
	v_add_f32_e32 v181, 1.0, v181
	v_add_f32_e32 v182, 1.0, v182
	v_add_f32_e32 v183, 1.0, v183
	v_add_f32_e32 v184, 1.0, v184
	v_add_f32_e32 v185, 1.0, v185
	v_add_f32_e32 v186, 1.0, v186
	v_add_f32_e32 v187, 1.0, v187
	v_add_f32_e32 v188, 1.0, v188
	v_add_f32_e32 v189, 1.0, v189
	v_add_f32_e32 v190, 1.0, v190
	v_add_f32_e32 v191, 1.0, v191
	v_add_f32_e32 v192, 1.0, v192
	v_add_f32_e32 v193, 1.0, v193
	v_rcp_f32_e32 v178, v178
	v_rcp_f32_e32 v179, v179
	v_rcp_f32_e32 v180, v180
	v_rcp_f32_e32 v181, v181
	v_rcp_f32_e32 v182, v182
	v_rcp_f32_e32 v183, v183
	v_rcp_f32_e32 v184, v184
	v_rcp_f32_e32 v185, v185
	v_rcp_f32_e32 v186, v186
	v_rcp_f32_e32 v187, v187
	v_rcp_f32_e32 v188, v188
	v_rcp_f32_e32 v189, v189
	v_rcp_f32_e32 v190, v190
	v_rcp_f32_e32 v191, v191
	v_rcp_f32_e32 v192, v192
	v_rcp_f32_e32 v193, v193
	v_mul_f32_e32 v178, v175, v178
	v_mul_f32_e32 v179, v175, v179
	v_mul_f32_e32 v180, v175, v180
	v_mul_f32_e32 v181, v175, v181
	v_mul_f32_e32 v182, v175, v182
	v_mul_f32_e32 v183, v175, v183
	v_mul_f32_e32 v184, v175, v184
	v_mul_f32_e32 v185, v175, v185
	v_exp_f32_e32 v104, v178
	v_exp_f32_e32 v105, v179
	v_exp_f32_e32 v106, v180
	v_exp_f32_e32 v107, v181
	v_exp_f32_e32 v108, v182
	v_exp_f32_e32 v109, v183
	v_exp_f32_e32 v110, v184
	v_exp_f32_e32 v111, v185
	s_nop 0
	v_fma_f32 v194, -v104, v104, 1.0
	v_fma_f32 v195, -v105, v105, 1.0
	v_fma_f32 v196, -v106, v106, 1.0
	v_fma_f32 v197, -v107, v107, 1.0
	v_fma_f32 v198, -v108, v108, 1.0
	v_fma_f32 v199, -v109, v109, 1.0
	v_fma_f32 v200, -v110, v110, 1.0
	v_fma_f32 v201, -v111, v111, 1.0
	v_max_f32_e32 v194, 0, v194
	v_max_f32_e32 v195, 0, v195
	v_max_f32_e32 v196, 0, v196
	v_max_f32_e32 v197, 0, v197
	v_max_f32_e32 v198, 0, v198
	v_max_f32_e32 v199, 0, v199
	v_max_f32_e32 v200, 0, v200
	v_max_f32_e32 v201, 0, v201
	v_sqrt_f32_e32 v194, v194
	v_sqrt_f32_e32 v195, v195
	v_sqrt_f32_e32 v196, v196
	v_sqrt_f32_e32 v197, v197
	v_sqrt_f32_e32 v198, v198
	v_sqrt_f32_e32 v199, v199
	v_sqrt_f32_e32 v200, v200
	v_sqrt_f32_e32 v201, v201
	s_waitcnt lgkmcnt(0)
	v_lshlrev_b32_e32 v152, 16, v152
	v_lshlrev_b32_e32 v153, 16, v153
	v_lshlrev_b32_e32 v154, 16, v154
	v_lshlrev_b32_e32 v155, 16, v155
	v_lshlrev_b32_e32 v156, 16, v156
	v_lshlrev_b32_e32 v157, 16, v157
	v_lshlrev_b32_e32 v158, 16, v158
	v_lshlrev_b32_e32 v159, 16, v159
	v_mul_f32_e32 v194, v194, v186
	v_mul_f32_e32 v195, v195, v187
	v_mul_f32_e32 v196, v196, v188
	v_mul_f32_e32 v197, v197, v189
	v_mul_f32_e32 v198, v198, v190
	v_mul_f32_e32 v199, v199, v191
	v_mul_f32_e32 v200, v200, v192
	v_mul_f32_e32 v201, v201, v193
	v_mul_f32_e32 v152, v194, v152
	v_mul_f32_e32 v153, v195, v153
	v_mul_f32_e32 v154, v196, v154
	v_mul_f32_e32 v155, v197, v155
	v_mul_f32_e32 v156, v198, v156
	v_mul_f32_e32 v157, v199, v157
	v_mul_f32_e32 v158, v200, v158
	v_mul_f32_e32 v159, v201, v159
	v_fma_f32 v145, v97, v144, v145
	v_fma_f32 v149, v101, v148, v149
	v_fma_f32 v153, v105, v152, v153
	v_fma_f32 v157, v109, v156, v157
	v_mul_f32_e32 v97, v97, v96
	v_mul_f32_e32 v101, v101, v100
	v_mul_f32_e32 v105, v105, v104
	v_mul_f32_e32 v109, v109, v108
	v_fma_f32 v146, v98, v145, v146
	v_fma_f32 v150, v102, v149, v150
	v_fma_f32 v154, v106, v153, v154
	v_fma_f32 v158, v110, v157, v158
	v_mul_f32_e32 v98, v98, v97
	v_mul_f32_e32 v102, v102, v101
	v_mul_f32_e32 v106, v106, v105
	v_mul_f32_e32 v110, v110, v109
	v_fma_f32 v147, v99, v146, v147
	v_fma_f32 v151, v103, v150, v151
	v_fma_f32 v155, v107, v154, v155
	v_fma_f32 v159, v111, v158, v159
	v_mul_f32_e32 v99, v99, v98
	v_mul_f32_e32 v103, v103, v102
	v_mul_f32_e32 v107, v107, v106
	v_mul_f32_e32 v111, v111, v110
	ds_bpermute_b32 v178, v204, v99
	ds_bpermute_b32 v182, v204, v147
	ds_bpermute_b32 v179, v204, v103
	ds_bpermute_b32 v183, v204, v151
	ds_bpermute_b32 v180, v204, v107
	ds_bpermute_b32 v184, v204, v155
	ds_bpermute_b32 v181, v204, v111
	ds_bpermute_b32 v185, v204, v159
	s_waitcnt lgkmcnt(0)
	v_fma_f32 v186, v182, v99, v147
	v_cndmask_b32_e64 v178, 1.0, v178, s[34:35]
	v_fma_f32 v187, v183, v103, v151
	v_cndmask_b32_e64 v179, 1.0, v179, s[34:35]
	v_fma_f32 v188, v184, v107, v155
	v_cndmask_b32_e64 v180, 1.0, v180, s[34:35]
	v_fma_f32 v189, v185, v111, v159
	v_cndmask_b32_e64 v181, 1.0, v181, s[34:35]
	v_cndmask_b32_e64 v223, v147, v186, s[34:35]
	v_mul_f32_e32 v219, v99, v178
	v_cndmask_b32_e64 v224, v151, v187, s[34:35]
	v_mul_f32_e32 v220, v103, v179
	v_cndmask_b32_e64 v225, v155, v188, s[34:35]
	v_mul_f32_e32 v221, v107, v180
	v_cndmask_b32_e64 v226, v159, v189, s[34:35]
	v_mul_f32_e32 v222, v111, v181
	ds_bpermute_b32 v178, v205, v219
	ds_bpermute_b32 v182, v205, v223
	ds_bpermute_b32 v179, v205, v220
	ds_bpermute_b32 v183, v205, v224
	ds_bpermute_b32 v180, v205, v221
	ds_bpermute_b32 v184, v205, v225
	ds_bpermute_b32 v181, v205, v222
	ds_bpermute_b32 v185, v205, v226
	s_waitcnt lgkmcnt(0)
	v_fma_f32 v186, v182, v219, v223
	v_cndmask_b32_e64 v178, 1.0, v178, s[36:37]
	v_fma_f32 v187, v183, v220, v224
	v_cndmask_b32_e64 v179, 1.0, v179, s[36:37]
	v_fma_f32 v188, v184, v221, v225
	v_cndmask_b32_e64 v180, 1.0, v180, s[36:37]
	v_fma_f32 v189, v185, v222, v226
	v_cndmask_b32_e64 v181, 1.0, v181, s[36:37]
	v_cndmask_b32_e64 v223, v223, v186, s[36:37]
	v_mul_f32_e32 v219, v219, v178
	v_cndmask_b32_e64 v224, v224, v187, s[36:37]
	v_mul_f32_e32 v220, v220, v179
	v_cndmask_b32_e64 v225, v225, v188, s[36:37]
	v_mul_f32_e32 v221, v221, v180
	v_cndmask_b32_e64 v226, v226, v189, s[36:37]
	v_mul_f32_e32 v222, v222, v181
	ds_bpermute_b32 v227, v204, v219
	ds_bpermute_b32 v231, v204, v223
	ds_bpermute_b32 v235, v206, v219
	ds_bpermute_b32 v239, v206, v223
	ds_bpermute_b32 v228, v204, v220
	ds_bpermute_b32 v232, v204, v224
	ds_bpermute_b32 v236, v206, v220
	ds_bpermute_b32 v244, v206, v224
	ds_bpermute_b32 v229, v204, v221
	ds_bpermute_b32 v233, v204, v225
	ds_bpermute_b32 v237, v206, v221
	ds_bpermute_b32 v245, v206, v225
	ds_bpermute_b32 v230, v204, v222
	ds_bpermute_b32 v234, v204, v226
	ds_bpermute_b32 v238, v206, v222
	ds_bpermute_b32 v246, v206, v226
	s_waitcnt lgkmcnt(0)
	v_cndmask_b32_e64 v227, 1.0, v227, s[34:35]
	v_cndmask_b32_e64 v231, 0, v231, s[34:35]
	v_cndmask_b32_e64 v228, 1.0, v228, s[34:35]
	v_cndmask_b32_e64 v232, 0, v232, s[34:35]
	v_cndmask_b32_e64 v229, 1.0, v229, s[34:35]
	v_cndmask_b32_e64 v233, 0, v233, s[34:35]
	v_cndmask_b32_e64 v230, 1.0, v230, s[34:35]
	v_cndmask_b32_e64 v234, 0, v234, s[34:35]
	v_mov_b32_e32 v190, v235
	v_mov_b32_e32 v194, v239
	v_mov_b32_e32 v198, v190
	v_mov_b32_e32 v201, v194
	v_fma_f32 v194, v194, v236, v244
	v_mul_f32_e32 v190, v190, v236
	v_mov_b32_e32 v199, v190
	v_mov_b32_e32 v177, v194
	v_fma_f32 v194, v194, v237, v245
	v_mul_f32_e32 v190, v190, v237
	v_mov_b32_e32 v200, v190
	v_mov_b32_e32 v203, v194
	v_fma_f32 v194, v194, v238, v246
	v_mul_f32_e32 v190, v190, v238
	v_mov_b32_e32 v191, v194
	ds_write_b64 v207, v[190:191] offset:1024
	s_waitcnt vmcnt(0)
	s_waitcnt lgkmcnt(0)
	s_barrier
	s_cmp_gt_u32 s13, 15
	s_cbranch_scc1 .Lmylru_nodma_2
	s_add_i32 s58, s13, 2
	s_cmp_lt_u32 s58, 2
	s_lshl_b32 s50, s58, 7
	s_lshl_b32 s51, s9, 8
	s_add_i32 s51, s51, 0x8000
	s_add_i32 s51, s51, s50
	s_lshl_b32 s59, s9, 11
	s_add_i32 s59, s59, s50
	s_addk_i32 s59, 0xff00
	s_cmp_lt_u32 s58, 2
	s_cselect_b32 s59, s51, s59
	s_lshl_b32 s52, s59, 11
	s_add_u32 s46, s16, s52
	s_addc_u32 s47, s17, 0
	s_lshl_b32 s52, s6, 13
	s_add_i32 s52, s52, 0x10000
	s_mov_b32 m0, s52
	s_add_i32 s52, s52, 0x400
	global_load_lds_dwordx4 v211, s[46:47]
	s_mov_b32 m0, s52
	s_add_i32 s52, s52, 0x400
	global_load_lds_dwordx4 v212, s[46:47]
	s_mov_b32 m0, s52
	s_add_i32 s52, s52, 0x400
	global_load_lds_dwordx4 v213, s[46:47]
	s_mov_b32 m0, s52
	s_add_i32 s52, s52, 0x400
	global_load_lds_dwordx4 v214, s[46:47]
	s_mov_b32 m0, s52
	s_add_i32 s52, s52, 0x400
	global_load_lds_dwordx4 v215, s[46:47]
	s_mov_b32 m0, s52
	s_add_i32 s52, s52, 0x400
	global_load_lds_dwordx4 v216, s[46:47]
	s_mov_b32 m0, s52
	s_add_i32 s52, s52, 0x400
	global_load_lds_dwordx4 v217, s[46:47]
	s_mov_b32 m0, s52
	s_nop 0
	global_load_lds_dwordx4 v218, s[46:47]
.Lmylru_nodma_2:
	s_cmp_eq_u32 s7, 0
	s_cbranch_scc1 .Lmylru_ne_2
	s_cmp_eq_u32 s13, 17
	s_cbranch_scc1 .Lmylru_ne_2
	v_mov_b32_e32 v163, v162
	ds_read_b128 v[112:115], v163
	ds_read_b128 v[116:119], v163 offset:8192
	ds_read_b128 v[120:123], v163 offset:16384
	ds_read_b128 v[124:127], v163 offset:24576
	s_waitcnt lgkmcnt(3)
	v_mfma_f32_16x16x32_bf16 v[64:67], v[112:115], v[0:3], 0
	v_mfma_f32_16x16x32_bf16 v[68:71], v[112:115], v[32:35], 0
	v_xor_b32_e32 v164, 0x40, v163
	ds_read_b128 v[112:115], v164
	s_waitcnt lgkmcnt(3)
	v_mfma_f32_16x16x32_bf16 v[72:75], v[116:119], v[0:3], 0
	v_mfma_f32_16x16x32_bf16 v[76:79], v[116:119], v[32:35], 0
	ds_read_b128 v[116:119], v164 offset:8192
	s_waitcnt lgkmcnt(3)
	v_mfma_f32_16x16x32_bf16 v[80:83], v[120:123], v[0:3], 0
	v_mfma_f32_16x16x32_bf16 v[84:87], v[120:123], v[32:35], 0
	ds_read_b128 v[120:123], v164 offset:16384
	s_waitcnt lgkmcnt(3)
	v_mfma_f32_16x16x32_bf16 v[88:91], v[124:127], v[0:3], 0
	v_mfma_f32_16x16x32_bf16 v[92:95], v[124:127], v[32:35], 0
	ds_read_b128 v[124:127], v164 offset:24576
	s_waitcnt lgkmcnt(3)
	v_mfma_f32_16x16x32_bf16 v[64:67], v[112:115], v[4:7], v[64:67]
	v_mfma_f32_16x16x32_bf16 v[68:71], v[112:115], v[36:39], v[68:71]
	v_xor_b32_e32 v164, 0x80, v163
	ds_read_b128 v[112:115], v164
	s_waitcnt lgkmcnt(3)
	v_mfma_f32_16x16x32_bf16 v[72:75], v[116:119], v[4:7], v[72:75]
	v_mfma_f32_16x16x32_bf16 v[76:79], v[116:119], v[36:39], v[76:79]
	ds_read_b128 v[116:119], v164 offset:8192
	s_waitcnt lgkmcnt(3)
	v_mfma_f32_16x16x32_bf16 v[80:83], v[120:123], v[4:7], v[80:83]
	v_mfma_f32_16x16x32_bf16 v[84:87], v[120:123], v[36:39], v[84:87]
	ds_read_b128 v[120:123], v164 offset:16384
	s_waitcnt lgkmcnt(3)
	v_mfma_f32_16x16x32_bf16 v[88:91], v[124:127], v[4:7], v[88:91]
	v_mfma_f32_16x16x32_bf16 v[92:95], v[124:127], v[36:39], v[92:95]
	ds_read_b128 v[124:127], v164 offset:24576
	s_waitcnt lgkmcnt(3)
	v_mfma_f32_16x16x32_bf16 v[64:67], v[112:115], v[8:11], v[64:67]
	v_mfma_f32_16x16x32_bf16 v[68:71], v[112:115], v[40:43], v[68:71]
	v_xor_b32_e32 v164, 0xc0, v163
	ds_read_b128 v[112:115], v164
	s_waitcnt lgkmcnt(3)
	v_mfma_f32_16x16x32_bf16 v[72:75], v[116:119], v[8:11], v[72:75]
	v_mfma_f32_16x16x32_bf16 v[76:79], v[116:119], v[40:43], v[76:79]
	ds_read_b128 v[116:119], v164 offset:8192
	s_waitcnt lgkmcnt(3)
	v_mfma_f32_16x16x32_bf16 v[80:83], v[120:123], v[8:11], v[80:83]
	v_mfma_f32_16x16x32_bf16 v[84:87], v[120:123], v[40:43], v[84:87]
	ds_read_b128 v[120:123], v164 offset:16384
	s_waitcnt lgkmcnt(3)
	v_mfma_f32_16x16x32_bf16 v[88:91], v[124:127], v[8:11], v[88:91]
	v_mfma_f32_16x16x32_bf16 v[92:95], v[124:127], v[40:43], v[92:95]
	ds_read_b128 v[124:127], v164 offset:24576
	s_waitcnt lgkmcnt(3)
	v_mfma_f32_16x16x32_bf16 v[64:67], v[112:115], v[12:15], v[64:67]
	v_mfma_f32_16x16x32_bf16 v[68:71], v[112:115], v[44:47], v[68:71]
	v_xor_b32_e32 v164, 0x100, v163
	ds_read_b128 v[112:115], v164
	s_waitcnt lgkmcnt(3)
	v_mfma_f32_16x16x32_bf16 v[72:75], v[116:119], v[12:15], v[72:75]
	v_mfma_f32_16x16x32_bf16 v[76:79], v[116:119], v[44:47], v[76:79]
	ds_read_b128 v[116:119], v164 offset:8192
	s_waitcnt lgkmcnt(3)
	v_mfma_f32_16x16x32_bf16 v[80:83], v[120:123], v[12:15], v[80:83]
	v_mfma_f32_16x16x32_bf16 v[84:87], v[120:123], v[44:47], v[84:87]
	ds_read_b128 v[120:123], v164 offset:16384
	s_waitcnt lgkmcnt(3)
	v_mfma_f32_16x16x32_bf16 v[88:91], v[124:127], v[12:15], v[88:91]
	v_mfma_f32_16x16x32_bf16 v[92:95], v[124:127], v[44:47], v[92:95]
	ds_read_b128 v[124:127], v164 offset:24576
	s_waitcnt lgkmcnt(3)
	v_mfma_f32_16x16x32_bf16 v[64:67], v[112:115], v[16:19], v[64:67]
	v_mfma_f32_16x16x32_bf16 v[68:71], v[112:115], v[48:51], v[68:71]
	v_xor_b32_e32 v164, 0x140, v163
	ds_read_b128 v[112:115], v164
	s_waitcnt lgkmcnt(3)
	v_mfma_f32_16x16x32_bf16 v[72:75], v[116:119], v[16:19], v[72:75]
	v_mfma_f32_16x16x32_bf16 v[76:79], v[116:119], v[48:51], v[76:79]
	ds_read_b128 v[116:119], v164 offset:8192
	s_waitcnt lgkmcnt(3)
	v_mfma_f32_16x16x32_bf16 v[80:83], v[120:123], v[16:19], v[80:83]
	v_mfma_f32_16x16x32_bf16 v[84:87], v[120:123], v[48:51], v[84:87]
	ds_read_b128 v[120:123], v164 offset:16384
	s_waitcnt lgkmcnt(3)
	v_mfma_f32_16x16x32_bf16 v[88:91], v[124:127], v[16:19], v[88:91]
	v_mfma_f32_16x16x32_bf16 v[92:95], v[124:127], v[48:51], v[92:95]
	ds_read_b128 v[124:127], v164 offset:24576
	s_waitcnt lgkmcnt(3)
	v_mfma_f32_16x16x32_bf16 v[64:67], v[112:115], v[20:23], v[64:67]
	v_mfma_f32_16x16x32_bf16 v[68:71], v[112:115], v[52:55], v[68:71]
	v_xor_b32_e32 v164, 0x180, v163
	ds_read_b128 v[112:115], v164
	s_waitcnt lgkmcnt(3)
	v_mfma_f32_16x16x32_bf16 v[72:75], v[116:119], v[20:23], v[72:75]
	v_mfma_f32_16x16x32_bf16 v[76:79], v[116:119], v[52:55], v[76:79]
	ds_read_b128 v[116:119], v164 offset:8192
	s_waitcnt lgkmcnt(3)
	v_mfma_f32_16x16x32_bf16 v[80:83], v[120:123], v[20:23], v[80:83]
	v_mfma_f32_16x16x32_bf16 v[84:87], v[120:123], v[52:55], v[84:87]
	ds_read_b128 v[120:123], v164 offset:16384
	s_waitcnt lgkmcnt(3)
	v_mfma_f32_16x16x32_bf16 v[88:91], v[124:127], v[20:23], v[88:91]
	v_mfma_f32_16x16x32_bf16 v[92:95], v[124:127], v[52:55], v[92:95]
	ds_read_b128 v[124:127], v164 offset:24576
	s_waitcnt lgkmcnt(3)
	v_mfma_f32_16x16x32_bf16 v[64:67], v[112:115], v[24:27], v[64:67]
	v_mfma_f32_16x16x32_bf16 v[68:71], v[112:115], v[56:59], v[68:71]
	v_xor_b32_e32 v164, 0x1c0, v163
	ds_read_b128 v[112:115], v164
	s_waitcnt lgkmcnt(3)
	v_mfma_f32_16x16x32_bf16 v[72:75], v[116:119], v[24:27], v[72:75]
	v_mfma_f32_16x16x32_bf16 v[76:79], v[116:119], v[56:59], v[76:79]
	ds_read_b128 v[116:119], v164 offset:8192
	s_waitcnt lgkmcnt(3)
	v_mfma_f32_16x16x32_bf16 v[80:83], v[120:123], v[24:27], v[80:83]
	v_mfma_f32_16x16x32_bf16 v[84:87], v[120:123], v[56:59], v[84:87]
	ds_read_b128 v[120:123], v164 offset:16384
	s_waitcnt lgkmcnt(3)
	v_mfma_f32_16x16x32_bf16 v[88:91], v[124:127], v[24:27], v[88:91]
	v_mfma_f32_16x16x32_bf16 v[92:95], v[124:127], v[56:59], v[92:95]
	ds_read_b128 v[124:127], v164 offset:24576
	s_waitcnt lgkmcnt(3)
	v_mfma_f32_16x16x32_bf16 v[64:67], v[112:115], v[28:31], v[64:67]
	v_mfma_f32_16x16x32_bf16 v[68:71], v[112:115], v[60:63], v[68:71]
	s_waitcnt lgkmcnt(2)
	v_mfma_f32_16x16x32_bf16 v[72:75], v[116:119], v[28:31], v[72:75]
	v_mfma_f32_16x16x32_bf16 v[76:79], v[116:119], v[60:63], v[76:79]
	s_waitcnt lgkmcnt(1)
	v_mfma_f32_16x16x32_bf16 v[80:83], v[120:123], v[28:31], v[80:83]
	v_mfma_f32_16x16x32_bf16 v[84:87], v[120:123], v[60:63], v[84:87]
	s_waitcnt lgkmcnt(0)
	v_mfma_f32_16x16x32_bf16 v[88:91], v[124:127], v[28:31], v[88:91]
	v_mfma_f32_16x16x32_bf16 v[92:95], v[124:127], v[60:63], v[92:95]

.Lmylru_loop_0:
	s_add_i32 s54, s13, -2
	s_lshl_b32 s55, s54, 14
	s_lshl_b32 s56, s6, 11
	s_add_i32 s55, s55, s56
	s_add_u32 s44, s22, s55
	s_addc_u32 s45, s23, 0
	s_cmp_eq_u32 s7, 0
	s_cbranch_scc0 .Lmylru_nm_3
	v_mov_b32_e32 v163, v162
	ds_read_b128 v[96:99], v163
	ds_read_b128 v[100:103], v163 offset:8192
	ds_read_b128 v[104:107], v163 offset:16384
	ds_read_b128 v[108:111], v163 offset:24576
	v_xor_b32_e32 v164, 0x40, v163
	ds_read_b128 v[112:115], v164
	ds_read_b128 v[116:119], v164 offset:8192
	ds_read_b128 v[120:123], v164 offset:16384
	ds_read_b128 v[124:127], v164 offset:24576
	s_waitcnt lgkmcnt(7)
	v_mfma_f32_16x16x32_bf16 v[64:67], v[96:99], v[0:3], 0
	v_mfma_f32_16x16x32_bf16 v[68:71], v[96:99], v[32:35], 0
	v_xor_b32_e32 v164, 0x80, v163
	ds_read_b128 v[96:99], v164
	s_waitcnt lgkmcnt(7)
	v_mfma_f32_16x16x32_bf16 v[72:75], v[100:103], v[0:3], 0
	v_mfma_f32_16x16x32_bf16 v[76:79], v[100:103], v[32:35], 0
	ds_read_b128 v[100:103], v164 offset:8192
	s_waitcnt lgkmcnt(7)
	v_mfma_f32_16x16x32_bf16 v[80:83], v[104:107], v[0:3], 0
	v_mfma_f32_16x16x32_bf16 v[84:87], v[104:107], v[32:35], 0
	ds_read_b128 v[104:107], v164 offset:16384
	s_waitcnt lgkmcnt(7)
	v_mfma_f32_16x16x32_bf16 v[88:91], v[108:111], v[0:3], 0
	v_mfma_f32_16x16x32_bf16 v[92:95], v[108:111], v[32:35], 0
	ds_read_b128 v[108:111], v164 offset:24576
	s_waitcnt lgkmcnt(7)
	v_mfma_f32_16x16x32_bf16 v[64:67], v[112:115], v[4:7], v[64:67]
	v_mfma_f32_16x16x32_bf16 v[68:71], v[112:115], v[36:39], v[68:71]
	v_xor_b32_e32 v164, 0xc0, v163
	ds_read_b128 v[112:115], v164
	s_waitcnt lgkmcnt(7)
	v_mfma_f32_16x16x32_bf16 v[72:75], v[116:119], v[4:7], v[72:75]
	v_mfma_f32_16x16x32_bf16 v[76:79], v[116:119], v[36:39], v[76:79]
	ds_read_b128 v[116:119], v164 offset:8192
	s_waitcnt lgkmcnt(7)
	v_mfma_f32_16x16x32_bf16 v[80:83], v[120:123], v[4:7], v[80:83]
	v_mfma_f32_16x16x32_bf16 v[84:87], v[120:123], v[36:39], v[84:87]
	ds_read_b128 v[120:123], v164 offset:16384
	s_waitcnt lgkmcnt(7)
	v_mfma_f32_16x16x32_bf16 v[88:91], v[124:127], v[4:7], v[88:91]
	v_mfma_f32_16x16x32_bf16 v[92:95], v[124:127], v[36:39], v[92:95]
	ds_read_b128 v[124:127], v164 offset:24576
	s_waitcnt lgkmcnt(7)
	v_mfma_f32_16x16x32_bf16 v[64:67], v[96:99], v[8:11], v[64:67]
	v_mfma_f32_16x16x32_bf16 v[68:71], v[96:99], v[40:43], v[68:71]
	v_xor_b32_e32 v164, 0x100, v163
	ds_read_b128 v[96:99], v164
	s_waitcnt lgkmcnt(7)
	v_mfma_f32_16x16x32_bf16 v[72:75], v[100:103], v[8:11], v[72:75]
	v_mfma_f32_16x16x32_bf16 v[76:79], v[100:103], v[40:43], v[76:79]
	ds_read_b128 v[100:103], v164 offset:8192
	s_waitcnt lgkmcnt(7)
	v_mfma_f32_16x16x32_bf16 v[80:83], v[104:107], v[8:11], v[80:83]
	v_mfma_f32_16x16x32_bf16 v[84:87], v[104:107], v[40:43], v[84:87]
	ds_read_b128 v[104:107], v164 offset:16384
	s_waitcnt lgkmcnt(7)
	v_mfma_f32_16x16x32_bf16 v[88:91], v[108:111], v[8:11], v[88:91]
	v_mfma_f32_16x16x32_bf16 v[92:95], v[108:111], v[40:43], v[92:95]
	ds_read_b128 v[108:111], v164 offset:24576
	s_waitcnt lgkmcnt(7)
	v_mfma_f32_16x16x32_bf16 v[64:67], v[112:115], v[12:15], v[64:67]
	v_mfma_f32_16x16x32_bf16 v[68:71], v[112:115], v[44:47], v[68:71]
	v_xor_b32_e32 v164, 0x140, v163
	ds_read_b128 v[112:115], v164
	s_waitcnt lgkmcnt(7)
	v_mfma_f32_16x16x32_bf16 v[72:75], v[116:119], v[12:15], v[72:75]
	v_mfma_f32_16x16x32_bf16 v[76:79], v[116:119], v[44:47], v[76:79]
	ds_read_b128 v[116:119], v164 offset:8192
	s_waitcnt lgkmcnt(7)
	v_mfma_f32_16x16x32_bf16 v[80:83], v[120:123], v[12:15], v[80:83]
	v_mfma_f32_16x16x32_bf16 v[84:87], v[120:123], v[44:47], v[84:87]
	ds_read_b128 v[120:123], v164 offset:16384
	s_waitcnt lgkmcnt(7)
	v_mfma_f32_16x16x32_bf16 v[88:91], v[124:127], v[12:15], v[88:91]
	v_mfma_f32_16x16x32_bf16 v[92:95], v[124:127], v[44:47], v[92:95]
	ds_read_b128 v[124:127], v164 offset:24576
	s_waitcnt lgkmcnt(7)
	v_mfma_f32_16x16x32_bf16 v[64:67], v[96:99], v[16:19], v[64:67]
	v_mfma_f32_16x16x32_bf16 v[68:71], v[96:99], v[48:51], v[68:71]
	v_xor_b32_e32 v164, 0x180, v163
	ds_read_b128 v[96:99], v164
	s_waitcnt lgkmcnt(7)
	v_mfma_f32_16x16x32_bf16 v[72:75], v[100:103], v[16:19], v[72:75]
	v_mfma_f32_16x16x32_bf16 v[76:79], v[100:103], v[48:51], v[76:79]
	ds_read_b128 v[100:103], v164 offset:8192
	s_waitcnt lgkmcnt(7)
	v_mfma_f32_16x16x32_bf16 v[80:83], v[104:107], v[16:19], v[80:83]
	v_mfma_f32_16x16x32_bf16 v[84:87], v[104:107], v[48:51], v[84:87]
	ds_read_b128 v[104:107], v164 offset:16384
	s_waitcnt lgkmcnt(7)
	v_mfma_f32_16x16x32_bf16 v[88:91], v[108:111], v[16:19], v[88:91]
	v_mfma_f32_16x16x32_bf16 v[92:95], v[108:111], v[48:51], v[92:95]
	ds_read_b128 v[108:111], v164 offset:24576
	s_waitcnt lgkmcnt(7)
	v_mfma_f32_16x16x32_bf16 v[64:67], v[112:115], v[20:23], v[64:67]
	v_mfma_f32_16x16x32_bf16 v[68:71], v[112:115], v[52:55], v[68:71]
	v_xor_b32_e32 v164, 0x1c0, v163
	ds_read_b128 v[112:115], v164
	s_waitcnt lgkmcnt(7)
	v_mfma_f32_16x16x32_bf16 v[72:75], v[116:119], v[20:23], v[72:75]
	v_mfma_f32_16x16x32_bf16 v[76:79], v[116:119], v[52:55], v[76:79]
	ds_read_b128 v[116:119], v164 offset:8192
	s_waitcnt lgkmcnt(7)
	v_mfma_f32_16x16x32_bf16 v[80:83], v[120:123], v[20:23], v[80:83]
	v_mfma_f32_16x16x32_bf16 v[84:87], v[120:123], v[52:55], v[84:87]
	ds_read_b128 v[120:123], v164 offset:16384
	s_waitcnt lgkmcnt(7)
	v_mfma_f32_16x16x32_bf16 v[88:91], v[124:127], v[20:23], v[88:91]
	v_mfma_f32_16x16x32_bf16 v[92:95], v[124:127], v[52:55], v[92:95]
	ds_read_b128 v[124:127], v164 offset:24576
	s_waitcnt lgkmcnt(7)
	v_mfma_f32_16x16x32_bf16 v[64:67], v[96:99], v[24:27], v[64:67]
	v_mfma_f32_16x16x32_bf16 v[68:71], v[96:99], v[56:59], v[68:71]
	s_waitcnt lgkmcnt(6)
	v_mfma_f32_16x16x32_bf16 v[72:75], v[100:103], v[24:27], v[72:75]
	v_mfma_f32_16x16x32_bf16 v[76:79], v[100:103], v[56:59], v[76:79]
	s_waitcnt lgkmcnt(5)
	v_mfma_f32_16x16x32_bf16 v[80:83], v[104:107], v[24:27], v[80:83]
	v_mfma_f32_16x16x32_bf16 v[84:87], v[104:107], v[56:59], v[84:87]
	s_waitcnt lgkmcnt(4)
	v_mfma_f32_16x16x32_bf16 v[88:91], v[108:111], v[24:27], v[88:91]
	v_mfma_f32_16x16x32_bf16 v[92:95], v[108:111], v[56:59], v[92:95]
	s_waitcnt lgkmcnt(3)
	v_mfma_f32_16x16x32_bf16 v[64:67], v[112:115], v[28:31], v[64:67]
	v_mfma_f32_16x16x32_bf16 v[68:71], v[112:115], v[60:63], v[68:71]
	s_waitcnt lgkmcnt(2)
	v_mfma_f32_16x16x32_bf16 v[72:75], v[116:119], v[28:31], v[72:75]
	v_mfma_f32_16x16x32_bf16 v[76:79], v[116:119], v[60:63], v[76:79]
	s_waitcnt lgkmcnt(1)
	v_mfma_f32_16x16x32_bf16 v[80:83], v[120:123], v[28:31], v[80:83]
	v_mfma_f32_16x16x32_bf16 v[84:87], v[120:123], v[60:63], v[84:87]
	s_waitcnt lgkmcnt(0)
	v_mfma_f32_16x16x32_bf16 v[88:91], v[124:127], v[28:31], v[88:91]
	v_mfma_f32_16x16x32_bf16 v[92:95], v[124:127], v[60:63], v[92:95]
.Lmylru_nm_3:
	v_mov_b32_e32 v169, v165
	v_mov_b32_e32 v170, v166
	v_mov_b32_e32 v171, v167
	v_mov_b32_e32 v172, v168
	ds_read_u16 v144, v169
	ds_read_u16 v145, v170
	ds_read_u16 v146, v171
	ds_read_u16 v147, v172
	ds_read_u16 v148, v169 offset:8192
	ds_read_u16 v149, v170 offset:8192
	ds_read_u16 v150, v171 offset:8192
	ds_read_u16 v151, v172 offset:8192
	ds_read_u16 v152, v169 offset:16384
	ds_read_u16 v153, v170 offset:16384
	ds_read_u16 v154, v171 offset:16384
	ds_read_u16 v155, v172 offset:16384
	ds_read_u16 v156, v169 offset:24576
	ds_read_u16 v157, v170 offset:24576
	ds_read_u16 v158, v171 offset:24576
	ds_read_u16 v159, v172 offset:24576
	s_nop 7
	v_fma_f32 v178, v64, s53, v173
	v_fma_f32 v179, v65, s53, v173
	v_fma_f32 v180, v66, s53, v173
	v_fma_f32 v181, v67, s53, v173
	v_fma_f32 v182, v72, s53, v173
	v_fma_f32 v183, v73, s53, v173
	v_fma_f32 v184, v74, s53, v173
	v_fma_f32 v185, v75, s53, v173
	v_fma_f32 v186, v68, s53, v174
	v_fma_f32 v187, v69, s53, v174
	v_fma_f32 v188, v70, s53, v174
	v_fma_f32 v189, v71, s53, v174
	v_fma_f32 v190, v76, s53, v174
	v_fma_f32 v191, v77, s53, v174
	v_fma_f32 v192, v78, s53, v174
	v_fma_f32 v193, v79, s53, v174
	v_exp_f32_e32 v178, v178
	v_exp_f32_e32 v179, v179
	v_exp_f32_e32 v180, v180
	v_exp_f32_e32 v181, v181
	v_exp_f32_e32 v182, v182
	v_exp_f32_e32 v183, v183
	v_exp_f32_e32 v184, v184
	v_exp_f32_e32 v185, v185
	v_exp_f32_e32 v186, v186
	v_exp_f32_e32 v187, v187
	v_exp_f32_e32 v188, v188
	v_exp_f32_e32 v189, v189
	v_exp_f32_e32 v190, v190
	v_exp_f32_e32 v191, v191
	v_exp_f32_e32 v192, v192
	v_exp_f32_e32 v193, v193
	v_add_f32_e32 v178, 1.0, v178
	v_add_f32_e32 v179, 1.0, v179
	v_add_f32_e32 v180, 1.0, v180
	v_add_f32_e32 v181, 1.0, v181
	v_add_f32_e32 v182, 1.0, v182
	v_add_f32_e32 v183, 1.0, v183
	v_add_f32_e32 v184, 1.0, v184
	v_add_f32_e32 v185, 1.0, v185
	v_add_f32_e32 v186, 1.0, v186
	v_add_f32_e32 v187, 1.0, v187
	v_add_f32_e32 v188, 1.0, v188
	v_add_f32_e32 v189, 1.0, v189
	v_add_f32_e32 v190, 1.0, v190
	v_add_f32_e32 v191, 1.0, v191
	v_add_f32_e32 v192, 1.0, v192
	v_add_f32_e32 v193, 1.0, v193
	v_rcp_f32_e32 v178, v178
	v_rcp_f32_e32 v179, v179
	v_rcp_f32_e32 v180, v180
	v_rcp_f32_e32 v181, v181
	v_rcp_f32_e32 v182, v182
	v_rcp_f32_e32 v183, v183
	v_rcp_f32_e32 v184, v184
	v_rcp_f32_e32 v185, v185
	v_rcp_f32_e32 v186, v186
	v_rcp_f32_e32 v187, v187
	v_rcp_f32_e32 v188, v188
	v_rcp_f32_e32 v189, v189
	v_rcp_f32_e32 v190, v190
	v_rcp_f32_e32 v191, v191
	v_rcp_f32_e32 v192, v192
	v_rcp_f32_e32 v193, v193
	v_mul_f32_e32 v178, v175, v178
	v_mul_f32_e32 v179, v175, v179
	v_mul_f32_e32 v180, v175, v180
	v_mul_f32_e32 v181, v175, v181
	v_mul_f32_e32 v182, v175, v182
	v_mul_f32_e32 v183, v175, v183
	v_mul_f32_e32 v184, v175, v184
	v_mul_f32_e32 v185, v175, v185
	v_exp_f32_e32 v96, v178
	v_exp_f32_e32 v97, v179
	v_exp_f32_e32 v98, v180
	v_exp_f32_e32 v99, v181
	v_exp_f32_e32 v100, v182
	v_exp_f32_e32 v101, v183
	v_exp_f32_e32 v102, v184
	v_exp_f32_e32 v103, v185
	s_nop 0
	v_fma_f32 v194, -v96, v96, 1.0
	v_fma_f32 v195, -v97, v97, 1.0
	v_fma_f32 v196, -v98, v98, 1.0
	v_fma_f32 v197, -v99, v99, 1.0
	v_fma_f32 v198, -v100, v100, 1.0
	v_fma_f32 v199, -v101, v101, 1.0
	v_fma_f32 v200, -v102, v102, 1.0
	v_fma_f32 v201, -v103, v103, 1.0
	v_max_f32_e32 v194, 0, v194
	v_max_f32_e32 v195, 0, v195
	v_max_f32_e32 v196, 0, v196
	v_max_f32_e32 v197, 0, v197
	v_max_f32_e32 v198, 0, v198
	v_max_f32_e32 v199, 0, v199
	v_max_f32_e32 v200, 0, v200
	v_max_f32_e32 v201, 0, v201
	v_sqrt_f32_e32 v194, v194
	v_sqrt_f32_e32 v195, v195
	v_sqrt_f32_e32 v196, v196
	v_sqrt_f32_e32 v197, v197
	v_sqrt_f32_e32 v198, v198
	v_sqrt_f32_e32 v199, v199
	v_sqrt_f32_e32 v200, v200
	v_sqrt_f32_e32 v201, v201
	s_waitcnt lgkmcnt(8)
	v_lshlrev_b32_e32 v144, 16, v144
	v_lshlrev_b32_e32 v145, 16, v145
	v_lshlrev_b32_e32 v146, 16, v146
	v_lshlrev_b32_e32 v147, 16, v147
	v_lshlrev_b32_e32 v148, 16, v148
	v_lshlrev_b32_e32 v149, 16, v149
	v_lshlrev_b32_e32 v150, 16, v150
	v_lshlrev_b32_e32 v151, 16, v151
	v_mul_f32_e32 v194, v194, v186
	v_mul_f32_e32 v195, v195, v187
	v_mul_f32_e32 v196, v196, v188
	v_mul_f32_e32 v197, v197, v189
	v_mul_f32_e32 v198, v198, v190
	v_mul_f32_e32 v199, v199, v191
	v_mul_f32_e32 v200, v200, v192
	v_mul_f32_e32 v201, v201, v193
	v_mul_f32_e32 v144, v194, v144
	v_mul_f32_e32 v145, v195, v145
	v_mul_f32_e32 v146, v196, v146
	v_mul_f32_e32 v147, v197, v147
	v_mul_f32_e32 v148, v198, v148
	v_mul_f32_e32 v149, v199, v149
	v_mul_f32_e32 v150, v200, v150
	v_mul_f32_e32 v151, v201, v151
	v_fma_f32 v178, v80, s53, v173
	v_fma_f32 v179, v81, s53, v173
	v_fma_f32 v180, v82, s53, v173
	v_fma_f32 v181, v83, s53, v173
	v_fma_f32 v182, v88, s53, v173
	v_fma_f32 v183, v89, s53, v173
	v_fma_f32 v184, v90, s53, v173
	v_fma_f32 v185, v91, s53, v173
	v_fma_f32 v186, v84, s53, v174
	v_fma_f32 v187, v85, s53, v174
	v_fma_f32 v188, v86, s53, v174
	v_fma_f32 v189, v87, s53, v174
	v_fma_f32 v190, v92, s53, v174
	v_fma_f32 v191, v93, s53, v174
	v_fma_f32 v192, v94, s53, v174
	v_fma_f32 v193, v95, s53, v174
	v_exp_f32_e32 v178, v178
	v_exp_f32_e32 v179, v179
	v_exp_f32_e32 v180, v180
	v_exp_f32_e32 v181, v181
	v_exp_f32_e32 v182, v182
	v_exp_f32_e32 v183, v183
	v_exp_f32_e32 v184, v184
	v_exp_f32_e32 v185, v185
	v_exp_f32_e32 v186, v186
	v_exp_f32_e32 v187, v187
	v_exp_f32_e32 v188, v188
	v_exp_f32_e32 v189, v189
	v_exp_f32_e32 v190, v190
	v_exp_f32_e32 v191, v191
	v_exp_f32_e32 v192, v192
	v_exp_f32_e32 v193, v193
	v_add_f32_e32 v178, 1.0, v178
	v_add_f32_e32 v179, 1.0, v179
	v_add_f32_e32 v180, 1.0, v180
	v_add_f32_e32 v181, 1.0, v181
	v_add_f32_e32 v182, 1.0, v182
	v_add_f32_e32 v183, 1.0, v183
	v_add_f32_e32 v184, 1.0, v184
	v_add_f32_e32 v185, 1.0, v185
	v_add_f32_e32 v186, 1.0, v186
	v_add_f32_e32 v187, 1.0, v187
	v_add_f32_e32 v188, 1.0, v188
	v_add_f32_e32 v189, 1.0, v189
	v_add_f32_e32 v190, 1.0, v190
	v_add_f32_e32 v191, 1.0, v191
	v_add_f32_e32 v192, 1.0, v192
	v_add_f32_e32 v193, 1.0, v193
	v_rcp_f32_e32 v178, v178
	v_rcp_f32_e32 v179, v179
	v_rcp_f32_e32 v180, v180
	v_rcp_f32_e32 v181, v181
	v_rcp_f32_e32 v182, v182
	v_rcp_f32_e32 v183, v183
	v_rcp_f32_e32 v184, v184
	v_rcp_f32_e32 v185, v185
	v_rcp_f32_e32 v186, v186
	v_rcp_f32_e32 v187, v187
	v_rcp_f32_e32 v188, v188
	v_rcp_f32_e32 v189, v189
	v_rcp_f32_e32 v190, v190
	v_rcp_f32_e32 v191, v191
	v_rcp_f32_e32 v192, v192
	v_rcp_f32_e32 v193, v193
	v_mul_f32_e32 v178, v175, v178
	v_mul_f32_e32 v179, v175, v179
	v_mul_f32_e32 v180, v175, v180
	v_mul_f32_e32 v181, v175, v181
	v_mul_f32_e32 v182, v175, v182
	v_mul_f32_e32 v183, v175, v183
	v_mul_f32_e32 v184, v175, v184
	v_mul_f32_e32 v185, v175, v185
	v_exp_f32_e32 v104, v178
	v_exp_f32_e32 v105, v179
	v_exp_f32_e32 v106, v180
	v_exp_f32_e32 v107, v181
	v_exp_f32_e32 v108, v182
	v_exp_f32_e32 v109, v183
	v_exp_f32_e32 v110, v184
	v_exp_f32_e32 v111, v185
	s_nop 0
	v_fma_f32 v194, -v104, v104, 1.0
	v_fma_f32 v195, -v105, v105, 1.0
	v_fma_f32 v196, -v106, v106, 1.0
	v_fma_f32 v197, -v107, v107, 1.0
	v_fma_f32 v198, -v108, v108, 1.0
	v_fma_f32 v199, -v109, v109, 1.0
	v_fma_f32 v200, -v110, v110, 1.0
	v_fma_f32 v201, -v111, v111, 1.0
	v_max_f32_e32 v194, 0, v194
	v_max_f32_e32 v195, 0, v195
	v_max_f32_e32 v196, 0, v196
	v_max_f32_e32 v197, 0, v197
	v_max_f32_e32 v198, 0, v198
	v_max_f32_e32 v199, 0, v199
	v_max_f32_e32 v200, 0, v200
	v_max_f32_e32 v201, 0, v201
	v_sqrt_f32_e32 v194, v194
	v_sqrt_f32_e32 v195, v195
	v_sqrt_f32_e32 v196, v196
	v_sqrt_f32_e32 v197, v197
	v_sqrt_f32_e32 v198, v198
	v_sqrt_f32_e32 v199, v199
	v_sqrt_f32_e32 v200, v200
	v_sqrt_f32_e32 v201, v201
	s_waitcnt lgkmcnt(0)
	v_lshlrev_b32_e32 v152, 16, v152
	v_lshlrev_b32_e32 v153, 16, v153
	v_lshlrev_b32_e32 v154, 16, v154
	v_lshlrev_b32_e32 v155, 16, v155
	v_lshlrev_b32_e32 v156, 16, v156
	v_lshlrev_b32_e32 v157, 16, v157
	v_lshlrev_b32_e32 v158, 16, v158
	v_lshlrev_b32_e32 v159, 16, v159
	v_mul_f32_e32 v194, v194, v186
	v_mul_f32_e32 v195, v195, v187
	v_mul_f32_e32 v196, v196, v188
	v_mul_f32_e32 v197, v197, v189
	v_mul_f32_e32 v198, v198, v190
	v_mul_f32_e32 v199, v199, v191
	v_mul_f32_e32 v200, v200, v192
	v_mul_f32_e32 v201, v201, v193
	v_mul_f32_e32 v152, v194, v152
	v_mul_f32_e32 v153, v195, v153
	v_mul_f32_e32 v154, v196, v154
	v_mul_f32_e32 v155, v197, v155
	v_mul_f32_e32 v156, v198, v156
	v_mul_f32_e32 v157, v199, v157
	v_mul_f32_e32 v158, v200, v158
	v_mul_f32_e32 v159, v201, v159
	v_fma_f32 v145, v97, v144, v145
	v_fma_f32 v149, v101, v148, v149
	v_fma_f32 v153, v105, v152, v153
	v_fma_f32 v157, v109, v156, v157
	v_mul_f32_e32 v97, v97, v96
	v_mul_f32_e32 v101, v101, v100
	v_mul_f32_e32 v105, v105, v104
	v_mul_f32_e32 v109, v109, v108
	v_fma_f32 v146, v98, v145, v146
	v_fma_f32 v150, v102, v149, v150
	v_fma_f32 v154, v106, v153, v154
	v_fma_f32 v158, v110, v157, v158
	v_mul_f32_e32 v98, v98, v97
	v_mul_f32_e32 v102, v102, v101
	v_mul_f32_e32 v106, v106, v105
	v_mul_f32_e32 v110, v110, v109
	v_fma_f32 v147, v99, v146, v147
	v_fma_f32 v151, v103, v150, v151
	v_fma_f32 v155, v107, v154, v155
	v_fma_f32 v159, v111, v158, v159
	v_mul_f32_e32 v99, v99, v98
	v_mul_f32_e32 v103, v103, v102
	v_mul_f32_e32 v107, v107, v106
	v_mul_f32_e32 v111, v111, v110
	ds_bpermute_b32 v178, v204, v99
	ds_bpermute_b32 v182, v204, v147
	ds_bpermute_b32 v179, v204, v103
	ds_bpermute_b32 v183, v204, v151
	ds_bpermute_b32 v180, v204, v107
	ds_bpermute_b32 v184, v204, v155
	ds_bpermute_b32 v181, v204, v111
	ds_bpermute_b32 v185, v204, v159
	s_waitcnt lgkmcnt(0)
	v_fma_f32 v186, v182, v99, v147
	v_cndmask_b32_e64 v178, 1.0, v178, s[34:35]
	v_fma_f32 v187, v183, v103, v151
	v_cndmask_b32_e64 v179, 1.0, v179, s[34:35]
	v_fma_f32 v188, v184, v107, v155
	v_cndmask_b32_e64 v180, 1.0, v180, s[34:35]
	v_fma_f32 v189, v185, v111, v159
	v_cndmask_b32_e64 v181, 1.0, v181, s[34:35]
	v_cndmask_b32_e64 v223, v147, v186, s[34:35]
	v_mul_f32_e32 v219, v99, v178
	v_cndmask_b32_e64 v224, v151, v187, s[34:35]
	v_mul_f32_e32 v220, v103, v179
	v_cndmask_b32_e64 v225, v155, v188, s[34:35]
	v_mul_f32_e32 v221, v107, v180
	v_cndmask_b32_e64 v226, v159, v189, s[34:35]
	v_mul_f32_e32 v222, v111, v181
	ds_bpermute_b32 v178, v205, v219
	ds_bpermute_b32 v182, v205, v223
	ds_bpermute_b32 v179, v205, v220
	ds_bpermute_b32 v183, v205, v224
	ds_bpermute_b32 v180, v205, v221
	ds_bpermute_b32 v184, v205, v225
	ds_bpermute_b32 v181, v205, v222
	ds_bpermute_b32 v185, v205, v226
	s_waitcnt lgkmcnt(0)
	v_fma_f32 v186, v182, v219, v223
	v_cndmask_b32_e64 v178, 1.0, v178, s[36:37]
	v_fma_f32 v187, v183, v220, v224
	v_cndmask_b32_e64 v179, 1.0, v179, s[36:37]
	v_fma_f32 v188, v184, v221, v225
	v_cndmask_b32_e64 v180, 1.0, v180, s[36:37]
	v_fma_f32 v189, v185, v222, v226
	v_cndmask_b32_e64 v181, 1.0, v181, s[36:37]
	v_cndmask_b32_e64 v223, v223, v186, s[36:37]
	v_mul_f32_e32 v219, v219, v178
	v_cndmask_b32_e64 v224, v224, v187, s[36:37]
	v_mul_f32_e32 v220, v220, v179
	v_cndmask_b32_e64 v225, v225, v188, s[36:37]
	v_mul_f32_e32 v221, v221, v180
	v_cndmask_b32_e64 v226, v226, v189, s[36:37]
	v_mul_f32_e32 v222, v222, v181
	ds_bpermute_b32 v227, v204, v219
	ds_bpermute_b32 v231, v204, v223
	ds_bpermute_b32 v235, v206, v219
	ds_bpermute_b32 v239, v206, v223
	ds_bpermute_b32 v228, v204, v220
	ds_bpermute_b32 v232, v204, v224
	ds_bpermute_b32 v236, v206, v220
	ds_bpermute_b32 v244, v206, v224
	ds_bpermute_b32 v229, v204, v221
	ds_bpermute_b32 v233, v204, v225
	ds_bpermute_b32 v237, v206, v221
	ds_bpermute_b32 v245, v206, v225
	ds_bpermute_b32 v230, v204, v222
	ds_bpermute_b32 v234, v204, v226
	ds_bpermute_b32 v238, v206, v222
	ds_bpermute_b32 v246, v206, v226
	s_waitcnt lgkmcnt(0)
	v_cndmask_b32_e64 v227, 1.0, v227, s[34:35]
	v_cndmask_b32_e64 v231, 0, v231, s[34:35]
	v_cndmask_b32_e64 v228, 1.0, v228, s[34:35]
	v_cndmask_b32_e64 v232, 0, v232, s[34:35]
	v_cndmask_b32_e64 v229, 1.0, v229, s[34:35]
	v_cndmask_b32_e64 v233, 0, v233, s[34:35]
	v_cndmask_b32_e64 v230, 1.0, v230, s[34:35]
	v_cndmask_b32_e64 v234, 0, v234, s[34:35]
	v_mov_b32_e32 v190, v235
	v_mov_b32_e32 v194, v239
	v_mov_b32_e32 v198, v190
	v_mov_b32_e32 v201, v194
	v_fma_f32 v194, v194, v236, v244
	v_mul_f32_e32 v190, v190, v236
	v_mov_b32_e32 v199, v190
	v_mov_b32_e32 v177, v194
	v_fma_f32 v194, v194, v237, v245
	v_mul_f32_e32 v190, v190, v237
	v_mov_b32_e32 v200, v190
	v_mov_b32_e32 v203, v194
	v_fma_f32 v194, v194, v238, v246
	v_mul_f32_e32 v190, v190, v238
	v_mov_b32_e32 v191, v194
	ds_write_b64 v207, v[190:191]
	s_cmp_eq_u32 s13, 2
	s_cbranch_scc1 .Lmylru_t0_3
	s_waitcnt vmcnt(8)
	s_branch .Lmylru_t1_3

.Lmylru_ne_3:
	ds_read_b64 v[178:179], v208
	ds_read_b64 v[180:181], v208 offset:512
	s_waitcnt lgkmcnt(0)
	v_fma_f32 v182, v176, v178, v179
	v_cndmask_b32_e64 v183, v176, v182, s[38:39]
	v_fma_f32 v176, v182, v180, v181
	v_mov_b32_e32 v184, v183
	v_fma_f32 v185, v183, v198, v201
	v_fma_f32 v186, v183, v199, v177
	v_fma_f32 v187, v183, v200, v203
	v_fma_f32 v184, v184, v227, v231
	v_fma_f32 v185, v185, v228, v232
	v_fma_f32 v186, v186, v229, v233
	v_fma_f32 v187, v187, v230, v234
	v_fma_f32 v144, v184, v96, v144
	v_fma_f32 v148, v185, v100, v148
	v_fma_f32 v152, v186, v104, v152
	v_fma_f32 v156, v187, v108, v156
	v_fma_f32 v145, v184, v97, v145
	v_fma_f32 v149, v185, v101, v149
	v_fma_f32 v153, v186, v105, v153
	v_fma_f32 v157, v187, v109, v157
	v_fma_f32 v146, v184, v98, v146
	v_fma_f32 v150, v185, v102, v150
	v_fma_f32 v154, v186, v106, v154
	v_fma_f32 v158, v187, v110, v158
	v_fma_f32 v147, v184, v99, v147
	v_fma_f32 v151, v185, v103, v151
	v_fma_f32 v155, v186, v107, v155
	v_fma_f32 v159, v187, v111, v159
	v_cvt_pk_bf16_f32 v178, v144, v145
	v_cvt_pk_bf16_f32 v179, v146, v147
	v_cvt_pk_bf16_f32 v180, v148, v149
	v_cvt_pk_bf16_f32 v181, v150, v151
	v_cvt_pk_bf16_f32 v182, v152, v153
	v_cvt_pk_bf16_f32 v183, v154, v155
	v_cvt_pk_bf16_f32 v184, v156, v157
	v_cvt_pk_bf16_f32 v185, v158, v159
	global_store_dword v209, v178, s[44:45]
	global_store_dword v209, v179, s[44:45] offset:256
	global_store_dword v209, v180, s[44:45] offset:512
	global_store_dword v209, v181, s[44:45] offset:768
	global_store_dword v209, v182, s[44:45] offset:1024
	global_store_dword v209, v183, s[44:45] offset:1280
	global_store_dword v209, v184, s[44:45] offset:1536
	global_store_dword v209, v185, s[44:45] offset:1792
	s_add_i32 s13, s13, 1
	s_add_i32 s54, s13, -2
	s_lshl_b32 s55, s54, 14
	s_lshl_b32 s56, s6, 11
	s_add_i32 s55, s55, s56
	s_add_u32 s44, s22, s55
	s_addc_u32 s45, s23, 0
	s_cmp_eq_u32 s7, 0
	s_cbranch_scc0 .Lmylru_nm_4
	v_or_b32_e32 v163, 0x10000, v162
	ds_read_b128 v[96:99], v163
	ds_read_b128 v[100:103], v163 offset:8192
	ds_read_b128 v[104:107], v163 offset:16384
	ds_read_b128 v[108:111], v163 offset:24576
	v_xor_b32_e32 v164, 0x40, v163
	ds_read_b128 v[112:115], v164
	ds_read_b128 v[116:119], v164 offset:8192
	ds_read_b128 v[120:123], v164 offset:16384
	ds_read_b128 v[124:127], v164 offset:24576
	s_waitcnt lgkmcnt(7)
	v_mfma_f32_16x16x32_bf16 v[64:67], v[96:99], v[0:3], 0
	v_mfma_f32_16x16x32_bf16 v[68:71], v[96:99], v[32:35], 0
	v_xor_b32_e32 v164, 0x80, v163
	ds_read_b128 v[96:99], v164
	s_waitcnt lgkmcnt(7)
	v_mfma_f32_16x16x32_bf16 v[72:75], v[100:103], v[0:3], 0
	v_mfma_f32_16x16x32_bf16 v[76:79], v[100:103], v[32:35], 0
	ds_read_b128 v[100:103], v164 offset:8192
	s_waitcnt lgkmcnt(7)
	v_mfma_f32_16x16x32_bf16 v[80:83], v[104:107], v[0:3], 0
	v_mfma_f32_16x16x32_bf16 v[84:87], v[104:107], v[32:35], 0
	ds_read_b128 v[104:107], v164 offset:16384
	s_waitcnt lgkmcnt(7)
	v_mfma_f32_16x16x32_bf16 v[88:91], v[108:111], v[0:3], 0
	v_mfma_f32_16x16x32_bf16 v[92:95], v[108:111], v[32:35], 0
	ds_read_b128 v[108:111], v164 offset:24576
	s_waitcnt lgkmcnt(7)
	v_mfma_f32_16x16x32_bf16 v[64:67], v[112:115], v[4:7], v[64:67]
	v_mfma_f32_16x16x32_bf16 v[68:71], v[112:115], v[36:39], v[68:71]
	v_xor_b32_e32 v164, 0xc0, v163
	ds_read_b128 v[112:115], v164
	s_waitcnt lgkmcnt(7)
	v_mfma_f32_16x16x32_bf16 v[72:75], v[116:119], v[4:7], v[72:75]
	v_mfma_f32_16x16x32_bf16 v[76:79], v[116:119], v[36:39], v[76:79]
	ds_read_b128 v[116:119], v164 offset:8192
	s_waitcnt lgkmcnt(7)
	v_mfma_f32_16x16x32_bf16 v[80:83], v[120:123], v[4:7], v[80:83]
	v_mfma_f32_16x16x32_bf16 v[84:87], v[120:123], v[36:39], v[84:87]
	ds_read_b128 v[120:123], v164 offset:16384
	s_waitcnt lgkmcnt(7)
	v_mfma_f32_16x16x32_bf16 v[88:91], v[124:127], v[4:7], v[88:91]
	v_mfma_f32_16x16x32_bf16 v[92:95], v[124:127], v[36:39], v[92:95]
	ds_read_b128 v[124:127], v164 offset:24576
	s_waitcnt lgkmcnt(7)
	v_mfma_f32_16x16x32_bf16 v[64:67], v[96:99], v[8:11], v[64:67]
	v_mfma_f32_16x16x32_bf16 v[68:71], v[96:99], v[40:43], v[68:71]
	v_xor_b32_e32 v164, 0x100, v163
	ds_read_b128 v[96:99], v164
	s_waitcnt lgkmcnt(7)
	v_mfma_f32_16x16x32_bf16 v[72:75], v[100:103], v[8:11], v[72:75]
	v_mfma_f32_16x16x32_bf16 v[76:79], v[100:103], v[40:43], v[76:79]
	ds_read_b128 v[100:103], v164 offset:8192
	s_waitcnt lgkmcnt(7)
	v_mfma_f32_16x16x32_bf16 v[80:83], v[104:107], v[8:11], v[80:83]
	v_mfma_f32_16x16x32_bf16 v[84:87], v[104:107], v[40:43], v[84:87]
	ds_read_b128 v[104:107], v164 offset:16384
	s_waitcnt lgkmcnt(7)
	v_mfma_f32_16x16x32_bf16 v[88:91], v[108:111], v[8:11], v[88:91]
	v_mfma_f32_16x16x32_bf16 v[92:95], v[108:111], v[40:43], v[92:95]
	ds_read_b128 v[108:111], v164 offset:24576
	s_waitcnt lgkmcnt(7)
	v_mfma_f32_16x16x32_bf16 v[64:67], v[112:115], v[12:15], v[64:67]
	v_mfma_f32_16x16x32_bf16 v[68:71], v[112:115], v[44:47], v[68:71]
	v_xor_b32_e32 v164, 0x140, v163
	ds_read_b128 v[112:115], v164
	s_waitcnt lgkmcnt(7)
	v_mfma_f32_16x16x32_bf16 v[72:75], v[116:119], v[12:15], v[72:75]
	v_mfma_f32_16x16x32_bf16 v[76:79], v[116:119], v[44:47], v[76:79]
	ds_read_b128 v[116:119], v164 offset:8192
	s_waitcnt lgkmcnt(7)
	v_mfma_f32_16x16x32_bf16 v[80:83], v[120:123], v[12:15], v[80:83]
	v_mfma_f32_16x16x32_bf16 v[84:87], v[120:123], v[44:47], v[84:87]
	ds_read_b128 v[120:123], v164 offset:16384
	s_waitcnt lgkmcnt(7)
	v_mfma_f32_16x16x32_bf16 v[88:91], v[124:127], v[12:15], v[88:91]
	v_mfma_f32_16x16x32_bf16 v[92:95], v[124:127], v[44:47], v[92:95]
	ds_read_b128 v[124:127], v164 offset:24576
	s_waitcnt lgkmcnt(7)
	v_mfma_f32_16x16x32_bf16 v[64:67], v[96:99], v[16:19], v[64:67]
	v_mfma_f32_16x16x32_bf16 v[68:71], v[96:99], v[48:51], v[68:71]
	v_xor_b32_e32 v164, 0x180, v163
	ds_read_b128 v[96:99], v164
	s_waitcnt lgkmcnt(7)
	v_mfma_f32_16x16x32_bf16 v[72:75], v[100:103], v[16:19], v[72:75]
	v_mfma_f32_16x16x32_bf16 v[76:79], v[100:103], v[48:51], v[76:79]
	ds_read_b128 v[100:103], v164 offset:8192
	s_waitcnt lgkmcnt(7)
	v_mfma_f32_16x16x32_bf16 v[80:83], v[104:107], v[16:19], v[80:83]
	v_mfma_f32_16x16x32_bf16 v[84:87], v[104:107], v[48:51], v[84:87]
	ds_read_b128 v[104:107], v164 offset:16384
	s_waitcnt lgkmcnt(7)
	v_mfma_f32_16x16x32_bf16 v[88:91], v[108:111], v[16:19], v[88:91]
	v_mfma_f32_16x16x32_bf16 v[92:95], v[108:111], v[48:51], v[92:95]
	ds_read_b128 v[108:111], v164 offset:24576
	s_waitcnt lgkmcnt(7)
	v_mfma_f32_16x16x32_bf16 v[64:67], v[112:115], v[20:23], v[64:67]
	v_mfma_f32_16x16x32_bf16 v[68:71], v[112:115], v[52:55], v[68:71]
	v_xor_b32_e32 v164, 0x1c0, v163
	ds_read_b128 v[112:115], v164
	s_waitcnt lgkmcnt(7)
	v_mfma_f32_16x16x32_bf16 v[72:75], v[116:119], v[20:23], v[72:75]
	v_mfma_f32_16x16x32_bf16 v[76:79], v[116:119], v[52:55], v[76:79]
	ds_read_b128 v[116:119], v164 offset:8192
	s_waitcnt lgkmcnt(7)
	v_mfma_f32_16x16x32_bf16 v[80:83], v[120:123], v[20:23], v[80:83]
	v_mfma_f32_16x16x32_bf16 v[84:87], v[120:123], v[52:55], v[84:87]
	ds_read_b128 v[120:123], v164 offset:16384
	s_waitcnt lgkmcnt(7)
	v_mfma_f32_16x16x32_bf16 v[88:91], v[124:127], v[20:23], v[88:91]
	v_mfma_f32_16x16x32_bf16 v[92:95], v[124:127], v[52:55], v[92:95]
	ds_read_b128 v[124:127], v164 offset:24576
	s_waitcnt lgkmcnt(7)
	v_mfma_f32_16x16x32_bf16 v[64:67], v[96:99], v[24:27], v[64:67]
	v_mfma_f32_16x16x32_bf16 v[68:71], v[96:99], v[56:59], v[68:71]
	s_waitcnt lgkmcnt(6)
	v_mfma_f32_16x16x32_bf16 v[72:75], v[100:103], v[24:27], v[72:75]
	v_mfma_f32_16x16x32_bf16 v[76:79], v[100:103], v[56:59], v[76:79]
	s_waitcnt lgkmcnt(5)
	v_mfma_f32_16x16x32_bf16 v[80:83], v[104:107], v[24:27], v[80:83]
	v_mfma_f32_16x16x32_bf16 v[84:87], v[104:107], v[56:59], v[84:87]
	s_waitcnt lgkmcnt(4)
	v_mfma_f32_16x16x32_bf16 v[88:91], v[108:111], v[24:27], v[88:91]
	v_mfma_f32_16x16x32_bf16 v[92:95], v[108:111], v[56:59], v[92:95]
	s_waitcnt lgkmcnt(3)
	v_mfma_f32_16x16x32_bf16 v[64:67], v[112:115], v[28:31], v[64:67]
	v_mfma_f32_16x16x32_bf16 v[68:71], v[112:115], v[60:63], v[68:71]
	s_waitcnt lgkmcnt(2)
	v_mfma_f32_16x16x32_bf16 v[72:75], v[116:119], v[28:31], v[72:75]
	v_mfma_f32_16x16x32_bf16 v[76:79], v[116:119], v[60:63], v[76:79]
	s_waitcnt lgkmcnt(1)
	v_mfma_f32_16x16x32_bf16 v[80:83], v[120:123], v[28:31], v[80:83]
	v_mfma_f32_16x16x32_bf16 v[84:87], v[120:123], v[60:63], v[84:87]
	s_waitcnt lgkmcnt(0)
	v_mfma_f32_16x16x32_bf16 v[88:91], v[124:127], v[28:31], v[88:91]
	v_mfma_f32_16x16x32_bf16 v[92:95], v[124:127], v[60:63], v[92:95]
.Lmylru_nm_4:
	v_or_b32_e32 v169, 0x10000, v165
	v_or_b32_e32 v170, 0x10000, v166
	v_or_b32_e32 v171, 0x10000, v167
	v_or_b32_e32 v172, 0x10000, v168
	ds_read_u16 v144, v169
	ds_read_u16 v145, v170
	ds_read_u16 v146, v171
	ds_read_u16 v147, v172
	ds_read_u16 v148, v169 offset:8192
	ds_read_u16 v149, v170 offset:8192
	ds_read_u16 v150, v171 offset:8192
	ds_read_u16 v151, v172 offset:8192
	ds_read_u16 v152, v169 offset:16384
	ds_read_u16 v153, v170 offset:16384
	ds_read_u16 v154, v171 offset:16384
	ds_read_u16 v155, v172 offset:16384
	ds_read_u16 v156, v169 offset:24576
	ds_read_u16 v157, v170 offset:24576
	ds_read_u16 v158, v171 offset:24576
	ds_read_u16 v159, v172 offset:24576
	s_nop 7
	v_fma_f32 v178, v64, s53, v173
	v_fma_f32 v179, v65, s53, v173
	v_fma_f32 v180, v66, s53, v173
	v_fma_f32 v181, v67, s53, v173
	v_fma_f32 v182, v72, s53, v173
	v_fma_f32 v183, v73, s53, v173
	v_fma_f32 v184, v74, s53, v173
	v_fma_f32 v185, v75, s53, v173
	v_fma_f32 v186, v68, s53, v174
	v_fma_f32 v187, v69, s53, v174
	v_fma_f32 v188, v70, s53, v174
	v_fma_f32 v189, v71, s53, v174
	v_fma_f32 v190, v76, s53, v174
	v_fma_f32 v191, v77, s53, v174
	v_fma_f32 v192, v78, s53, v174
	v_fma_f32 v193, v79, s53, v174
	v_exp_f32_e32 v178, v178
	v_exp_f32_e32 v179, v179
	v_exp_f32_e32 v180, v180
	v_exp_f32_e32 v181, v181
	v_exp_f32_e32 v182, v182
	v_exp_f32_e32 v183, v183
	v_exp_f32_e32 v184, v184
	v_exp_f32_e32 v185, v185
	v_exp_f32_e32 v186, v186
	v_exp_f32_e32 v187, v187
	v_exp_f32_e32 v188, v188
	v_exp_f32_e32 v189, v189
	v_exp_f32_e32 v190, v190
	v_exp_f32_e32 v191, v191
	v_exp_f32_e32 v192, v192
	v_exp_f32_e32 v193, v193
	v_add_f32_e32 v178, 1.0, v178
	v_add_f32_e32 v179, 1.0, v179
	v_add_f32_e32 v180, 1.0, v180
	v_add_f32_e32 v181, 1.0, v181
	v_add_f32_e32 v182, 1.0, v182
	v_add_f32_e32 v183, 1.0, v183
	v_add_f32_e32 v184, 1.0, v184
	v_add_f32_e32 v185, 1.0, v185
	v_add_f32_e32 v186, 1.0, v186
	v_add_f32_e32 v187, 1.0, v187
	v_add_f32_e32 v188, 1.0, v188
	v_add_f32_e32 v189, 1.0, v189
	v_add_f32_e32 v190, 1.0, v190
	v_add_f32_e32 v191, 1.0, v191
	v_add_f32_e32 v192, 1.0, v192
	v_add_f32_e32 v193, 1.0, v193
	v_rcp_f32_e32 v178, v178
	v_rcp_f32_e32 v179, v179
	v_rcp_f32_e32 v180, v180
	v_rcp_f32_e32 v181, v181
	v_rcp_f32_e32 v182, v182
	v_rcp_f32_e32 v183, v183
	v_rcp_f32_e32 v184, v184
	v_rcp_f32_e32 v185, v185
	v_rcp_f32_e32 v186, v186
	v_rcp_f32_e32 v187, v187
	v_rcp_f32_e32 v188, v188
	v_rcp_f32_e32 v189, v189
	v_rcp_f32_e32 v190, v190
	v_rcp_f32_e32 v191, v191
	v_rcp_f32_e32 v192, v192
	v_rcp_f32_e32 v193, v193
	v_mul_f32_e32 v178, v175, v178
	v_mul_f32_e32 v179, v175, v179
	v_mul_f32_e32 v180, v175, v180
	v_mul_f32_e32 v181, v175, v181
	v_mul_f32_e32 v182, v175, v182
	v_mul_f32_e32 v183, v175, v183
	v_mul_f32_e32 v184, v175, v184
	v_mul_f32_e32 v185, v175, v185
	v_exp_f32_e32 v96, v178
	v_exp_f32_e32 v97, v179
	v_exp_f32_e32 v98, v180
	v_exp_f32_e32 v99, v181
	v_exp_f32_e32 v100, v182
	v_exp_f32_e32 v101, v183
	v_exp_f32_e32 v102, v184
	v_exp_f32_e32 v103, v185
	s_nop 0
	v_fma_f32 v194, -v96, v96, 1.0
	v_fma_f32 v195, -v97, v97, 1.0
	v_fma_f32 v196, -v98, v98, 1.0
	v_fma_f32 v197, -v99, v99, 1.0
	v_fma_f32 v198, -v100, v100, 1.0
	v_fma_f32 v199, -v101, v101, 1.0
	v_fma_f32 v200, -v102, v102, 1.0
	v_fma_f32 v201, -v103, v103, 1.0
	v_max_f32_e32 v194, 0, v194
	v_max_f32_e32 v195, 0, v195
	v_max_f32_e32 v196, 0, v196
	v_max_f32_e32 v197, 0, v197
	v_max_f32_e32 v198, 0, v198
	v_max_f32_e32 v199, 0, v199
	v_max_f32_e32 v200, 0, v200
	v_max_f32_e32 v201, 0, v201
	v_sqrt_f32_e32 v194, v194
	v_sqrt_f32_e32 v195, v195
	v_sqrt_f32_e32 v196, v196
	v_sqrt_f32_e32 v197, v197
	v_sqrt_f32_e32 v198, v198
	v_sqrt_f32_e32 v199, v199
	v_sqrt_f32_e32 v200, v200
	v_sqrt_f32_e32 v201, v201
	s_waitcnt lgkmcnt(8)
	v_lshlrev_b32_e32 v144, 16, v144
	v_lshlrev_b32_e32 v145, 16, v145
	v_lshlrev_b32_e32 v146, 16, v146
	v_lshlrev_b32_e32 v147, 16, v147
	v_lshlrev_b32_e32 v148, 16, v148
	v_lshlrev_b32_e32 v149, 16, v149
	v_lshlrev_b32_e32 v150, 16, v150
	v_lshlrev_b32_e32 v151, 16, v151
	v_mul_f32_e32 v194, v194, v186
	v_mul_f32_e32 v195, v195, v187
	v_mul_f32_e32 v196, v196, v188
	v_mul_f32_e32 v197, v197, v189
	v_mul_f32_e32 v198, v198, v190
	v_mul_f32_e32 v199, v199, v191
	v_mul_f32_e32 v200, v200, v192
	v_mul_f32_e32 v201, v201, v193
	v_mul_f32_e32 v144, v194, v144
	v_mul_f32_e32 v145, v195, v145
	v_mul_f32_e32 v146, v196, v146
	v_mul_f32_e32 v147, v197, v147
	v_mul_f32_e32 v148, v198, v148
	v_mul_f32_e32 v149, v199, v149
	v_mul_f32_e32 v150, v200, v150
	v_mul_f32_e32 v151, v201, v151
	v_fma_f32 v178, v80, s53, v173
	v_fma_f32 v179, v81, s53, v173
	v_fma_f32 v180, v82, s53, v173
	v_fma_f32 v181, v83, s53, v173
	v_fma_f32 v182, v88, s53, v173
	v_fma_f32 v183, v89, s53, v173
	v_fma_f32 v184, v90, s53, v173
	v_fma_f32 v185, v91, s53, v173
	v_fma_f32 v186, v84, s53, v174
	v_fma_f32 v187, v85, s53, v174
	v_fma_f32 v188, v86, s53, v174
	v_fma_f32 v189, v87, s53, v174
	v_fma_f32 v190, v92, s53, v174
	v_fma_f32 v191, v93, s53, v174
	v_fma_f32 v192, v94, s53, v174
	v_fma_f32 v193, v95, s53, v174
	v_exp_f32_e32 v178, v178
	v_exp_f32_e32 v179, v179
	v_exp_f32_e32 v180, v180
	v_exp_f32_e32 v181, v181
	v_exp_f32_e32 v182, v182
	v_exp_f32_e32 v183, v183
	v_exp_f32_e32 v184, v184
	v_exp_f32_e32 v185, v185
	v_exp_f32_e32 v186, v186
	v_exp_f32_e32 v187, v187
	v_exp_f32_e32 v188, v188
	v_exp_f32_e32 v189, v189
	v_exp_f32_e32 v190, v190
	v_exp_f32_e32 v191, v191
	v_exp_f32_e32 v192, v192
	v_exp_f32_e32 v193, v193
	v_add_f32_e32 v178, 1.0, v178
	v_add_f32_e32 v179, 1.0, v179
	v_add_f32_e32 v180, 1.0, v180
	v_add_f32_e32 v181, 1.0, v181
	v_add_f32_e32 v182, 1.0, v182
	v_add_f32_e32 v183, 1.0, v183
	v_add_f32_e32 v184, 1.0, v184
	v_add_f32_e32 v185, 1.0, v185
	v_add_f32_e32 v186, 1.0, v186
	v_add_f32_e32 v187, 1.0, v187
	v_add_f32_e32 v188, 1.0, v188
	v_add_f32_e32 v189, 1.0, v189
	v_add_f32_e32 v190, 1.0, v190
	v_add_f32_e32 v191, 1.0, v191
	v_add_f32_e32 v192, 1.0, v192
	v_add_f32_e32 v193, 1.0, v193
	v_rcp_f32_e32 v178, v178
	v_rcp_f32_e32 v179, v179
	v_rcp_f32_e32 v180, v180
	v_rcp_f32_e32 v181, v181
	v_rcp_f32_e32 v182, v182
	v_rcp_f32_e32 v183, v183
	v_rcp_f32_e32 v184, v184
	v_rcp_f32_e32 v185, v185
	v_rcp_f32_e32 v186, v186
	v_rcp_f32_e32 v187, v187
	v_rcp_f32_e32 v188, v188
	v_rcp_f32_e32 v189, v189
	v_rcp_f32_e32 v190, v190
	v_rcp_f32_e32 v191, v191
	v_rcp_f32_e32 v192, v192
	v_rcp_f32_e32 v193, v193
	v_mul_f32_e32 v178, v175, v178
	v_mul_f32_e32 v179, v175, v179
	v_mul_f32_e32 v180, v175, v180
	v_mul_f32_e32 v181, v175, v181
	v_mul_f32_e32 v182, v175, v182
	v_mul_f32_e32 v183, v175, v183
	v_mul_f32_e32 v184, v175, v184
	v_mul_f32_e32 v185, v175, v185
	v_exp_f32_e32 v104, v178
	v_exp_f32_e32 v105, v179
	v_exp_f32_e32 v106, v180
	v_exp_f32_e32 v107, v181
	v_exp_f32_e32 v108, v182
	v_exp_f32_e32 v109, v183
	v_exp_f32_e32 v110, v184
	v_exp_f32_e32 v111, v185
	s_nop 0
	v_fma_f32 v194, -v104, v104, 1.0
	v_fma_f32 v195, -v105, v105, 1.0
	v_fma_f32 v196, -v106, v106, 1.0
	v_fma_f32 v197, -v107, v107, 1.0
	v_fma_f32 v198, -v108, v108, 1.0
	v_fma_f32 v199, -v109, v109, 1.0
	v_fma_f32 v200, -v110, v110, 1.0
	v_fma_f32 v201, -v111, v111, 1.0
	v_max_f32_e32 v194, 0, v194
	v_max_f32_e32 v195, 0, v195
	v_max_f32_e32 v196, 0, v196
	v_max_f32_e32 v197, 0, v197
	v_max_f32_e32 v198, 0, v198
	v_max_f32_e32 v199, 0, v199
	v_max_f32_e32 v200, 0, v200
	v_max_f32_e32 v201, 0, v201
	v_sqrt_f32_e32 v194, v194
	v_sqrt_f32_e32 v195, v195
	v_sqrt_f32_e32 v196, v196
	v_sqrt_f32_e32 v197, v197
	v_sqrt_f32_e32 v198, v198
	v_sqrt_f32_e32 v199, v199
	v_sqrt_f32_e32 v200, v200
	v_sqrt_f32_e32 v201, v201
	s_waitcnt lgkmcnt(0)
	v_lshlrev_b32_e32 v152, 16, v152
	v_lshlrev_b32_e32 v153, 16, v153
	v_lshlrev_b32_e32 v154, 16, v154
	v_lshlrev_b32_e32 v155, 16, v155
	v_lshlrev_b32_e32 v156, 16, v156
	v_lshlrev_b32_e32 v157, 16, v157
	v_lshlrev_b32_e32 v158, 16, v158
	v_lshlrev_b32_e32 v159, 16, v159
	v_mul_f32_e32 v194, v194, v186
	v_mul_f32_e32 v195, v195, v187
	v_mul_f32_e32 v196, v196, v188
	v_mul_f32_e32 v197, v197, v189
	v_mul_f32_e32 v198, v198, v190
	v_mul_f32_e32 v199, v199, v191
	v_mul_f32_e32 v200, v200, v192
	v_mul_f32_e32 v201, v201, v193
	v_mul_f32_e32 v152, v194, v152
	v_mul_f32_e32 v153, v195, v153
	v_mul_f32_e32 v154, v196, v154
	v_mul_f32_e32 v155, v197, v155
	v_mul_f32_e32 v156, v198, v156
	v_mul_f32_e32 v157, v199, v157
	v_mul_f32_e32 v158, v200, v158
	v_mul_f32_e32 v159, v201, v159
	v_fma_f32 v145, v97, v144, v145
	v_fma_f32 v149, v101, v148, v149
	v_fma_f32 v153, v105, v152, v153
	v_fma_f32 v157, v109, v156, v157
	v_mul_f32_e32 v97, v97, v96
	v_mul_f32_e32 v101, v101, v100
	v_mul_f32_e32 v105, v105, v104
	v_mul_f32_e32 v109, v109, v108
	v_fma_f32 v146, v98, v145, v146
	v_fma_f32 v150, v102, v149, v150
	v_fma_f32 v154, v106, v153, v154
	v_fma_f32 v158, v110, v157, v158
	v_mul_f32_e32 v98, v98, v97
	v_mul_f32_e32 v102, v102, v101
	v_mul_f32_e32 v106, v106, v105
	v_mul_f32_e32 v110, v110, v109
	v_fma_f32 v147, v99, v146, v147
	v_fma_f32 v151, v103, v150, v151
	v_fma_f32 v155, v107, v154, v155
	v_fma_f32 v159, v111, v158, v159
	v_mul_f32_e32 v99, v99, v98
	v_mul_f32_e32 v103, v103, v102
	v_mul_f32_e32 v107, v107, v106
	v_mul_f32_e32 v111, v111, v110
	ds_bpermute_b32 v178, v204, v99
	ds_bpermute_b32 v182, v204, v147
	ds_bpermute_b32 v179, v204, v103
	ds_bpermute_b32 v183, v204, v151
	ds_bpermute_b32 v180, v204, v107
	ds_bpermute_b32 v184, v204, v155
	ds_bpermute_b32 v181, v204, v111
	ds_bpermute_b32 v185, v204, v159
	s_waitcnt lgkmcnt(0)
	v_fma_f32 v186, v182, v99, v147
	v_cndmask_b32_e64 v178, 1.0, v178, s[34:35]
	v_fma_f32 v187, v183, v103, v151
	v_cndmask_b32_e64 v179, 1.0, v179, s[34:35]
	v_fma_f32 v188, v184, v107, v155
	v_cndmask_b32_e64 v180, 1.0, v180, s[34:35]
	v_fma_f32 v189, v185, v111, v159
	v_cndmask_b32_e64 v181, 1.0, v181, s[34:35]
	v_cndmask_b32_e64 v223, v147, v186, s[34:35]
	v_mul_f32_e32 v219, v99, v178
	v_cndmask_b32_e64 v224, v151, v187, s[34:35]
	v_mul_f32_e32 v220, v103, v179
	v_cndmask_b32_e64 v225, v155, v188, s[34:35]
	v_mul_f32_e32 v221, v107, v180
	v_cndmask_b32_e64 v226, v159, v189, s[34:35]
	v_mul_f32_e32 v222, v111, v181
	ds_bpermute_b32 v178, v205, v219
	ds_bpermute_b32 v182, v205, v223
	ds_bpermute_b32 v179, v205, v220
	ds_bpermute_b32 v183, v205, v224
	ds_bpermute_b32 v180, v205, v221
	ds_bpermute_b32 v184, v205, v225
	ds_bpermute_b32 v181, v205, v222
	ds_bpermute_b32 v185, v205, v226
	s_waitcnt lgkmcnt(0)
	v_fma_f32 v186, v182, v219, v223
	v_cndmask_b32_e64 v178, 1.0, v178, s[36:37]
	v_fma_f32 v187, v183, v220, v224
	v_cndmask_b32_e64 v179, 1.0, v179, s[36:37]
	v_fma_f32 v188, v184, v221, v225
	v_cndmask_b32_e64 v180, 1.0, v180, s[36:37]
	v_fma_f32 v189, v185, v222, v226
	v_cndmask_b32_e64 v181, 1.0, v181, s[36:37]
	v_cndmask_b32_e64 v223, v223, v186, s[36:37]
	v_mul_f32_e32 v219, v219, v178
	v_cndmask_b32_e64 v224, v224, v187, s[36:37]
	v_mul_f32_e32 v220, v220, v179
	v_cndmask_b32_e64 v225, v225, v188, s[36:37]
	v_mul_f32_e32 v221, v221, v180
	v_cndmask_b32_e64 v226, v226, v189, s[36:37]
	v_mul_f32_e32 v222, v222, v181
	ds_bpermute_b32 v227, v204, v219
	ds_bpermute_b32 v231, v204, v223
	ds_bpermute_b32 v235, v206, v219
	ds_bpermute_b32 v239, v206, v223
	ds_bpermute_b32 v228, v204, v220
	ds_bpermute_b32 v232, v204, v224
	ds_bpermute_b32 v236, v206, v220
	ds_bpermute_b32 v244, v206, v224
	ds_bpermute_b32 v229, v204, v221
	ds_bpermute_b32 v233, v204, v225
	ds_bpermute_b32 v237, v206, v221
	ds_bpermute_b32 v245, v206, v225
	ds_bpermute_b32 v230, v204, v222
	ds_bpermute_b32 v234, v204, v226
	ds_bpermute_b32 v238, v206, v222
	ds_bpermute_b32 v246, v206, v226
	s_waitcnt lgkmcnt(0)
	v_cndmask_b32_e64 v227, 1.0, v227, s[34:35]
	v_cndmask_b32_e64 v231, 0, v231, s[34:35]
	v_cndmask_b32_e64 v228, 1.0, v228, s[34:35]
	v_cndmask_b32_e64 v232, 0, v232, s[34:35]
	v_cndmask_b32_e64 v229, 1.0, v229, s[34:35]
	v_cndmask_b32_e64 v233, 0, v233, s[34:35]
	v_cndmask_b32_e64 v230, 1.0, v230, s[34:35]
	v_cndmask_b32_e64 v234, 0, v234, s[34:35]
	v_mov_b32_e32 v190, v235
	v_mov_b32_e32 v194, v239
	v_mov_b32_e32 v198, v190
	v_mov_b32_e32 v201, v194
	v_fma_f32 v194, v194, v236, v244
	v_mul_f32_e32 v190, v190, v236
	v_mov_b32_e32 v199, v190
	v_mov_b32_e32 v177, v194
	v_fma_f32 v194, v194, v237, v245
	v_mul_f32_e32 v190, v190, v237
	v_mov_b32_e32 v200, v190
	v_mov_b32_e32 v203, v194
	v_fma_f32 v194, v194, v238, v246
	v_mul_f32_e32 v190, v190, v238
	v_mov_b32_e32 v191, v194
	ds_write_b64 v207, v[190:191] offset:1024
	s_cmp_eq_u32 s13, 2
	s_cbranch_scc1 .Lmylru_t0_4
	s_waitcnt vmcnt(8)
	s_branch .Lmylru_t1_4

.Lmylru_ne_4:
	ds_read_b64 v[178:179], v208 offset:1024
	ds_read_b64 v[180:181], v208 offset:1536
	s_waitcnt lgkmcnt(0)
	v_fma_f32 v182, v176, v178, v179
	v_cndmask_b32_e64 v183, v176, v182, s[38:39]
	v_fma_f32 v176, v182, v180, v181
	v_mov_b32_e32 v184, v183
	v_fma_f32 v185, v183, v198, v201
	v_fma_f32 v186, v183, v199, v177
	v_fma_f32 v187, v183, v200, v203
	v_fma_f32 v184, v184, v227, v231
	v_fma_f32 v185, v185, v228, v232
	v_fma_f32 v186, v186, v229, v233
	v_fma_f32 v187, v187, v230, v234
	v_fma_f32 v144, v184, v96, v144
	v_fma_f32 v148, v185, v100, v148
	v_fma_f32 v152, v186, v104, v152
	v_fma_f32 v156, v187, v108, v156
	v_fma_f32 v145, v184, v97, v145
	v_fma_f32 v149, v185, v101, v149
	v_fma_f32 v153, v186, v105, v153
	v_fma_f32 v157, v187, v109, v157
	v_fma_f32 v146, v184, v98, v146
	v_fma_f32 v150, v185, v102, v150
	v_fma_f32 v154, v186, v106, v154
	v_fma_f32 v158, v187, v110, v158
	v_fma_f32 v147, v184, v99, v147
	v_fma_f32 v151, v185, v103, v151
	v_fma_f32 v155, v186, v107, v155
	v_fma_f32 v159, v187, v111, v159
	v_cvt_pk_bf16_f32 v178, v144, v145
	v_cvt_pk_bf16_f32 v179, v146, v147
	v_cvt_pk_bf16_f32 v180, v148, v149
	v_cvt_pk_bf16_f32 v181, v150, v151
	v_cvt_pk_bf16_f32 v182, v152, v153
	v_cvt_pk_bf16_f32 v183, v154, v155
	v_cvt_pk_bf16_f32 v184, v156, v157
	v_cvt_pk_bf16_f32 v185, v158, v159
	global_store_dword v209, v178, s[44:45]
	global_store_dword v209, v179, s[44:45] offset:256
	global_store_dword v209, v180, s[44:45] offset:512
	global_store_dword v209, v181, s[44:45] offset:768
	global_store_dword v209, v182, s[44:45] offset:1024
	global_store_dword v209, v183, s[44:45] offset:1280
	global_store_dword v209, v184, s[44:45] offset:1536
	global_store_dword v209, v185, s[44:45] offset:1792
	s_add_i32 s13, s13, 1
	s_add_i32 s60, s60, -1
	s_cmp_lg_u32 s60, 0
	s_cbranch_scc1 .Lmylru_loop_0
	s_lshl_b32 s50, s10, 10
	s_lshl_b32 s51, s11, 6
	s_add_i32 s50, s50, s51
	s_lshl_b32 s51, s8, 4
	s_add_i32 s50, s50, s51
	s_add_i32 s50, s50, 512
	s_lshl_b32 s50, s50, 9
	s_add_u32 s46, s2, s50
	s_addc_u32 s47, s3, 0
	s_add_u32 s46, s46, 0x1000000
	s_addc_u32 s47, s47, 0
	s_add_u32 s48, s46, 0x20000
	s_addc_u32 s49, s47, 0
	v_lshlrev_b32_e32 v178, 9, v160
	v_lshl_add_u32 v178, v161, 4, v178
	global_load_dwordx4 v[0:3], v178, s[46:47]
	global_load_dwordx4 v[4:7], v178, s[46:47] offset:64
	global_load_dwordx4 v[8:11], v178, s[46:47] offset:128
	global_load_dwordx4 v[12:15], v178, s[46:47] offset:192
	global_load_dwordx4 v[16:19], v178, s[46:47] offset:256
	global_load_dwordx4 v[20:23], v178, s[46:47] offset:320
	global_load_dwordx4 v[24:27], v178, s[46:47] offset:384
	global_load_dwordx4 v[28:31], v178, s[46:47] offset:448
	global_load_dwordx4 v[32:35], v178, s[48:49]
	global_load_dwordx4 v[36:39], v178, s[48:49] offset:64
	global_load_dwordx4 v[40:43], v178, s[48:49] offset:128
	global_load_dwordx4 v[44:47], v178, s[48:49] offset:192
	global_load_dwordx4 v[48:51], v178, s[48:49] offset:256
	global_load_dwordx4 v[52:55], v178, s[48:49] offset:320
	global_load_dwordx4 v[56:59], v178, s[48:49] offset:384
	global_load_dwordx4 v[60:63], v178, s[48:49] offset:448
	s_load_dwordx2 s[46:47], s[0:1], 0xc8
	s_load_dwordx2 s[48:49], s[0:1], 0xd8
	s_load_dwordx2 s[40:41], s[0:1], 0xe0
	s_lshl_b32 s50, s10, 8
	s_lshl_b32 s51, s11, 6
	s_add_i32 s50, s50, s51
	s_lshl_b32 s51, s8, 4
	s_add_i32 s50, s50, s51
	v_add_u32_e32 v179, s50, v160
	v_lshlrev_b32_e32 v179, 2, v179
	s_waitcnt lgkmcnt(0)
	global_load_dword v173, v179, s[46:47]
	global_load_dword v174, v179, s[48:49]
	global_load_dword v175, v179, s[40:41]
	v_cmp_gt_u32_e64 s[34:35], 48, v202
	v_cmp_gt_u32_e64 s[36:37], 32, v202
	v_add_u32_e32 v204, 16, v202
	v_add_u32_e32 v205, 32, v202
	v_mov_b32_e32 v206, v160
	s_cmp_eq_u32 s7, 0
	s_cselect_b64 s[38:39], -1, 0
	v_and_b32_e32 v204, 63, v204
	v_lshlrev_b32_e32 v204, 2, v204
	v_and_b32_e32 v205, 63, v205
	v_lshlrev_b32_e32 v205, 2, v205
	v_and_b32_e32 v206, 63, v206
	v_lshlrev_b32_e32 v206, 2, v206
	v_mov_b32_e32 v176, 0
	s_mov_b32 s53, 0xbfb8aa3b
	s_waitcnt vmcnt(0)
	v_mul_f32_e32 v173, s53, v173
	v_mul_f32_e32 v174, s53, v174
	v_mul_f32_e32 v175, s53, v175
	v_exp_f32_e32 v175, v175
	s_nop 0
	v_add_f32_e32 v180, 1.0, v175
	v_log_f32_e32 v180, v180
	v_mov_b32_e32 v181, 0x3eaaaaab
	v_fma_f32 v181, v175, v181, -0.5
	v_fma_f32 v181, v175, v181, 1.0
	v_mul_f32_e32 v181, v175, v181
	v_mul_f32_e32 v181, 0x3fb8aa3b, v181
	v_cmp_gt_f32_e32 vcc, 0x3cf5c28f, v175
	s_nop 1
	v_cndmask_b32_e32 v175, v180, v181, vcc
	v_mul_f32_e32 v175, 0xc1000000, v175
	s_mov_b32 s13, 0
	s_barrier
	s_cmp_lt_u32 s13, 2
	s_sub_i32 s50, 1, s13
	s_lshl_b32 s50, s50, 7
	s_lshl_b32 s51, s9, 8
	s_add_i32 s51, s51, 0x8000
	s_add_i32 s51, s51, s50
	s_sub_i32 s50, 17, s13
	s_lshl_b32 s50, s50, 7
	s_lshl_b32 s59, s9, 11
	s_add_i32 s59, s59, s50
	s_cmp_lt_u32 s13, 2
	s_cselect_b32 s59, s51, s59
	s_lshl_b32 s52, s59, 11
	s_add_u32 s46, s16, s52
	s_addc_u32 s47, s17, 0
	s_lshl_b32 s52, s6, 13
	s_mov_b32 m0, s52
	s_add_i32 s52, s52, 0x400
	global_load_lds_dwordx4 v211, s[46:47]
	s_mov_b32 m0, s52
	s_add_i32 s52, s52, 0x400
	global_load_lds_dwordx4 v212, s[46:47]
	s_mov_b32 m0, s52
	s_add_i32 s52, s52, 0x400
	global_load_lds_dwordx4 v213, s[46:47]
	s_mov_b32 m0, s52
	s_add_i32 s52, s52, 0x400
	global_load_lds_dwordx4 v214, s[46:47]
	s_mov_b32 m0, s52
	s_add_i32 s52, s52, 0x400
	global_load_lds_dwordx4 v215, s[46:47]
	s_mov_b32 m0, s52
	s_add_i32 s52, s52, 0x400
	global_load_lds_dwordx4 v216, s[46:47]
	s_mov_b32 m0, s52
	s_add_i32 s52, s52, 0x400
	global_load_lds_dwordx4 v217, s[46:47]
	s_mov_b32 m0, s52
	s_nop 0
	global_load_lds_dwordx4 v218, s[46:47]
	s_mov_b32 s58, 1
	s_cmp_lt_u32 s58, 2
	s_sub_i32 s50, 1, s58
	s_lshl_b32 s50, s50, 7
	s_lshl_b32 s51, s9, 8
	s_add_i32 s51, s51, 0x8000
	s_add_i32 s51, s51, s50
	s_sub_i32 s50, 17, s58
	s_lshl_b32 s50, s50, 7
	s_lshl_b32 s59, s9, 11
	s_add_i32 s59, s59, s50
	s_cmp_lt_u32 s58, 2
	s_cselect_b32 s59, s51, s59
	s_lshl_b32 s52, s59, 11
	s_add_u32 s46, s16, s52
	s_addc_u32 s47, s17, 0
	s_lshl_b32 s52, s6, 13
	s_add_i32 s52, s52, 0x10000
	s_mov_b32 m0, s52
	s_add_i32 s52, s52, 0x400
	global_load_lds_dwordx4 v211, s[46:47]
	s_mov_b32 m0, s52
	s_add_i32 s52, s52, 0x400
	global_load_lds_dwordx4 v212, s[46:47]
	s_mov_b32 m0, s52
	s_add_i32 s52, s52, 0x400
	global_load_lds_dwordx4 v213, s[46:47]
	s_mov_b32 m0, s52
	s_add_i32 s52, s52, 0x400
	global_load_lds_dwordx4 v214, s[46:47]
	s_mov_b32 m0, s52
	s_add_i32 s52, s52, 0x400
	global_load_lds_dwordx4 v215, s[46:47]
	s_mov_b32 m0, s52
	s_add_i32 s52, s52, 0x400
	global_load_lds_dwordx4 v216, s[46:47]
	s_mov_b32 m0, s52
	s_add_i32 s52, s52, 0x400
	global_load_lds_dwordx4 v217, s[46:47]
	s_mov_b32 m0, s52
	s_nop 0
	global_load_lds_dwordx4 v218, s[46:47]
	s_waitcnt vmcnt(8)
	s_barrier
	s_cmp_eq_u32 s7, 0
	s_cbranch_scc1 .Lmylru_p0_1
	v_mov_b32_e32 v163, v162
	ds_read_b128 v[112:115], v163
	ds_read_b128 v[116:119], v163 offset:8192
	ds_read_b128 v[120:123], v163 offset:16384
	ds_read_b128 v[124:127], v163 offset:24576
	s_waitcnt lgkmcnt(3)
	v_mfma_f32_16x16x32_bf16 v[64:67], v[112:115], v[0:3], 0
	v_mfma_f32_16x16x32_bf16 v[68:71], v[112:115], v[32:35], 0
	v_xor_b32_e32 v164, 0x40, v163
	ds_read_b128 v[112:115], v164
	s_waitcnt lgkmcnt(3)
	v_mfma_f32_16x16x32_bf16 v[72:75], v[116:119], v[0:3], 0
	v_mfma_f32_16x16x32_bf16 v[76:79], v[116:119], v[32:35], 0
	ds_read_b128 v[116:119], v164 offset:8192
	s_waitcnt lgkmcnt(3)
	v_mfma_f32_16x16x32_bf16 v[80:83], v[120:123], v[0:3], 0
	v_mfma_f32_16x16x32_bf16 v[84:87], v[120:123], v[32:35], 0
	ds_read_b128 v[120:123], v164 offset:16384
	s_waitcnt lgkmcnt(3)
	v_mfma_f32_16x16x32_bf16 v[88:91], v[124:127], v[0:3], 0
	v_mfma_f32_16x16x32_bf16 v[92:95], v[124:127], v[32:35], 0
	ds_read_b128 v[124:127], v164 offset:24576
	s_waitcnt lgkmcnt(3)
	v_mfma_f32_16x16x32_bf16 v[64:67], v[112:115], v[4:7], v[64:67]
	v_mfma_f32_16x16x32_bf16 v[68:71], v[112:115], v[36:39], v[68:71]
	v_xor_b32_e32 v164, 0x80, v163
	ds_read_b128 v[112:115], v164
	s_waitcnt lgkmcnt(3)
	v_mfma_f32_16x16x32_bf16 v[72:75], v[116:119], v[4:7], v[72:75]
	v_mfma_f32_16x16x32_bf16 v[76:79], v[116:119], v[36:39], v[76:79]
	ds_read_b128 v[116:119], v164 offset:8192
	s_waitcnt lgkmcnt(3)
	v_mfma_f32_16x16x32_bf16 v[80:83], v[120:123], v[4:7], v[80:83]
	v_mfma_f32_16x16x32_bf16 v[84:87], v[120:123], v[36:39], v[84:87]
	ds_read_b128 v[120:123], v164 offset:16384
	s_waitcnt lgkmcnt(3)
	v_mfma_f32_16x16x32_bf16 v[88:91], v[124:127], v[4:7], v[88:91]
	v_mfma_f32_16x16x32_bf16 v[92:95], v[124:127], v[36:39], v[92:95]
	ds_read_b128 v[124:127], v164 offset:24576
	s_waitcnt lgkmcnt(3)
	v_mfma_f32_16x16x32_bf16 v[64:67], v[112:115], v[8:11], v[64:67]
	v_mfma_f32_16x16x32_bf16 v[68:71], v[112:115], v[40:43], v[68:71]
	v_xor_b32_e32 v164, 0xc0, v163
	ds_read_b128 v[112:115], v164
	s_waitcnt lgkmcnt(3)
	v_mfma_f32_16x16x32_bf16 v[72:75], v[116:119], v[8:11], v[72:75]
	v_mfma_f32_16x16x32_bf16 v[76:79], v[116:119], v[40:43], v[76:79]
	ds_read_b128 v[116:119], v164 offset:8192
	s_waitcnt lgkmcnt(3)
	v_mfma_f32_16x16x32_bf16 v[80:83], v[120:123], v[8:11], v[80:83]
	v_mfma_f32_16x16x32_bf16 v[84:87], v[120:123], v[40:43], v[84:87]
	ds_read_b128 v[120:123], v164 offset:16384
	s_waitcnt lgkmcnt(3)
	v_mfma_f32_16x16x32_bf16 v[88:91], v[124:127], v[8:11], v[88:91]
	v_mfma_f32_16x16x32_bf16 v[92:95], v[124:127], v[40:43], v[92:95]
	ds_read_b128 v[124:127], v164 offset:24576
	s_waitcnt lgkmcnt(3)
	v_mfma_f32_16x16x32_bf16 v[64:67], v[112:115], v[12:15], v[64:67]
	v_mfma_f32_16x16x32_bf16 v[68:71], v[112:115], v[44:47], v[68:71]
	v_xor_b32_e32 v164, 0x100, v163
	ds_read_b128 v[112:115], v164
	s_waitcnt lgkmcnt(3)
	v_mfma_f32_16x16x32_bf16 v[72:75], v[116:119], v[12:15], v[72:75]
	v_mfma_f32_16x16x32_bf16 v[76:79], v[116:119], v[44:47], v[76:79]
	ds_read_b128 v[116:119], v164 offset:8192
	s_waitcnt lgkmcnt(3)
	v_mfma_f32_16x16x32_bf16 v[80:83], v[120:123], v[12:15], v[80:83]
	v_mfma_f32_16x16x32_bf16 v[84:87], v[120:123], v[44:47], v[84:87]
	ds_read_b128 v[120:123], v164 offset:16384
	s_waitcnt lgkmcnt(3)
	v_mfma_f32_16x16x32_bf16 v[88:91], v[124:127], v[12:15], v[88:91]
	v_mfma_f32_16x16x32_bf16 v[92:95], v[124:127], v[44:47], v[92:95]
	ds_read_b128 v[124:127], v164 offset:24576
	s_waitcnt lgkmcnt(3)
	v_mfma_f32_16x16x32_bf16 v[64:67], v[112:115], v[16:19], v[64:67]
	v_mfma_f32_16x16x32_bf16 v[68:71], v[112:115], v[48:51], v[68:71]
	v_xor_b32_e32 v164, 0x140, v163
	ds_read_b128 v[112:115], v164
	s_waitcnt lgkmcnt(3)
	v_mfma_f32_16x16x32_bf16 v[72:75], v[116:119], v[16:19], v[72:75]
	v_mfma_f32_16x16x32_bf16 v[76:79], v[116:119], v[48:51], v[76:79]
	ds_read_b128 v[116:119], v164 offset:8192
	s_waitcnt lgkmcnt(3)
	v_mfma_f32_16x16x32_bf16 v[80:83], v[120:123], v[16:19], v[80:83]
	v_mfma_f32_16x16x32_bf16 v[84:87], v[120:123], v[48:51], v[84:87]
	ds_read_b128 v[120:123], v164 offset:16384
	s_waitcnt lgkmcnt(3)
	v_mfma_f32_16x16x32_bf16 v[88:91], v[124:127], v[16:19], v[88:91]
	v_mfma_f32_16x16x32_bf16 v[92:95], v[124:127], v[48:51], v[92:95]
	ds_read_b128 v[124:127], v164 offset:24576
	s_waitcnt lgkmcnt(3)
	v_mfma_f32_16x16x32_bf16 v[64:67], v[112:115], v[20:23], v[64:67]
	v_mfma_f32_16x16x32_bf16 v[68:71], v[112:115], v[52:55], v[68:71]
	v_xor_b32_e32 v164, 0x180, v163
	ds_read_b128 v[112:115], v164
	s_waitcnt lgkmcnt(3)
	v_mfma_f32_16x16x32_bf16 v[72:75], v[116:119], v[20:23], v[72:75]
	v_mfma_f32_16x16x32_bf16 v[76:79], v[116:119], v[52:55], v[76:79]
	ds_read_b128 v[116:119], v164 offset:8192
	s_waitcnt lgkmcnt(3)
	v_mfma_f32_16x16x32_bf16 v[80:83], v[120:123], v[20:23], v[80:83]
	v_mfma_f32_16x16x32_bf16 v[84:87], v[120:123], v[52:55], v[84:87]
	ds_read_b128 v[120:123], v164 offset:16384
	s_waitcnt lgkmcnt(3)
	v_mfma_f32_16x16x32_bf16 v[88:91], v[124:127], v[20:23], v[88:91]
	v_mfma_f32_16x16x32_bf16 v[92:95], v[124:127], v[52:55], v[92:95]
	ds_read_b128 v[124:127], v164 offset:24576
	s_waitcnt lgkmcnt(3)
	v_mfma_f32_16x16x32_bf16 v[64:67], v[112:115], v[24:27], v[64:67]
	v_mfma_f32_16x16x32_bf16 v[68:71], v[112:115], v[56:59], v[68:71]
	v_xor_b32_e32 v164, 0x1c0, v163
	ds_read_b128 v[112:115], v164
	s_waitcnt lgkmcnt(3)
	v_mfma_f32_16x16x32_bf16 v[72:75], v[116:119], v[24:27], v[72:75]
	v_mfma_f32_16x16x32_bf16 v[76:79], v[116:119], v[56:59], v[76:79]
	ds_read_b128 v[116:119], v164 offset:8192
	s_waitcnt lgkmcnt(3)
	v_mfma_f32_16x16x32_bf16 v[80:83], v[120:123], v[24:27], v[80:83]
	v_mfma_f32_16x16x32_bf16 v[84:87], v[120:123], v[56:59], v[84:87]
	ds_read_b128 v[120:123], v164 offset:16384
	s_waitcnt lgkmcnt(3)
	v_mfma_f32_16x16x32_bf16 v[88:91], v[124:127], v[24:27], v[88:91]
	v_mfma_f32_16x16x32_bf16 v[92:95], v[124:127], v[56:59], v[92:95]
	ds_read_b128 v[124:127], v164 offset:24576
	s_waitcnt lgkmcnt(3)
	v_mfma_f32_16x16x32_bf16 v[64:67], v[112:115], v[28:31], v[64:67]
	v_mfma_f32_16x16x32_bf16 v[68:71], v[112:115], v[60:63], v[68:71]
	s_waitcnt lgkmcnt(2)
	v_mfma_f32_16x16x32_bf16 v[72:75], v[116:119], v[28:31], v[72:75]
	v_mfma_f32_16x16x32_bf16 v[76:79], v[116:119], v[60:63], v[76:79]
	s_waitcnt lgkmcnt(1)
	v_mfma_f32_16x16x32_bf16 v[80:83], v[120:123], v[28:31], v[80:83]
	v_mfma_f32_16x16x32_bf16 v[84:87], v[120:123], v[60:63], v[84:87]
	s_waitcnt lgkmcnt(0)
	v_mfma_f32_16x16x32_bf16 v[88:91], v[124:127], v[28:31], v[88:91]
	v_mfma_f32_16x16x32_bf16 v[92:95], v[124:127], v[60:63], v[92:95]

.Lmylru_nm_5:
	v_mov_b32_e32 v169, v165
	v_mov_b32_e32 v170, v166
	v_mov_b32_e32 v171, v167
	v_mov_b32_e32 v172, v168
	ds_read_u16 v144, v169
	ds_read_u16 v145, v170
	ds_read_u16 v146, v171
	ds_read_u16 v147, v172
	ds_read_u16 v148, v169 offset:8192
	ds_read_u16 v149, v170 offset:8192
	ds_read_u16 v150, v171 offset:8192
	ds_read_u16 v151, v172 offset:8192
	ds_read_u16 v152, v169 offset:16384
	ds_read_u16 v153, v170 offset:16384
	ds_read_u16 v154, v171 offset:16384
	ds_read_u16 v155, v172 offset:16384
	ds_read_u16 v156, v169 offset:24576
	ds_read_u16 v157, v170 offset:24576
	ds_read_u16 v158, v171 offset:24576
	ds_read_u16 v159, v172 offset:24576
	s_nop 7
	v_fma_f32 v178, v64, s53, v173
	v_fma_f32 v179, v65, s53, v173
	v_fma_f32 v180, v66, s53, v173
	v_fma_f32 v181, v67, s53, v173
	v_fma_f32 v182, v72, s53, v173
	v_fma_f32 v183, v73, s53, v173
	v_fma_f32 v184, v74, s53, v173
	v_fma_f32 v185, v75, s53, v173
	v_fma_f32 v186, v68, s53, v174
	v_fma_f32 v187, v69, s53, v174
	v_fma_f32 v188, v70, s53, v174
	v_fma_f32 v189, v71, s53, v174
	v_fma_f32 v190, v76, s53, v174
	v_fma_f32 v191, v77, s53, v174
	v_fma_f32 v192, v78, s53, v174
	v_fma_f32 v193, v79, s53, v174
	v_exp_f32_e32 v178, v178
	v_exp_f32_e32 v179, v179
	v_exp_f32_e32 v180, v180
	v_exp_f32_e32 v181, v181
	v_exp_f32_e32 v182, v182
	v_exp_f32_e32 v183, v183
	v_exp_f32_e32 v184, v184
	v_exp_f32_e32 v185, v185
	v_exp_f32_e32 v186, v186
	v_exp_f32_e32 v187, v187
	v_exp_f32_e32 v188, v188
	v_exp_f32_e32 v189, v189
	v_exp_f32_e32 v190, v190
	v_exp_f32_e32 v191, v191
	v_exp_f32_e32 v192, v192
	v_exp_f32_e32 v193, v193
	v_add_f32_e32 v178, 1.0, v178
	v_add_f32_e32 v179, 1.0, v179
	v_add_f32_e32 v180, 1.0, v180
	v_add_f32_e32 v181, 1.0, v181
	v_add_f32_e32 v182, 1.0, v182
	v_add_f32_e32 v183, 1.0, v183
	v_add_f32_e32 v184, 1.0, v184
	v_add_f32_e32 v185, 1.0, v185
	v_add_f32_e32 v186, 1.0, v186
	v_add_f32_e32 v187, 1.0, v187
	v_add_f32_e32 v188, 1.0, v188
	v_add_f32_e32 v189, 1.0, v189
	v_add_f32_e32 v190, 1.0, v190
	v_add_f32_e32 v191, 1.0, v191
	v_add_f32_e32 v192, 1.0, v192
	v_add_f32_e32 v193, 1.0, v193
	v_rcp_f32_e32 v178, v178
	v_rcp_f32_e32 v179, v179
	v_rcp_f32_e32 v180, v180
	v_rcp_f32_e32 v181, v181
	v_rcp_f32_e32 v182, v182
	v_rcp_f32_e32 v183, v183
	v_rcp_f32_e32 v184, v184
	v_rcp_f32_e32 v185, v185
	v_rcp_f32_e32 v186, v186
	v_rcp_f32_e32 v187, v187
	v_rcp_f32_e32 v188, v188
	v_rcp_f32_e32 v189, v189
	v_rcp_f32_e32 v190, v190
	v_rcp_f32_e32 v191, v191
	v_rcp_f32_e32 v192, v192
	v_rcp_f32_e32 v193, v193
	v_mul_f32_e32 v178, v175, v178
	v_mul_f32_e32 v179, v175, v179
	v_mul_f32_e32 v180, v175, v180
	v_mul_f32_e32 v181, v175, v181
	v_mul_f32_e32 v182, v175, v182
	v_mul_f32_e32 v183, v175, v183
	v_mul_f32_e32 v184, v175, v184
	v_mul_f32_e32 v185, v175, v185
	v_exp_f32_e32 v96, v178
	v_exp_f32_e32 v97, v179
	v_exp_f32_e32 v98, v180
	v_exp_f32_e32 v99, v181
	v_exp_f32_e32 v100, v182
	v_exp_f32_e32 v101, v183
	v_exp_f32_e32 v102, v184
	v_exp_f32_e32 v103, v185
	s_nop 0
	v_fma_f32 v194, -v96, v96, 1.0
	v_fma_f32 v195, -v97, v97, 1.0
	v_fma_f32 v196, -v98, v98, 1.0
	v_fma_f32 v197, -v99, v99, 1.0
	v_fma_f32 v198, -v100, v100, 1.0
	v_fma_f32 v199, -v101, v101, 1.0
	v_fma_f32 v200, -v102, v102, 1.0
	v_fma_f32 v201, -v103, v103, 1.0
	v_max_f32_e32 v194, 0, v194
	v_max_f32_e32 v195, 0, v195
	v_max_f32_e32 v196, 0, v196
	v_max_f32_e32 v197, 0, v197
	v_max_f32_e32 v198, 0, v198
	v_max_f32_e32 v199, 0, v199
	v_max_f32_e32 v200, 0, v200
	v_max_f32_e32 v201, 0, v201
	v_sqrt_f32_e32 v194, v194
	v_sqrt_f32_e32 v195, v195
	v_sqrt_f32_e32 v196, v196
	v_sqrt_f32_e32 v197, v197
	v_sqrt_f32_e32 v198, v198
	v_sqrt_f32_e32 v199, v199
	v_sqrt_f32_e32 v200, v200
	v_sqrt_f32_e32 v201, v201
	s_waitcnt lgkmcnt(8)
	v_lshlrev_b32_e32 v144, 16, v144
	v_lshlrev_b32_e32 v145, 16, v145
	v_lshlrev_b32_e32 v146, 16, v146
	v_lshlrev_b32_e32 v147, 16, v147
	v_lshlrev_b32_e32 v148, 16, v148
	v_lshlrev_b32_e32 v149, 16, v149
	v_lshlrev_b32_e32 v150, 16, v150
	v_lshlrev_b32_e32 v151, 16, v151
	v_mul_f32_e32 v194, v194, v186
	v_mul_f32_e32 v195, v195, v187
	v_mul_f32_e32 v196, v196, v188
	v_mul_f32_e32 v197, v197, v189
	v_mul_f32_e32 v198, v198, v190
	v_mul_f32_e32 v199, v199, v191
	v_mul_f32_e32 v200, v200, v192
	v_mul_f32_e32 v201, v201, v193
	v_mul_f32_e32 v144, v194, v144
	v_mul_f32_e32 v145, v195, v145
	v_mul_f32_e32 v146, v196, v146
	v_mul_f32_e32 v147, v197, v147
	v_mul_f32_e32 v148, v198, v148
	v_mul_f32_e32 v149, v199, v149
	v_mul_f32_e32 v150, v200, v150
	v_mul_f32_e32 v151, v201, v151
	v_fma_f32 v178, v80, s53, v173
	v_fma_f32 v179, v81, s53, v173
	v_fma_f32 v180, v82, s53, v173
	v_fma_f32 v181, v83, s53, v173
	v_fma_f32 v182, v88, s53, v173
	v_fma_f32 v183, v89, s53, v173
	v_fma_f32 v184, v90, s53, v173
	v_fma_f32 v185, v91, s53, v173
	v_fma_f32 v186, v84, s53, v174
	v_fma_f32 v187, v85, s53, v174
	v_fma_f32 v188, v86, s53, v174
	v_fma_f32 v189, v87, s53, v174
	v_fma_f32 v190, v92, s53, v174
	v_fma_f32 v191, v93, s53, v174
	v_fma_f32 v192, v94, s53, v174
	v_fma_f32 v193, v95, s53, v174
	v_exp_f32_e32 v178, v178
	v_exp_f32_e32 v179, v179
	v_exp_f32_e32 v180, v180
	v_exp_f32_e32 v181, v181
	v_exp_f32_e32 v182, v182
	v_exp_f32_e32 v183, v183
	v_exp_f32_e32 v184, v184
	v_exp_f32_e32 v185, v185
	v_exp_f32_e32 v186, v186
	v_exp_f32_e32 v187, v187
	v_exp_f32_e32 v188, v188
	v_exp_f32_e32 v189, v189
	v_exp_f32_e32 v190, v190
	v_exp_f32_e32 v191, v191
	v_exp_f32_e32 v192, v192
	v_exp_f32_e32 v193, v193
	v_add_f32_e32 v178, 1.0, v178
	v_add_f32_e32 v179, 1.0, v179
	v_add_f32_e32 v180, 1.0, v180
	v_add_f32_e32 v181, 1.0, v181
	v_add_f32_e32 v182, 1.0, v182
	v_add_f32_e32 v183, 1.0, v183
	v_add_f32_e32 v184, 1.0, v184
	v_add_f32_e32 v185, 1.0, v185
	v_add_f32_e32 v186, 1.0, v186
	v_add_f32_e32 v187, 1.0, v187
	v_add_f32_e32 v188, 1.0, v188
	v_add_f32_e32 v189, 1.0, v189
	v_add_f32_e32 v190, 1.0, v190
	v_add_f32_e32 v191, 1.0, v191
	v_add_f32_e32 v192, 1.0, v192
	v_add_f32_e32 v193, 1.0, v193
	v_rcp_f32_e32 v178, v178
	v_rcp_f32_e32 v179, v179
	v_rcp_f32_e32 v180, v180
	v_rcp_f32_e32 v181, v181
	v_rcp_f32_e32 v182, v182
	v_rcp_f32_e32 v183, v183
	v_rcp_f32_e32 v184, v184
	v_rcp_f32_e32 v185, v185
	v_rcp_f32_e32 v186, v186
	v_rcp_f32_e32 v187, v187
	v_rcp_f32_e32 v188, v188
	v_rcp_f32_e32 v189, v189
	v_rcp_f32_e32 v190, v190
	v_rcp_f32_e32 v191, v191
	v_rcp_f32_e32 v192, v192
	v_rcp_f32_e32 v193, v193
	v_mul_f32_e32 v178, v175, v178
	v_mul_f32_e32 v179, v175, v179
	v_mul_f32_e32 v180, v175, v180
	v_mul_f32_e32 v181, v175, v181
	v_mul_f32_e32 v182, v175, v182
	v_mul_f32_e32 v183, v175, v183
	v_mul_f32_e32 v184, v175, v184
	v_mul_f32_e32 v185, v175, v185
	v_exp_f32_e32 v104, v178
	v_exp_f32_e32 v105, v179
	v_exp_f32_e32 v106, v180
	v_exp_f32_e32 v107, v181
	v_exp_f32_e32 v108, v182
	v_exp_f32_e32 v109, v183
	v_exp_f32_e32 v110, v184
	v_exp_f32_e32 v111, v185
	s_nop 0
	v_fma_f32 v194, -v104, v104, 1.0
	v_fma_f32 v195, -v105, v105, 1.0
	v_fma_f32 v196, -v106, v106, 1.0
	v_fma_f32 v197, -v107, v107, 1.0
	v_fma_f32 v198, -v108, v108, 1.0
	v_fma_f32 v199, -v109, v109, 1.0
	v_fma_f32 v200, -v110, v110, 1.0
	v_fma_f32 v201, -v111, v111, 1.0
	v_max_f32_e32 v194, 0, v194
	v_max_f32_e32 v195, 0, v195
	v_max_f32_e32 v196, 0, v196
	v_max_f32_e32 v197, 0, v197
	v_max_f32_e32 v198, 0, v198
	v_max_f32_e32 v199, 0, v199
	v_max_f32_e32 v200, 0, v200
	v_max_f32_e32 v201, 0, v201
	v_sqrt_f32_e32 v194, v194
	v_sqrt_f32_e32 v195, v195
	v_sqrt_f32_e32 v196, v196
	v_sqrt_f32_e32 v197, v197
	v_sqrt_f32_e32 v198, v198
	v_sqrt_f32_e32 v199, v199
	v_sqrt_f32_e32 v200, v200
	v_sqrt_f32_e32 v201, v201
	s_waitcnt lgkmcnt(0)
	v_lshlrev_b32_e32 v152, 16, v152
	v_lshlrev_b32_e32 v153, 16, v153
	v_lshlrev_b32_e32 v154, 16, v154
	v_lshlrev_b32_e32 v155, 16, v155
	v_lshlrev_b32_e32 v156, 16, v156
	v_lshlrev_b32_e32 v157, 16, v157
	v_lshlrev_b32_e32 v158, 16, v158
	v_lshlrev_b32_e32 v159, 16, v159
	v_mul_f32_e32 v194, v194, v186
	v_mul_f32_e32 v195, v195, v187
	v_mul_f32_e32 v196, v196, v188
	v_mul_f32_e32 v197, v197, v189
	v_mul_f32_e32 v198, v198, v190
	v_mul_f32_e32 v199, v199, v191
	v_mul_f32_e32 v200, v200, v192
	v_mul_f32_e32 v201, v201, v193
	v_mul_f32_e32 v152, v194, v152
	v_mul_f32_e32 v153, v195, v153
	v_mul_f32_e32 v154, v196, v154
	v_mul_f32_e32 v155, v197, v155
	v_mul_f32_e32 v156, v198, v156
	v_mul_f32_e32 v157, v199, v157
	v_mul_f32_e32 v158, v200, v158
	v_mul_f32_e32 v159, v201, v159
	v_fma_f32 v146, v98, v147, v146
	v_fma_f32 v150, v102, v151, v150
	v_fma_f32 v154, v106, v155, v154
	v_fma_f32 v158, v110, v159, v158
	v_mul_f32_e32 v98, v98, v99
	v_mul_f32_e32 v102, v102, v103
	v_mul_f32_e32 v106, v106, v107
	v_mul_f32_e32 v110, v110, v111
	v_fma_f32 v145, v97, v146, v145
	v_fma_f32 v149, v101, v150, v149
	v_fma_f32 v153, v105, v154, v153
	v_fma_f32 v157, v109, v158, v157
	v_mul_f32_e32 v97, v97, v98
	v_mul_f32_e32 v101, v101, v102
	v_mul_f32_e32 v105, v105, v106
	v_mul_f32_e32 v109, v109, v110
	v_fma_f32 v144, v96, v145, v144
	v_fma_f32 v148, v100, v149, v148
	v_fma_f32 v152, v104, v153, v152
	v_fma_f32 v156, v108, v157, v156
	v_mul_f32_e32 v96, v96, v97
	v_mul_f32_e32 v100, v100, v101
	v_mul_f32_e32 v104, v104, v105
	v_mul_f32_e32 v108, v108, v109
	ds_bpermute_b32 v178, v204, v96
	ds_bpermute_b32 v182, v204, v144
	ds_bpermute_b32 v179, v204, v100
	ds_bpermute_b32 v183, v204, v148
	ds_bpermute_b32 v180, v204, v104
	ds_bpermute_b32 v184, v204, v152
	ds_bpermute_b32 v181, v204, v108
	ds_bpermute_b32 v185, v204, v156
	s_waitcnt lgkmcnt(0)
	v_fma_f32 v186, v182, v96, v144
	v_cndmask_b32_e64 v178, 1.0, v178, s[34:35]
	v_fma_f32 v187, v183, v100, v148
	v_cndmask_b32_e64 v179, 1.0, v179, s[34:35]
	v_fma_f32 v188, v184, v104, v152
	v_cndmask_b32_e64 v180, 1.0, v180, s[34:35]
	v_fma_f32 v189, v185, v108, v156
	v_cndmask_b32_e64 v181, 1.0, v181, s[34:35]
	v_cndmask_b32_e64 v223, v144, v186, s[34:35]
	v_mul_f32_e32 v219, v96, v178
	v_cndmask_b32_e64 v224, v148, v187, s[34:35]
	v_mul_f32_e32 v220, v100, v179
	v_cndmask_b32_e64 v225, v152, v188, s[34:35]
	v_mul_f32_e32 v221, v104, v180
	v_cndmask_b32_e64 v226, v156, v189, s[34:35]
	v_mul_f32_e32 v222, v108, v181
	ds_bpermute_b32 v178, v205, v219
	ds_bpermute_b32 v182, v205, v223
	ds_bpermute_b32 v179, v205, v220
	ds_bpermute_b32 v183, v205, v224
	ds_bpermute_b32 v180, v205, v221
	ds_bpermute_b32 v184, v205, v225
	ds_bpermute_b32 v181, v205, v222
	ds_bpermute_b32 v185, v205, v226
	s_waitcnt lgkmcnt(0)
	v_fma_f32 v186, v182, v219, v223
	v_cndmask_b32_e64 v178, 1.0, v178, s[36:37]
	v_fma_f32 v187, v183, v220, v224
	v_cndmask_b32_e64 v179, 1.0, v179, s[36:37]
	v_fma_f32 v188, v184, v221, v225
	v_cndmask_b32_e64 v180, 1.0, v180, s[36:37]
	v_fma_f32 v189, v185, v222, v226
	v_cndmask_b32_e64 v181, 1.0, v181, s[36:37]
	v_cndmask_b32_e64 v223, v223, v186, s[36:37]
	v_mul_f32_e32 v219, v219, v178
	v_cndmask_b32_e64 v224, v224, v187, s[36:37]
	v_mul_f32_e32 v220, v220, v179
	v_cndmask_b32_e64 v225, v225, v188, s[36:37]
	v_mul_f32_e32 v221, v221, v180
	v_cndmask_b32_e64 v226, v226, v189, s[36:37]
	v_mul_f32_e32 v222, v222, v181
	ds_bpermute_b32 v227, v204, v219
	ds_bpermute_b32 v231, v204, v223
	ds_bpermute_b32 v235, v206, v219
	ds_bpermute_b32 v239, v206, v223
	ds_bpermute_b32 v228, v204, v220
	ds_bpermute_b32 v232, v204, v224
	ds_bpermute_b32 v236, v206, v220
	ds_bpermute_b32 v244, v206, v224
	ds_bpermute_b32 v229, v204, v221
	ds_bpermute_b32 v233, v204, v225
	ds_bpermute_b32 v237, v206, v221
	ds_bpermute_b32 v245, v206, v225
	ds_bpermute_b32 v230, v204, v222
	ds_bpermute_b32 v234, v204, v226
	ds_bpermute_b32 v238, v206, v222
	ds_bpermute_b32 v246, v206, v226
	s_waitcnt lgkmcnt(0)
	v_cndmask_b32_e64 v227, 1.0, v227, s[34:35]
	v_cndmask_b32_e64 v231, 0, v231, s[34:35]
	v_cndmask_b32_e64 v228, 1.0, v228, s[34:35]
	v_cndmask_b32_e64 v232, 0, v232, s[34:35]
	v_cndmask_b32_e64 v229, 1.0, v229, s[34:35]
	v_cndmask_b32_e64 v233, 0, v233, s[34:35]
	v_cndmask_b32_e64 v230, 1.0, v230, s[34:35]
	v_cndmask_b32_e64 v234, 0, v234, s[34:35]
	v_mov_b32_e32 v190, v238
	v_mov_b32_e32 v194, v246
	v_mov_b32_e32 v198, v190
	v_mov_b32_e32 v201, v194
	v_fma_f32 v194, v194, v237, v245
	v_mul_f32_e32 v190, v190, v237
	v_mov_b32_e32 v199, v190
	v_mov_b32_e32 v177, v194
	v_fma_f32 v194, v194, v236, v244
	v_mul_f32_e32 v190, v190, v236
	v_mov_b32_e32 v200, v190
	v_mov_b32_e32 v203, v194
	v_fma_f32 v194, v194, v235, v239
	v_mul_f32_e32 v190, v190, v235
	v_mov_b32_e32 v191, v194
	ds_write_b64 v207, v[190:191]
	s_waitcnt vmcnt(0)
	s_waitcnt lgkmcnt(0)
	s_barrier
	s_cmp_gt_u32 s13, 15
	s_cbranch_scc1 .Lmylru_nodma_5
	s_add_i32 s58, s13, 2
	s_cmp_lt_u32 s58, 2
	s_sub_i32 s50, 1, s58
	s_lshl_b32 s50, s50, 7
	s_lshl_b32 s51, s9, 8
	s_add_i32 s51, s51, 0x8000
	s_add_i32 s51, s51, s50
	s_sub_i32 s50, 17, s58
	s_lshl_b32 s50, s50, 7
	s_lshl_b32 s59, s9, 11
	s_add_i32 s59, s59, s50
	s_cmp_lt_u32 s58, 2
	s_cselect_b32 s59, s51, s59
	s_lshl_b32 s52, s59, 11
	s_add_u32 s46, s16, s52
	s_addc_u32 s47, s17, 0
	s_lshl_b32 s52, s6, 13
	s_mov_b32 m0, s52
	s_add_i32 s52, s52, 0x400
	global_load_lds_dwordx4 v211, s[46:47]
	s_mov_b32 m0, s52
	s_add_i32 s52, s52, 0x400
	global_load_lds_dwordx4 v212, s[46:47]
	s_mov_b32 m0, s52
	s_add_i32 s52, s52, 0x400
	global_load_lds_dwordx4 v213, s[46:47]
	s_mov_b32 m0, s52
	s_add_i32 s52, s52, 0x400
	global_load_lds_dwordx4 v214, s[46:47]
	s_mov_b32 m0, s52
	s_add_i32 s52, s52, 0x400
	global_load_lds_dwordx4 v215, s[46:47]
	s_mov_b32 m0, s52
	s_add_i32 s52, s52, 0x400
	global_load_lds_dwordx4 v216, s[46:47]
	s_mov_b32 m0, s52
	s_add_i32 s52, s52, 0x400
	global_load_lds_dwordx4 v217, s[46:47]
	s_mov_b32 m0, s52
	s_nop 0
	global_load_lds_dwordx4 v218, s[46:47]

.Lmylru_ne_5:
	ds_read_b64 v[178:179], v208 offset:512
	ds_read_b64 v[180:181], v208
	s_waitcnt lgkmcnt(0)
	v_fma_f32 v182, v176, v178, v179
	v_cndmask_b32_e64 v183, v176, v182, s[38:39]
	v_fma_f32 v176, v182, v180, v181
	s_add_i32 s13, s13, 1
	s_cmp_eq_u32 s7, 0
	s_cbranch_scc0 .Lmylru_nm_6
	v_or_b32_e32 v163, 0x10000, v162
	ds_read_b128 v[96:99], v163
	ds_read_b128 v[100:103], v163 offset:8192
	ds_read_b128 v[104:107], v163 offset:16384
	ds_read_b128 v[108:111], v163 offset:24576
	v_xor_b32_e32 v164, 0x40, v163
	ds_read_b128 v[112:115], v164
	ds_read_b128 v[116:119], v164 offset:8192
	ds_read_b128 v[120:123], v164 offset:16384
	ds_read_b128 v[124:127], v164 offset:24576
	s_waitcnt lgkmcnt(7)
	v_mfma_f32_16x16x32_bf16 v[64:67], v[96:99], v[0:3], 0
	v_mfma_f32_16x16x32_bf16 v[68:71], v[96:99], v[32:35], 0
	v_xor_b32_e32 v164, 0x80, v163
	ds_read_b128 v[96:99], v164
	s_waitcnt lgkmcnt(7)
	v_mfma_f32_16x16x32_bf16 v[72:75], v[100:103], v[0:3], 0
	v_mfma_f32_16x16x32_bf16 v[76:79], v[100:103], v[32:35], 0
	ds_read_b128 v[100:103], v164 offset:8192
	s_waitcnt lgkmcnt(7)
	v_mfma_f32_16x16x32_bf16 v[80:83], v[104:107], v[0:3], 0
	v_mfma_f32_16x16x32_bf16 v[84:87], v[104:107], v[32:35], 0
	ds_read_b128 v[104:107], v164 offset:16384
	s_waitcnt lgkmcnt(7)
	v_mfma_f32_16x16x32_bf16 v[88:91], v[108:111], v[0:3], 0
	v_mfma_f32_16x16x32_bf16 v[92:95], v[108:111], v[32:35], 0
	ds_read_b128 v[108:111], v164 offset:24576
	s_waitcnt lgkmcnt(7)
	v_mfma_f32_16x16x32_bf16 v[64:67], v[112:115], v[4:7], v[64:67]
	v_mfma_f32_16x16x32_bf16 v[68:71], v[112:115], v[36:39], v[68:71]
	v_xor_b32_e32 v164, 0xc0, v163
	ds_read_b128 v[112:115], v164
	s_waitcnt lgkmcnt(7)
	v_mfma_f32_16x16x32_bf16 v[72:75], v[116:119], v[4:7], v[72:75]
	v_mfma_f32_16x16x32_bf16 v[76:79], v[116:119], v[36:39], v[76:79]
	ds_read_b128 v[116:119], v164 offset:8192
	s_waitcnt lgkmcnt(7)
	v_mfma_f32_16x16x32_bf16 v[80:83], v[120:123], v[4:7], v[80:83]
	v_mfma_f32_16x16x32_bf16 v[84:87], v[120:123], v[36:39], v[84:87]
	ds_read_b128 v[120:123], v164 offset:16384
	s_waitcnt lgkmcnt(7)
	v_mfma_f32_16x16x32_bf16 v[88:91], v[124:127], v[4:7], v[88:91]
	v_mfma_f32_16x16x32_bf16 v[92:95], v[124:127], v[36:39], v[92:95]
	ds_read_b128 v[124:127], v164 offset:24576
	s_waitcnt lgkmcnt(7)
	v_mfma_f32_16x16x32_bf16 v[64:67], v[96:99], v[8:11], v[64:67]
	v_mfma_f32_16x16x32_bf16 v[68:71], v[96:99], v[40:43], v[68:71]
	v_xor_b32_e32 v164, 0x100, v163
	ds_read_b128 v[96:99], v164
	s_waitcnt lgkmcnt(7)
	v_mfma_f32_16x16x32_bf16 v[72:75], v[100:103], v[8:11], v[72:75]
	v_mfma_f32_16x16x32_bf16 v[76:79], v[100:103], v[40:43], v[76:79]
	ds_read_b128 v[100:103], v164 offset:8192
	s_waitcnt lgkmcnt(7)
	v_mfma_f32_16x16x32_bf16 v[80:83], v[104:107], v[8:11], v[80:83]
	v_mfma_f32_16x16x32_bf16 v[84:87], v[104:107], v[40:43], v[84:87]
	ds_read_b128 v[104:107], v164 offset:16384
	s_waitcnt lgkmcnt(7)
	v_mfma_f32_16x16x32_bf16 v[88:91], v[108:111], v[8:11], v[88:91]
	v_mfma_f32_16x16x32_bf16 v[92:95], v[108:111], v[40:43], v[92:95]
	ds_read_b128 v[108:111], v164 offset:24576
	s_waitcnt lgkmcnt(7)
	v_mfma_f32_16x16x32_bf16 v[64:67], v[112:115], v[12:15], v[64:67]
	v_mfma_f32_16x16x32_bf16 v[68:71], v[112:115], v[44:47], v[68:71]
	v_xor_b32_e32 v164, 0x140, v163
	ds_read_b128 v[112:115], v164
	s_waitcnt lgkmcnt(7)
	v_mfma_f32_16x16x32_bf16 v[72:75], v[116:119], v[12:15], v[72:75]
	v_mfma_f32_16x16x32_bf16 v[76:79], v[116:119], v[44:47], v[76:79]
	ds_read_b128 v[116:119], v164 offset:8192
	s_waitcnt lgkmcnt(7)
	v_mfma_f32_16x16x32_bf16 v[80:83], v[120:123], v[12:15], v[80:83]
	v_mfma_f32_16x16x32_bf16 v[84:87], v[120:123], v[44:47], v[84:87]
	ds_read_b128 v[120:123], v164 offset:16384
	s_waitcnt lgkmcnt(7)
	v_mfma_f32_16x16x32_bf16 v[88:91], v[124:127], v[12:15], v[88:91]
	v_mfma_f32_16x16x32_bf16 v[92:95], v[124:127], v[44:47], v[92:95]
	ds_read_b128 v[124:127], v164 offset:24576
	s_waitcnt lgkmcnt(7)
	v_mfma_f32_16x16x32_bf16 v[64:67], v[96:99], v[16:19], v[64:67]
	v_mfma_f32_16x16x32_bf16 v[68:71], v[96:99], v[48:51], v[68:71]
	v_xor_b32_e32 v164, 0x180, v163
	ds_read_b128 v[96:99], v164
	s_waitcnt lgkmcnt(7)
	v_mfma_f32_16x16x32_bf16 v[72:75], v[100:103], v[16:19], v[72:75]
	v_mfma_f32_16x16x32_bf16 v[76:79], v[100:103], v[48:51], v[76:79]
	ds_read_b128 v[100:103], v164 offset:8192
	s_waitcnt lgkmcnt(7)
	v_mfma_f32_16x16x32_bf16 v[80:83], v[104:107], v[16:19], v[80:83]
	v_mfma_f32_16x16x32_bf16 v[84:87], v[104:107], v[48:51], v[84:87]
	ds_read_b128 v[104:107], v164 offset:16384
	s_waitcnt lgkmcnt(7)
	v_mfma_f32_16x16x32_bf16 v[88:91], v[108:111], v[16:19], v[88:91]
	v_mfma_f32_16x16x32_bf16 v[92:95], v[108:111], v[48:51], v[92:95]
	ds_read_b128 v[108:111], v164 offset:24576
	s_waitcnt lgkmcnt(7)
	v_mfma_f32_16x16x32_bf16 v[64:67], v[112:115], v[20:23], v[64:67]
	v_mfma_f32_16x16x32_bf16 v[68:71], v[112:115], v[52:55], v[68:71]
	v_xor_b32_e32 v164, 0x1c0, v163
	ds_read_b128 v[112:115], v164
	s_waitcnt lgkmcnt(7)
	v_mfma_f32_16x16x32_bf16 v[72:75], v[116:119], v[20:23], v[72:75]
	v_mfma_f32_16x16x32_bf16 v[76:79], v[116:119], v[52:55], v[76:79]
	ds_read_b128 v[116:119], v164 offset:8192
	s_waitcnt lgkmcnt(7)
	v_mfma_f32_16x16x32_bf16 v[80:83], v[120:123], v[20:23], v[80:83]
	v_mfma_f32_16x16x32_bf16 v[84:87], v[120:123], v[52:55], v[84:87]
	ds_read_b128 v[120:123], v164 offset:16384
	s_waitcnt lgkmcnt(7)
	v_mfma_f32_16x16x32_bf16 v[88:91], v[124:127], v[20:23], v[88:91]
	v_mfma_f32_16x16x32_bf16 v[92:95], v[124:127], v[52:55], v[92:95]
	ds_read_b128 v[124:127], v164 offset:24576
	s_waitcnt lgkmcnt(7)
	v_mfma_f32_16x16x32_bf16 v[64:67], v[96:99], v[24:27], v[64:67]
	v_mfma_f32_16x16x32_bf16 v[68:71], v[96:99], v[56:59], v[68:71]
	s_waitcnt lgkmcnt(6)
	v_mfma_f32_16x16x32_bf16 v[72:75], v[100:103], v[24:27], v[72:75]
	v_mfma_f32_16x16x32_bf16 v[76:79], v[100:103], v[56:59], v[76:79]
	s_waitcnt lgkmcnt(5)
	v_mfma_f32_16x16x32_bf16 v[80:83], v[104:107], v[24:27], v[80:83]
	v_mfma_f32_16x16x32_bf16 v[84:87], v[104:107], v[56:59], v[84:87]
	s_waitcnt lgkmcnt(4)
	v_mfma_f32_16x16x32_bf16 v[88:91], v[108:111], v[24:27], v[88:91]
	v_mfma_f32_16x16x32_bf16 v[92:95], v[108:111], v[56:59], v[92:95]
	s_waitcnt lgkmcnt(3)
	v_mfma_f32_16x16x32_bf16 v[64:67], v[112:115], v[28:31], v[64:67]
	v_mfma_f32_16x16x32_bf16 v[68:71], v[112:115], v[60:63], v[68:71]
	s_waitcnt lgkmcnt(2)
	v_mfma_f32_16x16x32_bf16 v[72:75], v[116:119], v[28:31], v[72:75]
	v_mfma_f32_16x16x32_bf16 v[76:79], v[116:119], v[60:63], v[76:79]
	s_waitcnt lgkmcnt(1)
	v_mfma_f32_16x16x32_bf16 v[80:83], v[120:123], v[28:31], v[80:83]
	v_mfma_f32_16x16x32_bf16 v[84:87], v[120:123], v[60:63], v[84:87]
	s_waitcnt lgkmcnt(0)
	v_mfma_f32_16x16x32_bf16 v[88:91], v[124:127], v[28:31], v[88:91]
	v_mfma_f32_16x16x32_bf16 v[92:95], v[124:127], v[60:63], v[92:95]
.Lmylru_nm_6:
	v_or_b32_e32 v169, 0x10000, v165
	v_or_b32_e32 v170, 0x10000, v166
	v_or_b32_e32 v171, 0x10000, v167
	v_or_b32_e32 v172, 0x10000, v168
	ds_read_u16 v144, v169
	ds_read_u16 v145, v170
	ds_read_u16 v146, v171
	ds_read_u16 v147, v172
	ds_read_u16 v148, v169 offset:8192
	ds_read_u16 v149, v170 offset:8192
	ds_read_u16 v150, v171 offset:8192
	ds_read_u16 v151, v172 offset:8192
	ds_read_u16 v152, v169 offset:16384
	ds_read_u16 v153, v170 offset:16384
	ds_read_u16 v154, v171 offset:16384
	ds_read_u16 v155, v172 offset:16384
	ds_read_u16 v156, v169 offset:24576
	ds_read_u16 v157, v170 offset:24576
	ds_read_u16 v158, v171 offset:24576
	ds_read_u16 v159, v172 offset:24576
	s_nop 7
	v_fma_f32 v178, v64, s53, v173
	v_fma_f32 v179, v65, s53, v173
	v_fma_f32 v180, v66, s53, v173
	v_fma_f32 v181, v67, s53, v173
	v_fma_f32 v182, v72, s53, v173
	v_fma_f32 v183, v73, s53, v173
	v_fma_f32 v184, v74, s53, v173
	v_fma_f32 v185, v75, s53, v173
	v_fma_f32 v186, v68, s53, v174
	v_fma_f32 v187, v69, s53, v174
	v_fma_f32 v188, v70, s53, v174
	v_fma_f32 v189, v71, s53, v174
	v_fma_f32 v190, v76, s53, v174
	v_fma_f32 v191, v77, s53, v174
	v_fma_f32 v192, v78, s53, v174
	v_fma_f32 v193, v79, s53, v174
	v_exp_f32_e32 v178, v178
	v_exp_f32_e32 v179, v179
	v_exp_f32_e32 v180, v180
	v_exp_f32_e32 v181, v181
	v_exp_f32_e32 v182, v182
	v_exp_f32_e32 v183, v183
	v_exp_f32_e32 v184, v184
	v_exp_f32_e32 v185, v185
	v_exp_f32_e32 v186, v186
	v_exp_f32_e32 v187, v187
	v_exp_f32_e32 v188, v188
	v_exp_f32_e32 v189, v189
	v_exp_f32_e32 v190, v190
	v_exp_f32_e32 v191, v191
	v_exp_f32_e32 v192, v192
	v_exp_f32_e32 v193, v193
	v_add_f32_e32 v178, 1.0, v178
	v_add_f32_e32 v179, 1.0, v179
	v_add_f32_e32 v180, 1.0, v180
	v_add_f32_e32 v181, 1.0, v181
	v_add_f32_e32 v182, 1.0, v182
	v_add_f32_e32 v183, 1.0, v183
	v_add_f32_e32 v184, 1.0, v184
	v_add_f32_e32 v185, 1.0, v185
	v_add_f32_e32 v186, 1.0, v186
	v_add_f32_e32 v187, 1.0, v187
	v_add_f32_e32 v188, 1.0, v188
	v_add_f32_e32 v189, 1.0, v189
	v_add_f32_e32 v190, 1.0, v190
	v_add_f32_e32 v191, 1.0, v191
	v_add_f32_e32 v192, 1.0, v192
	v_add_f32_e32 v193, 1.0, v193
	v_rcp_f32_e32 v178, v178
	v_rcp_f32_e32 v179, v179
	v_rcp_f32_e32 v180, v180
	v_rcp_f32_e32 v181, v181
	v_rcp_f32_e32 v182, v182
	v_rcp_f32_e32 v183, v183
	v_rcp_f32_e32 v184, v184
	v_rcp_f32_e32 v185, v185
	v_rcp_f32_e32 v186, v186
	v_rcp_f32_e32 v187, v187
	v_rcp_f32_e32 v188, v188
	v_rcp_f32_e32 v189, v189
	v_rcp_f32_e32 v190, v190
	v_rcp_f32_e32 v191, v191
	v_rcp_f32_e32 v192, v192
	v_rcp_f32_e32 v193, v193
	v_mul_f32_e32 v178, v175, v178
	v_mul_f32_e32 v179, v175, v179
	v_mul_f32_e32 v180, v175, v180
	v_mul_f32_e32 v181, v175, v181
	v_mul_f32_e32 v182, v175, v182
	v_mul_f32_e32 v183, v175, v183
	v_mul_f32_e32 v184, v175, v184
	v_mul_f32_e32 v185, v175, v185
	v_exp_f32_e32 v96, v178
	v_exp_f32_e32 v97, v179
	v_exp_f32_e32 v98, v180
	v_exp_f32_e32 v99, v181
	v_exp_f32_e32 v100, v182
	v_exp_f32_e32 v101, v183
	v_exp_f32_e32 v102, v184
	v_exp_f32_e32 v103, v185
	s_nop 0
	v_fma_f32 v194, -v96, v96, 1.0
	v_fma_f32 v195, -v97, v97, 1.0
	v_fma_f32 v196, -v98, v98, 1.0
	v_fma_f32 v197, -v99, v99, 1.0
	v_fma_f32 v198, -v100, v100, 1.0
	v_fma_f32 v199, -v101, v101, 1.0
	v_fma_f32 v200, -v102, v102, 1.0
	v_fma_f32 v201, -v103, v103, 1.0
	v_max_f32_e32 v194, 0, v194
	v_max_f32_e32 v195, 0, v195
	v_max_f32_e32 v196, 0, v196
	v_max_f32_e32 v197, 0, v197
	v_max_f32_e32 v198, 0, v198
	v_max_f32_e32 v199, 0, v199
	v_max_f32_e32 v200, 0, v200
	v_max_f32_e32 v201, 0, v201
	v_sqrt_f32_e32 v194, v194
	v_sqrt_f32_e32 v195, v195
	v_sqrt_f32_e32 v196, v196
	v_sqrt_f32_e32 v197, v197
	v_sqrt_f32_e32 v198, v198
	v_sqrt_f32_e32 v199, v199
	v_sqrt_f32_e32 v200, v200
	v_sqrt_f32_e32 v201, v201
	s_waitcnt lgkmcnt(8)
	v_lshlrev_b32_e32 v144, 16, v144
	v_lshlrev_b32_e32 v145, 16, v145
	v_lshlrev_b32_e32 v146, 16, v146
	v_lshlrev_b32_e32 v147, 16, v147
	v_lshlrev_b32_e32 v148, 16, v148
	v_lshlrev_b32_e32 v149, 16, v149
	v_lshlrev_b32_e32 v150, 16, v150
	v_lshlrev_b32_e32 v151, 16, v151
	v_mul_f32_e32 v194, v194, v186
	v_mul_f32_e32 v195, v195, v187
	v_mul_f32_e32 v196, v196, v188
	v_mul_f32_e32 v197, v197, v189
	v_mul_f32_e32 v198, v198, v190
	v_mul_f32_e32 v199, v199, v191
	v_mul_f32_e32 v200, v200, v192
	v_mul_f32_e32 v201, v201, v193
	v_mul_f32_e32 v144, v194, v144
	v_mul_f32_e32 v145, v195, v145
	v_mul_f32_e32 v146, v196, v146
	v_mul_f32_e32 v147, v197, v147
	v_mul_f32_e32 v148, v198, v148
	v_mul_f32_e32 v149, v199, v149
	v_mul_f32_e32 v150, v200, v150
	v_mul_f32_e32 v151, v201, v151
	v_fma_f32 v178, v80, s53, v173
	v_fma_f32 v179, v81, s53, v173
	v_fma_f32 v180, v82, s53, v173
	v_fma_f32 v181, v83, s53, v173
	v_fma_f32 v182, v88, s53, v173
	v_fma_f32 v183, v89, s53, v173
	v_fma_f32 v184, v90, s53, v173
	v_fma_f32 v185, v91, s53, v173
	v_fma_f32 v186, v84, s53, v174
	v_fma_f32 v187, v85, s53, v174
	v_fma_f32 v188, v86, s53, v174
	v_fma_f32 v189, v87, s53, v174
	v_fma_f32 v190, v92, s53, v174
	v_fma_f32 v191, v93, s53, v174
	v_fma_f32 v192, v94, s53, v174
	v_fma_f32 v193, v95, s53, v174
	v_exp_f32_e32 v178, v178
	v_exp_f32_e32 v179, v179
	v_exp_f32_e32 v180, v180
	v_exp_f32_e32 v181, v181
	v_exp_f32_e32 v182, v182
	v_exp_f32_e32 v183, v183
	v_exp_f32_e32 v184, v184
	v_exp_f32_e32 v185, v185
	v_exp_f32_e32 v186, v186
	v_exp_f32_e32 v187, v187
	v_exp_f32_e32 v188, v188
	v_exp_f32_e32 v189, v189
	v_exp_f32_e32 v190, v190
	v_exp_f32_e32 v191, v191
	v_exp_f32_e32 v192, v192
	v_exp_f32_e32 v193, v193
	v_add_f32_e32 v178, 1.0, v178
	v_add_f32_e32 v179, 1.0, v179
	v_add_f32_e32 v180, 1.0, v180
	v_add_f32_e32 v181, 1.0, v181
	v_add_f32_e32 v182, 1.0, v182
	v_add_f32_e32 v183, 1.0, v183
	v_add_f32_e32 v184, 1.0, v184
	v_add_f32_e32 v185, 1.0, v185
	v_add_f32_e32 v186, 1.0, v186
	v_add_f32_e32 v187, 1.0, v187
	v_add_f32_e32 v188, 1.0, v188
	v_add_f32_e32 v189, 1.0, v189
	v_add_f32_e32 v190, 1.0, v190
	v_add_f32_e32 v191, 1.0, v191
	v_add_f32_e32 v192, 1.0, v192
	v_add_f32_e32 v193, 1.0, v193
	v_rcp_f32_e32 v178, v178
	v_rcp_f32_e32 v179, v179
	v_rcp_f32_e32 v180, v180
	v_rcp_f32_e32 v181, v181
	v_rcp_f32_e32 v182, v182
	v_rcp_f32_e32 v183, v183
	v_rcp_f32_e32 v184, v184
	v_rcp_f32_e32 v185, v185
	v_rcp_f32_e32 v186, v186
	v_rcp_f32_e32 v187, v187
	v_rcp_f32_e32 v188, v188
	v_rcp_f32_e32 v189, v189
	v_rcp_f32_e32 v190, v190
	v_rcp_f32_e32 v191, v191
	v_rcp_f32_e32 v192, v192
	v_rcp_f32_e32 v193, v193
	v_mul_f32_e32 v178, v175, v178
	v_mul_f32_e32 v179, v175, v179
	v_mul_f32_e32 v180, v175, v180
	v_mul_f32_e32 v181, v175, v181
	v_mul_f32_e32 v182, v175, v182
	v_mul_f32_e32 v183, v175, v183
	v_mul_f32_e32 v184, v175, v184
	v_mul_f32_e32 v185, v175, v185
	v_exp_f32_e32 v104, v178
	v_exp_f32_e32 v105, v179
	v_exp_f32_e32 v106, v180
	v_exp_f32_e32 v107, v181
	v_exp_f32_e32 v108, v182
	v_exp_f32_e32 v109, v183
	v_exp_f32_e32 v110, v184
	v_exp_f32_e32 v111, v185
	s_nop 0
	v_fma_f32 v194, -v104, v104, 1.0
	v_fma_f32 v195, -v105, v105, 1.0
	v_fma_f32 v196, -v106, v106, 1.0
	v_fma_f32 v197, -v107, v107, 1.0
	v_fma_f32 v198, -v108, v108, 1.0
	v_fma_f32 v199, -v109, v109, 1.0
	v_fma_f32 v200, -v110, v110, 1.0
	v_fma_f32 v201, -v111, v111, 1.0
	v_max_f32_e32 v194, 0, v194
	v_max_f32_e32 v195, 0, v195
	v_max_f32_e32 v196, 0, v196
	v_max_f32_e32 v197, 0, v197
	v_max_f32_e32 v198, 0, v198
	v_max_f32_e32 v199, 0, v199
	v_max_f32_e32 v200, 0, v200
	v_max_f32_e32 v201, 0, v201
	v_sqrt_f32_e32 v194, v194
	v_sqrt_f32_e32 v195, v195
	v_sqrt_f32_e32 v196, v196
	v_sqrt_f32_e32 v197, v197
	v_sqrt_f32_e32 v198, v198
	v_sqrt_f32_e32 v199, v199
	v_sqrt_f32_e32 v200, v200
	v_sqrt_f32_e32 v201, v201
	s_waitcnt lgkmcnt(0)
	v_lshlrev_b32_e32 v152, 16, v152
	v_lshlrev_b32_e32 v153, 16, v153
	v_lshlrev_b32_e32 v154, 16, v154
	v_lshlrev_b32_e32 v155, 16, v155
	v_lshlrev_b32_e32 v156, 16, v156
	v_lshlrev_b32_e32 v157, 16, v157
	v_lshlrev_b32_e32 v158, 16, v158
	v_lshlrev_b32_e32 v159, 16, v159
	v_mul_f32_e32 v194, v194, v186
	v_mul_f32_e32 v195, v195, v187
	v_mul_f32_e32 v196, v196, v188
	v_mul_f32_e32 v197, v197, v189
	v_mul_f32_e32 v198, v198, v190
	v_mul_f32_e32 v199, v199, v191
	v_mul_f32_e32 v200, v200, v192
	v_mul_f32_e32 v201, v201, v193
	v_mul_f32_e32 v152, v194, v152
	v_mul_f32_e32 v153, v195, v153
	v_mul_f32_e32 v154, v196, v154
	v_mul_f32_e32 v155, v197, v155
	v_mul_f32_e32 v156, v198, v156
	v_mul_f32_e32 v157, v199, v157
	v_mul_f32_e32 v158, v200, v158
	v_mul_f32_e32 v159, v201, v159
	v_fma_f32 v146, v98, v147, v146
	v_fma_f32 v150, v102, v151, v150
	v_fma_f32 v154, v106, v155, v154
	v_fma_f32 v158, v110, v159, v158
	v_mul_f32_e32 v98, v98, v99
	v_mul_f32_e32 v102, v102, v103
	v_mul_f32_e32 v106, v106, v107
	v_mul_f32_e32 v110, v110, v111
	v_fma_f32 v145, v97, v146, v145
	v_fma_f32 v149, v101, v150, v149
	v_fma_f32 v153, v105, v154, v153
	v_fma_f32 v157, v109, v158, v157
	v_mul_f32_e32 v97, v97, v98
	v_mul_f32_e32 v101, v101, v102
	v_mul_f32_e32 v105, v105, v106
	v_mul_f32_e32 v109, v109, v110
	v_fma_f32 v144, v96, v145, v144
	v_fma_f32 v148, v100, v149, v148
	v_fma_f32 v152, v104, v153, v152
	v_fma_f32 v156, v108, v157, v156
	v_mul_f32_e32 v96, v96, v97
	v_mul_f32_e32 v100, v100, v101
	v_mul_f32_e32 v104, v104, v105
	v_mul_f32_e32 v108, v108, v109
	ds_bpermute_b32 v178, v204, v96
	ds_bpermute_b32 v182, v204, v144
	ds_bpermute_b32 v179, v204, v100
	ds_bpermute_b32 v183, v204, v148
	ds_bpermute_b32 v180, v204, v104
	ds_bpermute_b32 v184, v204, v152
	ds_bpermute_b32 v181, v204, v108
	ds_bpermute_b32 v185, v204, v156
	s_waitcnt lgkmcnt(0)
	v_fma_f32 v186, v182, v96, v144
	v_cndmask_b32_e64 v178, 1.0, v178, s[34:35]
	v_fma_f32 v187, v183, v100, v148
	v_cndmask_b32_e64 v179, 1.0, v179, s[34:35]
	v_fma_f32 v188, v184, v104, v152
	v_cndmask_b32_e64 v180, 1.0, v180, s[34:35]
	v_fma_f32 v189, v185, v108, v156
	v_cndmask_b32_e64 v181, 1.0, v181, s[34:35]
	v_cndmask_b32_e64 v223, v144, v186, s[34:35]
	v_mul_f32_e32 v219, v96, v178
	v_cndmask_b32_e64 v224, v148, v187, s[34:35]
	v_mul_f32_e32 v220, v100, v179
	v_cndmask_b32_e64 v225, v152, v188, s[34:35]
	v_mul_f32_e32 v221, v104, v180
	v_cndmask_b32_e64 v226, v156, v189, s[34:35]
	v_mul_f32_e32 v222, v108, v181
	ds_bpermute_b32 v178, v205, v219
	ds_bpermute_b32 v182, v205, v223
	ds_bpermute_b32 v179, v205, v220
	ds_bpermute_b32 v183, v205, v224
	ds_bpermute_b32 v180, v205, v221
	ds_bpermute_b32 v184, v205, v225
	ds_bpermute_b32 v181, v205, v222
	ds_bpermute_b32 v185, v205, v226
	s_waitcnt lgkmcnt(0)
	v_fma_f32 v186, v182, v219, v223
	v_cndmask_b32_e64 v178, 1.0, v178, s[36:37]
	v_fma_f32 v187, v183, v220, v224
	v_cndmask_b32_e64 v179, 1.0, v179, s[36:37]
	v_fma_f32 v188, v184, v221, v225
	v_cndmask_b32_e64 v180, 1.0, v180, s[36:37]
	v_fma_f32 v189, v185, v222, v226
	v_cndmask_b32_e64 v181, 1.0, v181, s[36:37]
	v_cndmask_b32_e64 v223, v223, v186, s[36:37]
	v_mul_f32_e32 v219, v219, v178
	v_cndmask_b32_e64 v224, v224, v187, s[36:37]
	v_mul_f32_e32 v220, v220, v179
	v_cndmask_b32_e64 v225, v225, v188, s[36:37]
	v_mul_f32_e32 v221, v221, v180
	v_cndmask_b32_e64 v226, v226, v189, s[36:37]
	v_mul_f32_e32 v222, v222, v181
	ds_bpermute_b32 v227, v204, v219
	ds_bpermute_b32 v231, v204, v223
	ds_bpermute_b32 v235, v206, v219
	ds_bpermute_b32 v239, v206, v223
	ds_bpermute_b32 v228, v204, v220
	ds_bpermute_b32 v232, v204, v224
	ds_bpermute_b32 v236, v206, v220
	ds_bpermute_b32 v244, v206, v224
	ds_bpermute_b32 v229, v204, v221
	ds_bpermute_b32 v233, v204, v225
	ds_bpermute_b32 v237, v206, v221
	ds_bpermute_b32 v245, v206, v225
	ds_bpermute_b32 v230, v204, v222
	ds_bpermute_b32 v234, v204, v226
	ds_bpermute_b32 v238, v206, v222
	ds_bpermute_b32 v246, v206, v226
	s_waitcnt lgkmcnt(0)
	v_cndmask_b32_e64 v227, 1.0, v227, s[34:35]
	v_cndmask_b32_e64 v231, 0, v231, s[34:35]
	v_cndmask_b32_e64 v228, 1.0, v228, s[34:35]
	v_cndmask_b32_e64 v232, 0, v232, s[34:35]
	v_cndmask_b32_e64 v229, 1.0, v229, s[34:35]
	v_cndmask_b32_e64 v233, 0, v233, s[34:35]
	v_cndmask_b32_e64 v230, 1.0, v230, s[34:35]
	v_cndmask_b32_e64 v234, 0, v234, s[34:35]
	v_mov_b32_e32 v190, v238
	v_mov_b32_e32 v194, v246
	v_mov_b32_e32 v198, v190
	v_mov_b32_e32 v201, v194
	v_fma_f32 v194, v194, v237, v245
	v_mul_f32_e32 v190, v190, v237
	v_mov_b32_e32 v199, v190
	v_mov_b32_e32 v177, v194
	v_fma_f32 v194, v194, v236, v244
	v_mul_f32_e32 v190, v190, v236
	v_mov_b32_e32 v200, v190
	v_mov_b32_e32 v203, v194
	v_fma_f32 v194, v194, v235, v239
	v_mul_f32_e32 v190, v190, v235
	v_mov_b32_e32 v191, v194
	ds_write_b64 v207, v[190:191] offset:1024
	s_waitcnt vmcnt(0)
	s_waitcnt lgkmcnt(0)
	s_barrier
	s_cmp_gt_u32 s13, 15
	s_cbranch_scc1 .Lmylru_nodma_6
	s_add_i32 s58, s13, 2
	s_cmp_lt_u32 s58, 2
	s_sub_i32 s50, 1, s58
	s_lshl_b32 s50, s50, 7
	s_lshl_b32 s51, s9, 8
	s_add_i32 s51, s51, 0x8000
	s_add_i32 s51, s51, s50
	s_sub_i32 s50, 17, s58
	s_lshl_b32 s50, s50, 7
	s_lshl_b32 s59, s9, 11
	s_add_i32 s59, s59, s50
	s_cmp_lt_u32 s58, 2
	s_cselect_b32 s59, s51, s59
	s_lshl_b32 s52, s59, 11
	s_add_u32 s46, s16, s52
	s_addc_u32 s47, s17, 0
	s_lshl_b32 s52, s6, 13
	s_add_i32 s52, s52, 0x10000
	s_mov_b32 m0, s52
	s_add_i32 s52, s52, 0x400
	global_load_lds_dwordx4 v211, s[46:47]
	s_mov_b32 m0, s52
	s_add_i32 s52, s52, 0x400
	global_load_lds_dwordx4 v212, s[46:47]
	s_mov_b32 m0, s52
	s_add_i32 s52, s52, 0x400
	global_load_lds_dwordx4 v213, s[46:47]
	s_mov_b32 m0, s52
	s_add_i32 s52, s52, 0x400
	global_load_lds_dwordx4 v214, s[46:47]
	s_mov_b32 m0, s52
	s_add_i32 s52, s52, 0x400
	global_load_lds_dwordx4 v215, s[46:47]
	s_mov_b32 m0, s52
	s_add_i32 s52, s52, 0x400
	global_load_lds_dwordx4 v216, s[46:47]
	s_mov_b32 m0, s52
	s_add_i32 s52, s52, 0x400
	global_load_lds_dwordx4 v217, s[46:47]
	s_mov_b32 m0, s52
	s_nop 0
	global_load_lds_dwordx4 v218, s[46:47]

.Lmylru_loop_1:
	s_sub_i32 s54, 17, s13
	s_lshl_b32 s55, s54, 14
	s_lshl_b32 s56, s6, 11
	s_add_i32 s55, s55, s56
	s_add_u32 s44, s22, s55
	s_addc_u32 s45, s23, 0
	s_cmp_lt_u32 s13, 2
	s_sub_i32 s50, 1, s13
	s_lshl_b32 s50, s50, 7
	s_lshl_b32 s51, s9, 8
	s_add_i32 s51, s51, 0x8000
	s_add_i32 s51, s51, s50
	s_sub_i32 s50, 17, s13
	s_lshl_b32 s50, s50, 7
	s_lshl_b32 s57, s9, 11
	s_add_i32 s57, s57, s50
	s_cmp_lt_u32 s13, 2
	s_cselect_b32 s57, s51, s57
	s_lshl_b32 s57, s57, 11
	s_add_u32 s40, s18, s57
	s_addc_u32 s41, s19, 0
	s_add_u32 s42, s20, s57
	s_addc_u32 s43, s21, 0
	global_load_dword v247, v209, s[44:45]
	global_load_dword v248, v209, s[44:45] offset:256
	global_load_dword v249, v209, s[44:45] offset:512
	global_load_dword v250, v209, s[44:45] offset:768
	global_load_dword v251, v209, s[44:45] offset:1024
	global_load_dword v252, v209, s[44:45] offset:1280
	global_load_dword v253, v209, s[44:45] offset:1536
	global_load_dword v254, v209, s[44:45] offset:1792
	v_add_u32_e32 v182, 0x0, v210
	v_add_u32_e32 v183, 0x1000, v182
	global_load_ushort v128, v182, s[40:41]
	global_load_ushort v129, v182, s[40:41] offset:2048
	global_load_ushort v130, v183, s[40:41]
	global_load_ushort v131, v183, s[40:41] offset:2048
	v_add_u32_e32 v182, 0x8000, v210
	v_add_u32_e32 v183, 0x1000, v182
	global_load_ushort v132, v182, s[40:41]
	global_load_ushort v133, v182, s[40:41] offset:2048
	global_load_ushort v134, v183, s[40:41]
	global_load_ushort v135, v183, s[40:41] offset:2048
	v_add_u32_e32 v182, 0x10000, v210
	v_add_u32_e32 v183, 0x1000, v182
	global_load_ushort v136, v182, s[40:41]
	global_load_ushort v137, v182, s[40:41] offset:2048
	global_load_ushort v138, v183, s[40:41]
	global_load_ushort v139, v183, s[40:41] offset:2048
	v_add_u32_e32 v182, 0x18000, v210
	v_add_u32_e32 v183, 0x1000, v182
	global_load_ushort v140, v182, s[40:41]
	global_load_ushort v141, v182, s[40:41] offset:2048
	global_load_ushort v142, v183, s[40:41]
	global_load_ushort v143, v183, s[40:41] offset:2048
	s_cmp_eq_u32 s7, 0
	s_cbranch_scc0 .Lmylru_nm_7
	v_mov_b32_e32 v163, v162
	ds_read_b128 v[96:99], v163
	ds_read_b128 v[100:103], v163 offset:8192
	ds_read_b128 v[104:107], v163 offset:16384
	ds_read_b128 v[108:111], v163 offset:24576
	v_xor_b32_e32 v164, 0x40, v163
	ds_read_b128 v[112:115], v164
	ds_read_b128 v[116:119], v164 offset:8192
	ds_read_b128 v[120:123], v164 offset:16384
	ds_read_b128 v[124:127], v164 offset:24576
	s_waitcnt lgkmcnt(7)
	v_mfma_f32_16x16x32_bf16 v[64:67], v[96:99], v[0:3], 0
	v_mfma_f32_16x16x32_bf16 v[68:71], v[96:99], v[32:35], 0
	v_xor_b32_e32 v164, 0x80, v163
	ds_read_b128 v[96:99], v164
	s_waitcnt lgkmcnt(7)
	v_mfma_f32_16x16x32_bf16 v[72:75], v[100:103], v[0:3], 0
	v_mfma_f32_16x16x32_bf16 v[76:79], v[100:103], v[32:35], 0
	ds_read_b128 v[100:103], v164 offset:8192
	s_waitcnt lgkmcnt(7)
	v_mfma_f32_16x16x32_bf16 v[80:83], v[104:107], v[0:3], 0
	v_mfma_f32_16x16x32_bf16 v[84:87], v[104:107], v[32:35], 0
	ds_read_b128 v[104:107], v164 offset:16384
	s_waitcnt lgkmcnt(7)
	v_mfma_f32_16x16x32_bf16 v[88:91], v[108:111], v[0:3], 0
	v_mfma_f32_16x16x32_bf16 v[92:95], v[108:111], v[32:35], 0
	ds_read_b128 v[108:111], v164 offset:24576
	s_waitcnt lgkmcnt(7)
	v_mfma_f32_16x16x32_bf16 v[64:67], v[112:115], v[4:7], v[64:67]
	v_mfma_f32_16x16x32_bf16 v[68:71], v[112:115], v[36:39], v[68:71]
	v_xor_b32_e32 v164, 0xc0, v163
	ds_read_b128 v[112:115], v164
	s_waitcnt lgkmcnt(7)
	v_mfma_f32_16x16x32_bf16 v[72:75], v[116:119], v[4:7], v[72:75]
	v_mfma_f32_16x16x32_bf16 v[76:79], v[116:119], v[36:39], v[76:79]
	ds_read_b128 v[116:119], v164 offset:8192
	s_waitcnt lgkmcnt(7)
	v_mfma_f32_16x16x32_bf16 v[80:83], v[120:123], v[4:7], v[80:83]
	v_mfma_f32_16x16x32_bf16 v[84:87], v[120:123], v[36:39], v[84:87]
	ds_read_b128 v[120:123], v164 offset:16384
	s_waitcnt lgkmcnt(7)
	v_mfma_f32_16x16x32_bf16 v[88:91], v[124:127], v[4:7], v[88:91]
	v_mfma_f32_16x16x32_bf16 v[92:95], v[124:127], v[36:39], v[92:95]
	ds_read_b128 v[124:127], v164 offset:24576
	s_waitcnt lgkmcnt(7)
	v_mfma_f32_16x16x32_bf16 v[64:67], v[96:99], v[8:11], v[64:67]
	v_mfma_f32_16x16x32_bf16 v[68:71], v[96:99], v[40:43], v[68:71]
	v_xor_b32_e32 v164, 0x100, v163
	ds_read_b128 v[96:99], v164
	s_waitcnt lgkmcnt(7)
	v_mfma_f32_16x16x32_bf16 v[72:75], v[100:103], v[8:11], v[72:75]
	v_mfma_f32_16x16x32_bf16 v[76:79], v[100:103], v[40:43], v[76:79]
	ds_read_b128 v[100:103], v164 offset:8192
	s_waitcnt lgkmcnt(7)
	v_mfma_f32_16x16x32_bf16 v[80:83], v[104:107], v[8:11], v[80:83]
	v_mfma_f32_16x16x32_bf16 v[84:87], v[104:107], v[40:43], v[84:87]
	ds_read_b128 v[104:107], v164 offset:16384
	s_waitcnt lgkmcnt(7)
	v_mfma_f32_16x16x32_bf16 v[88:91], v[108:111], v[8:11], v[88:91]
	v_mfma_f32_16x16x32_bf16 v[92:95], v[108:111], v[40:43], v[92:95]
	ds_read_b128 v[108:111], v164 offset:24576
	s_waitcnt lgkmcnt(7)
	v_mfma_f32_16x16x32_bf16 v[64:67], v[112:115], v[12:15], v[64:67]
	v_mfma_f32_16x16x32_bf16 v[68:71], v[112:115], v[44:47], v[68:71]
	v_xor_b32_e32 v164, 0x140, v163
	ds_read_b128 v[112:115], v164
	s_waitcnt lgkmcnt(7)
	v_mfma_f32_16x16x32_bf16 v[72:75], v[116:119], v[12:15], v[72:75]
	v_mfma_f32_16x16x32_bf16 v[76:79], v[116:119], v[44:47], v[76:79]
	ds_read_b128 v[116:119], v164 offset:8192
	s_waitcnt lgkmcnt(7)
	v_mfma_f32_16x16x32_bf16 v[80:83], v[120:123], v[12:15], v[80:83]
	v_mfma_f32_16x16x32_bf16 v[84:87], v[120:123], v[44:47], v[84:87]
	ds_read_b128 v[120:123], v164 offset:16384
	s_waitcnt lgkmcnt(7)
	v_mfma_f32_16x16x32_bf16 v[88:91], v[124:127], v[12:15], v[88:91]
	v_mfma_f32_16x16x32_bf16 v[92:95], v[124:127], v[44:47], v[92:95]
	ds_read_b128 v[124:127], v164 offset:24576
	s_waitcnt lgkmcnt(7)
	v_mfma_f32_16x16x32_bf16 v[64:67], v[96:99], v[16:19], v[64:67]
	v_mfma_f32_16x16x32_bf16 v[68:71], v[96:99], v[48:51], v[68:71]
	v_xor_b32_e32 v164, 0x180, v163
	ds_read_b128 v[96:99], v164
	s_waitcnt lgkmcnt(7)
	v_mfma_f32_16x16x32_bf16 v[72:75], v[100:103], v[16:19], v[72:75]
	v_mfma_f32_16x16x32_bf16 v[76:79], v[100:103], v[48:51], v[76:79]
	ds_read_b128 v[100:103], v164 offset:8192
	s_waitcnt lgkmcnt(7)
	v_mfma_f32_16x16x32_bf16 v[80:83], v[104:107], v[16:19], v[80:83]
	v_mfma_f32_16x16x32_bf16 v[84:87], v[104:107], v[48:51], v[84:87]
	ds_read_b128 v[104:107], v164 offset:16384
	s_waitcnt lgkmcnt(7)
	v_mfma_f32_16x16x32_bf16 v[88:91], v[108:111], v[16:19], v[88:91]
	v_mfma_f32_16x16x32_bf16 v[92:95], v[108:111], v[48:51], v[92:95]
	ds_read_b128 v[108:111], v164 offset:24576
	s_waitcnt lgkmcnt(7)
	v_mfma_f32_16x16x32_bf16 v[64:67], v[112:115], v[20:23], v[64:67]
	v_mfma_f32_16x16x32_bf16 v[68:71], v[112:115], v[52:55], v[68:71]
	v_xor_b32_e32 v164, 0x1c0, v163
	ds_read_b128 v[112:115], v164
	s_waitcnt lgkmcnt(7)
	v_mfma_f32_16x16x32_bf16 v[72:75], v[116:119], v[20:23], v[72:75]
	v_mfma_f32_16x16x32_bf16 v[76:79], v[116:119], v[52:55], v[76:79]
	ds_read_b128 v[116:119], v164 offset:8192
	s_waitcnt lgkmcnt(7)
	v_mfma_f32_16x16x32_bf16 v[80:83], v[120:123], v[20:23], v[80:83]
	v_mfma_f32_16x16x32_bf16 v[84:87], v[120:123], v[52:55], v[84:87]
	ds_read_b128 v[120:123], v164 offset:16384
	s_waitcnt lgkmcnt(7)
	v_mfma_f32_16x16x32_bf16 v[88:91], v[124:127], v[20:23], v[88:91]
	v_mfma_f32_16x16x32_bf16 v[92:95], v[124:127], v[52:55], v[92:95]
	ds_read_b128 v[124:127], v164 offset:24576
	s_waitcnt lgkmcnt(7)
	v_mfma_f32_16x16x32_bf16 v[64:67], v[96:99], v[24:27], v[64:67]
	v_mfma_f32_16x16x32_bf16 v[68:71], v[96:99], v[56:59], v[68:71]
	s_waitcnt lgkmcnt(6)
	v_mfma_f32_16x16x32_bf16 v[72:75], v[100:103], v[24:27], v[72:75]
	v_mfma_f32_16x16x32_bf16 v[76:79], v[100:103], v[56:59], v[76:79]
	s_waitcnt lgkmcnt(5)
	v_mfma_f32_16x16x32_bf16 v[80:83], v[104:107], v[24:27], v[80:83]
	v_mfma_f32_16x16x32_bf16 v[84:87], v[104:107], v[56:59], v[84:87]
	s_waitcnt lgkmcnt(4)
	v_mfma_f32_16x16x32_bf16 v[88:91], v[108:111], v[24:27], v[88:91]
	v_mfma_f32_16x16x32_bf16 v[92:95], v[108:111], v[56:59], v[92:95]
	s_waitcnt lgkmcnt(3)
	v_mfma_f32_16x16x32_bf16 v[64:67], v[112:115], v[28:31], v[64:67]
	v_mfma_f32_16x16x32_bf16 v[68:71], v[112:115], v[60:63], v[68:71]
	s_waitcnt lgkmcnt(2)
	v_mfma_f32_16x16x32_bf16 v[72:75], v[116:119], v[28:31], v[72:75]
	v_mfma_f32_16x16x32_bf16 v[76:79], v[116:119], v[60:63], v[76:79]
	s_waitcnt lgkmcnt(1)
	v_mfma_f32_16x16x32_bf16 v[80:83], v[120:123], v[28:31], v[80:83]
	v_mfma_f32_16x16x32_bf16 v[84:87], v[120:123], v[60:63], v[84:87]
	s_waitcnt lgkmcnt(0)
	v_mfma_f32_16x16x32_bf16 v[88:91], v[124:127], v[28:31], v[88:91]
	v_mfma_f32_16x16x32_bf16 v[92:95], v[124:127], v[60:63], v[92:95]
.Lmylru_nm_7:
	v_mov_b32_e32 v169, v165
	v_mov_b32_e32 v170, v166
	v_mov_b32_e32 v171, v167
	v_mov_b32_e32 v172, v168
	ds_read_u16 v144, v169
	ds_read_u16 v145, v170
	ds_read_u16 v146, v171
	ds_read_u16 v147, v172
	ds_read_u16 v148, v169 offset:8192
	ds_read_u16 v149, v170 offset:8192
	ds_read_u16 v150, v171 offset:8192
	ds_read_u16 v151, v172 offset:8192
	ds_read_u16 v152, v169 offset:16384
	ds_read_u16 v153, v170 offset:16384
	ds_read_u16 v154, v171 offset:16384
	ds_read_u16 v155, v172 offset:16384
	ds_read_u16 v156, v169 offset:24576
	ds_read_u16 v157, v170 offset:24576
	ds_read_u16 v158, v171 offset:24576
	ds_read_u16 v159, v172 offset:24576
	s_nop 7
	v_fma_f32 v178, v64, s53, v173
	v_fma_f32 v179, v65, s53, v173
	v_fma_f32 v180, v66, s53, v173
	v_fma_f32 v181, v67, s53, v173
	v_fma_f32 v182, v72, s53, v173
	v_fma_f32 v183, v73, s53, v173
	v_fma_f32 v184, v74, s53, v173
	v_fma_f32 v185, v75, s53, v173
	v_fma_f32 v186, v68, s53, v174
	v_fma_f32 v187, v69, s53, v174
	v_fma_f32 v188, v70, s53, v174
	v_fma_f32 v189, v71, s53, v174
	v_fma_f32 v190, v76, s53, v174
	v_fma_f32 v191, v77, s53, v174
	v_fma_f32 v192, v78, s53, v174
	v_fma_f32 v193, v79, s53, v174
	v_exp_f32_e32 v178, v178
	v_exp_f32_e32 v179, v179
	v_exp_f32_e32 v180, v180
	v_exp_f32_e32 v181, v181
	v_exp_f32_e32 v182, v182
	v_exp_f32_e32 v183, v183
	v_exp_f32_e32 v184, v184
	v_exp_f32_e32 v185, v185
	v_exp_f32_e32 v186, v186
	v_exp_f32_e32 v187, v187
	v_exp_f32_e32 v188, v188
	v_exp_f32_e32 v189, v189
	v_exp_f32_e32 v190, v190
	v_exp_f32_e32 v191, v191
	v_exp_f32_e32 v192, v192
	v_exp_f32_e32 v193, v193
	v_add_f32_e32 v178, 1.0, v178
	v_add_f32_e32 v179, 1.0, v179
	v_add_f32_e32 v180, 1.0, v180
	v_add_f32_e32 v181, 1.0, v181
	v_add_f32_e32 v182, 1.0, v182
	v_add_f32_e32 v183, 1.0, v183
	v_add_f32_e32 v184, 1.0, v184
	v_add_f32_e32 v185, 1.0, v185
	v_add_f32_e32 v186, 1.0, v186
	v_add_f32_e32 v187, 1.0, v187
	v_add_f32_e32 v188, 1.0, v188
	v_add_f32_e32 v189, 1.0, v189
	v_add_f32_e32 v190, 1.0, v190
	v_add_f32_e32 v191, 1.0, v191
	v_add_f32_e32 v192, 1.0, v192
	v_add_f32_e32 v193, 1.0, v193
	v_rcp_f32_e32 v178, v178
	v_rcp_f32_e32 v179, v179
	v_rcp_f32_e32 v180, v180
	v_rcp_f32_e32 v181, v181
	v_rcp_f32_e32 v182, v182
	v_rcp_f32_e32 v183, v183
	v_rcp_f32_e32 v184, v184
	v_rcp_f32_e32 v185, v185
	v_rcp_f32_e32 v186, v186
	v_rcp_f32_e32 v187, v187
	v_rcp_f32_e32 v188, v188
	v_rcp_f32_e32 v189, v189
	v_rcp_f32_e32 v190, v190
	v_rcp_f32_e32 v191, v191
	v_rcp_f32_e32 v192, v192
	v_rcp_f32_e32 v193, v193
	v_mul_f32_e32 v178, v175, v178
	v_mul_f32_e32 v179, v175, v179
	v_mul_f32_e32 v180, v175, v180
	v_mul_f32_e32 v181, v175, v181
	v_mul_f32_e32 v182, v175, v182
	v_mul_f32_e32 v183, v175, v183
	v_mul_f32_e32 v184, v175, v184
	v_mul_f32_e32 v185, v175, v185
	v_exp_f32_e32 v96, v178
	v_exp_f32_e32 v97, v179
	v_exp_f32_e32 v98, v180
	v_exp_f32_e32 v99, v181
	v_exp_f32_e32 v100, v182
	v_exp_f32_e32 v101, v183
	v_exp_f32_e32 v102, v184
	v_exp_f32_e32 v103, v185
	s_nop 0
	v_fma_f32 v194, -v96, v96, 1.0
	v_fma_f32 v195, -v97, v97, 1.0
	v_fma_f32 v196, -v98, v98, 1.0
	v_fma_f32 v197, -v99, v99, 1.0
	v_fma_f32 v198, -v100, v100, 1.0
	v_fma_f32 v199, -v101, v101, 1.0
	v_fma_f32 v200, -v102, v102, 1.0
	v_fma_f32 v201, -v103, v103, 1.0
	v_max_f32_e32 v194, 0, v194
	v_max_f32_e32 v195, 0, v195
	v_max_f32_e32 v196, 0, v196
	v_max_f32_e32 v197, 0, v197
	v_max_f32_e32 v198, 0, v198
	v_max_f32_e32 v199, 0, v199
	v_max_f32_e32 v200, 0, v200
	v_max_f32_e32 v201, 0, v201
	v_sqrt_f32_e32 v194, v194
	v_sqrt_f32_e32 v195, v195
	v_sqrt_f32_e32 v196, v196
	v_sqrt_f32_e32 v197, v197
	v_sqrt_f32_e32 v198, v198
	v_sqrt_f32_e32 v199, v199
	v_sqrt_f32_e32 v200, v200
	v_sqrt_f32_e32 v201, v201
	s_waitcnt lgkmcnt(8)
	v_lshlrev_b32_e32 v144, 16, v144
	v_lshlrev_b32_e32 v145, 16, v145
	v_lshlrev_b32_e32 v146, 16, v146
	v_lshlrev_b32_e32 v147, 16, v147
	v_lshlrev_b32_e32 v148, 16, v148
	v_lshlrev_b32_e32 v149, 16, v149
	v_lshlrev_b32_e32 v150, 16, v150
	v_lshlrev_b32_e32 v151, 16, v151
	v_mul_f32_e32 v194, v194, v186
	v_mul_f32_e32 v195, v195, v187
	v_mul_f32_e32 v196, v196, v188
	v_mul_f32_e32 v197, v197, v189
	v_mul_f32_e32 v198, v198, v190
	v_mul_f32_e32 v199, v199, v191
	v_mul_f32_e32 v200, v200, v192
	v_mul_f32_e32 v201, v201, v193
	v_mul_f32_e32 v144, v194, v144
	v_mul_f32_e32 v145, v195, v145
	v_mul_f32_e32 v146, v196, v146
	v_mul_f32_e32 v147, v197, v147
	v_mul_f32_e32 v148, v198, v148
	v_mul_f32_e32 v149, v199, v149
	v_mul_f32_e32 v150, v200, v150
	v_mul_f32_e32 v151, v201, v151
	v_fma_f32 v178, v80, s53, v173
	v_fma_f32 v179, v81, s53, v173
	v_fma_f32 v180, v82, s53, v173
	v_fma_f32 v181, v83, s53, v173
	v_fma_f32 v182, v88, s53, v173
	v_fma_f32 v183, v89, s53, v173
	v_fma_f32 v184, v90, s53, v173
	v_fma_f32 v185, v91, s53, v173
	v_fma_f32 v186, v84, s53, v174
	v_fma_f32 v187, v85, s53, v174
	v_fma_f32 v188, v86, s53, v174
	v_fma_f32 v189, v87, s53, v174
	v_fma_f32 v190, v92, s53, v174
	v_fma_f32 v191, v93, s53, v174
	v_fma_f32 v192, v94, s53, v174
	v_fma_f32 v193, v95, s53, v174
	v_exp_f32_e32 v178, v178
	v_exp_f32_e32 v179, v179
	v_exp_f32_e32 v180, v180
	v_exp_f32_e32 v181, v181
	v_exp_f32_e32 v182, v182
	v_exp_f32_e32 v183, v183
	v_exp_f32_e32 v184, v184
	v_exp_f32_e32 v185, v185
	v_exp_f32_e32 v186, v186
	v_exp_f32_e32 v187, v187
	v_exp_f32_e32 v188, v188
	v_exp_f32_e32 v189, v189
	v_exp_f32_e32 v190, v190
	v_exp_f32_e32 v191, v191
	v_exp_f32_e32 v192, v192
	v_exp_f32_e32 v193, v193
	v_add_f32_e32 v178, 1.0, v178
	v_add_f32_e32 v179, 1.0, v179
	v_add_f32_e32 v180, 1.0, v180
	v_add_f32_e32 v181, 1.0, v181
	v_add_f32_e32 v182, 1.0, v182
	v_add_f32_e32 v183, 1.0, v183
	v_add_f32_e32 v184, 1.0, v184
	v_add_f32_e32 v185, 1.0, v185
	v_add_f32_e32 v186, 1.0, v186
	v_add_f32_e32 v187, 1.0, v187
	v_add_f32_e32 v188, 1.0, v188
	v_add_f32_e32 v189, 1.0, v189
	v_add_f32_e32 v190, 1.0, v190
	v_add_f32_e32 v191, 1.0, v191
	v_add_f32_e32 v192, 1.0, v192
	v_add_f32_e32 v193, 1.0, v193
	v_rcp_f32_e32 v178, v178
	v_rcp_f32_e32 v179, v179
	v_rcp_f32_e32 v180, v180
	v_rcp_f32_e32 v181, v181
	v_rcp_f32_e32 v182, v182
	v_rcp_f32_e32 v183, v183
	v_rcp_f32_e32 v184, v184
	v_rcp_f32_e32 v185, v185
	v_rcp_f32_e32 v186, v186
	v_rcp_f32_e32 v187, v187
	v_rcp_f32_e32 v188, v188
	v_rcp_f32_e32 v189, v189
	v_rcp_f32_e32 v190, v190
	v_rcp_f32_e32 v191, v191
	v_rcp_f32_e32 v192, v192
	v_rcp_f32_e32 v193, v193
	v_mul_f32_e32 v178, v175, v178
	v_mul_f32_e32 v179, v175, v179
	v_mul_f32_e32 v180, v175, v180
	v_mul_f32_e32 v181, v175, v181
	v_mul_f32_e32 v182, v175, v182
	v_mul_f32_e32 v183, v175, v183
	v_mul_f32_e32 v184, v175, v184
	v_mul_f32_e32 v185, v175, v185
	v_exp_f32_e32 v104, v178
	v_exp_f32_e32 v105, v179
	v_exp_f32_e32 v106, v180
	v_exp_f32_e32 v107, v181
	v_exp_f32_e32 v108, v182
	v_exp_f32_e32 v109, v183
	v_exp_f32_e32 v110, v184
	v_exp_f32_e32 v111, v185
	s_nop 0
	v_fma_f32 v194, -v104, v104, 1.0
	v_fma_f32 v195, -v105, v105, 1.0
	v_fma_f32 v196, -v106, v106, 1.0
	v_fma_f32 v197, -v107, v107, 1.0
	v_fma_f32 v198, -v108, v108, 1.0
	v_fma_f32 v199, -v109, v109, 1.0
	v_fma_f32 v200, -v110, v110, 1.0
	v_fma_f32 v201, -v111, v111, 1.0
	v_max_f32_e32 v194, 0, v194
	v_max_f32_e32 v195, 0, v195
	v_max_f32_e32 v196, 0, v196
	v_max_f32_e32 v197, 0, v197
	v_max_f32_e32 v198, 0, v198
	v_max_f32_e32 v199, 0, v199
	v_max_f32_e32 v200, 0, v200
	v_max_f32_e32 v201, 0, v201
	v_sqrt_f32_e32 v194, v194
	v_sqrt_f32_e32 v195, v195
	v_sqrt_f32_e32 v196, v196
	v_sqrt_f32_e32 v197, v197
	v_sqrt_f32_e32 v198, v198
	v_sqrt_f32_e32 v199, v199
	v_sqrt_f32_e32 v200, v200
	v_sqrt_f32_e32 v201, v201
	s_waitcnt lgkmcnt(0)
	v_lshlrev_b32_e32 v152, 16, v152
	v_lshlrev_b32_e32 v153, 16, v153
	v_lshlrev_b32_e32 v154, 16, v154
	v_lshlrev_b32_e32 v155, 16, v155
	v_lshlrev_b32_e32 v156, 16, v156
	v_lshlrev_b32_e32 v157, 16, v157
	v_lshlrev_b32_e32 v158, 16, v158
	v_lshlrev_b32_e32 v159, 16, v159
	v_mul_f32_e32 v194, v194, v186
	v_mul_f32_e32 v195, v195, v187
	v_mul_f32_e32 v196, v196, v188
	v_mul_f32_e32 v197, v197, v189
	v_mul_f32_e32 v198, v198, v190
	v_mul_f32_e32 v199, v199, v191
	v_mul_f32_e32 v200, v200, v192
	v_mul_f32_e32 v201, v201, v193
	v_mul_f32_e32 v152, v194, v152
	v_mul_f32_e32 v153, v195, v153
	v_mul_f32_e32 v154, v196, v154
	v_mul_f32_e32 v155, v197, v155
	v_mul_f32_e32 v156, v198, v156
	v_mul_f32_e32 v157, v199, v157
	v_mul_f32_e32 v158, v200, v158
	v_mul_f32_e32 v159, v201, v159
	v_fma_f32 v146, v98, v147, v146
	v_fma_f32 v150, v102, v151, v150
	v_fma_f32 v154, v106, v155, v154
	v_fma_f32 v158, v110, v159, v158
	v_mul_f32_e32 v98, v98, v99
	v_mul_f32_e32 v102, v102, v103
	v_mul_f32_e32 v106, v106, v107
	v_mul_f32_e32 v110, v110, v111
	v_fma_f32 v145, v97, v146, v145
	v_fma_f32 v149, v101, v150, v149
	v_fma_f32 v153, v105, v154, v153
	v_fma_f32 v157, v109, v158, v157
	v_mul_f32_e32 v97, v97, v98
	v_mul_f32_e32 v101, v101, v102
	v_mul_f32_e32 v105, v105, v106
	v_mul_f32_e32 v109, v109, v110
	v_fma_f32 v144, v96, v145, v144
	v_fma_f32 v148, v100, v149, v148
	v_fma_f32 v152, v104, v153, v152
	v_fma_f32 v156, v108, v157, v156
	v_mul_f32_e32 v96, v96, v97
	v_mul_f32_e32 v100, v100, v101
	v_mul_f32_e32 v104, v104, v105
	v_mul_f32_e32 v108, v108, v109
	ds_bpermute_b32 v178, v204, v96
	ds_bpermute_b32 v182, v204, v144
	ds_bpermute_b32 v179, v204, v100
	ds_bpermute_b32 v183, v204, v148
	ds_bpermute_b32 v180, v204, v104
	ds_bpermute_b32 v184, v204, v152
	ds_bpermute_b32 v181, v204, v108
	ds_bpermute_b32 v185, v204, v156
	s_waitcnt lgkmcnt(0)
	v_fma_f32 v186, v182, v96, v144
	v_cndmask_b32_e64 v178, 1.0, v178, s[34:35]
	v_fma_f32 v187, v183, v100, v148
	v_cndmask_b32_e64 v179, 1.0, v179, s[34:35]
	v_fma_f32 v188, v184, v104, v152
	v_cndmask_b32_e64 v180, 1.0, v180, s[34:35]
	v_fma_f32 v189, v185, v108, v156
	v_cndmask_b32_e64 v181, 1.0, v181, s[34:35]
	v_cndmask_b32_e64 v223, v144, v186, s[34:35]
	v_mul_f32_e32 v219, v96, v178
	v_cndmask_b32_e64 v224, v148, v187, s[34:35]
	v_mul_f32_e32 v220, v100, v179
	v_cndmask_b32_e64 v225, v152, v188, s[34:35]
	v_mul_f32_e32 v221, v104, v180
	v_cndmask_b32_e64 v226, v156, v189, s[34:35]
	v_mul_f32_e32 v222, v108, v181
	ds_bpermute_b32 v178, v205, v219
	ds_bpermute_b32 v182, v205, v223
	ds_bpermute_b32 v179, v205, v220
	ds_bpermute_b32 v183, v205, v224
	ds_bpermute_b32 v180, v205, v221
	ds_bpermute_b32 v184, v205, v225
	ds_bpermute_b32 v181, v205, v222
	ds_bpermute_b32 v185, v205, v226
	s_waitcnt lgkmcnt(0)
	v_fma_f32 v186, v182, v219, v223
	v_cndmask_b32_e64 v178, 1.0, v178, s[36:37]
	v_fma_f32 v187, v183, v220, v224
	v_cndmask_b32_e64 v179, 1.0, v179, s[36:37]
	v_fma_f32 v188, v184, v221, v225
	v_cndmask_b32_e64 v180, 1.0, v180, s[36:37]
	v_fma_f32 v189, v185, v222, v226
	v_cndmask_b32_e64 v181, 1.0, v181, s[36:37]
	v_cndmask_b32_e64 v223, v223, v186, s[36:37]
	v_mul_f32_e32 v219, v219, v178
	v_cndmask_b32_e64 v224, v224, v187, s[36:37]
	v_mul_f32_e32 v220, v220, v179
	v_cndmask_b32_e64 v225, v225, v188, s[36:37]
	v_mul_f32_e32 v221, v221, v180
	v_cndmask_b32_e64 v226, v226, v189, s[36:37]
	v_mul_f32_e32 v222, v222, v181
	ds_bpermute_b32 v227, v204, v219
	ds_bpermute_b32 v231, v204, v223
	ds_bpermute_b32 v235, v206, v219
	ds_bpermute_b32 v239, v206, v223
	ds_bpermute_b32 v228, v204, v220
	ds_bpermute_b32 v232, v204, v224
	ds_bpermute_b32 v236, v206, v220
	ds_bpermute_b32 v244, v206, v224
	ds_bpermute_b32 v229, v204, v221
	ds_bpermute_b32 v233, v204, v225
	ds_bpermute_b32 v237, v206, v221
	ds_bpermute_b32 v245, v206, v225
	ds_bpermute_b32 v230, v204, v222
	ds_bpermute_b32 v234, v204, v226
	ds_bpermute_b32 v238, v206, v222
	ds_bpermute_b32 v246, v206, v226
	s_waitcnt lgkmcnt(0)
	v_cndmask_b32_e64 v227, 1.0, v227, s[34:35]
	v_cndmask_b32_e64 v231, 0, v231, s[34:35]
	v_cndmask_b32_e64 v228, 1.0, v228, s[34:35]
	v_cndmask_b32_e64 v232, 0, v232, s[34:35]
	v_cndmask_b32_e64 v229, 1.0, v229, s[34:35]
	v_cndmask_b32_e64 v233, 0, v233, s[34:35]
	v_cndmask_b32_e64 v230, 1.0, v230, s[34:35]
	v_cndmask_b32_e64 v234, 0, v234, s[34:35]
	v_mov_b32_e32 v190, v238
	v_mov_b32_e32 v194, v246
	v_mov_b32_e32 v198, v190
	v_mov_b32_e32 v201, v194
	v_fma_f32 v194, v194, v237, v245
	v_mul_f32_e32 v190, v190, v237
	v_mov_b32_e32 v199, v190
	v_mov_b32_e32 v177, v194
	v_fma_f32 v194, v194, v236, v244
	v_mul_f32_e32 v190, v190, v236
	v_mov_b32_e32 v200, v190
	v_mov_b32_e32 v203, v194
	v_fma_f32 v194, v194, v235, v239
	v_mul_f32_e32 v190, v190, v235
	v_mov_b32_e32 v191, v194
	ds_write_b64 v207, v[190:191]
	s_cmp_eq_u32 s13, 2
	s_cbranch_scc1 .Lmylru_t0_7
	s_waitcnt vmcnt(40)
	s_branch .Lmylru_t1_7

.Lmylru_w1_7:
	v_lshlrev_b32_e32 v178, 16, v247
	v_add_f32_e32 v144, v144, v178
	v_lshlrev_b32_e32 v128, 16, v128
	v_mul_f32_e32 v144, v144, v128
	v_cvt_pk_bf16_f32 v144, v144, v144
	v_and_b32_e32 v179, 0xffff0000, v247
	v_add_f32_e32 v145, v145, v179
	v_lshlrev_b32_e32 v129, 16, v129
	v_mul_f32_e32 v145, v145, v129
	v_cvt_pk_bf16_f32 v145, v145, v145
	v_lshlrev_b32_e32 v180, 16, v248
	v_add_f32_e32 v146, v146, v180
	v_lshlrev_b32_e32 v130, 16, v130
	v_mul_f32_e32 v146, v146, v130
	v_cvt_pk_bf16_f32 v146, v146, v146
	v_and_b32_e32 v181, 0xffff0000, v248
	v_add_f32_e32 v147, v147, v181
	v_lshlrev_b32_e32 v131, 16, v131
	v_mul_f32_e32 v147, v147, v131
	v_cvt_pk_bf16_f32 v147, v147, v147
	v_lshlrev_b32_e32 v178, 16, v249
	v_add_f32_e32 v148, v148, v178
	v_lshlrev_b32_e32 v132, 16, v132
	v_mul_f32_e32 v148, v148, v132
	v_cvt_pk_bf16_f32 v148, v148, v148
	v_and_b32_e32 v179, 0xffff0000, v249
	v_add_f32_e32 v149, v149, v179
	v_lshlrev_b32_e32 v133, 16, v133
	v_mul_f32_e32 v149, v149, v133
	v_cvt_pk_bf16_f32 v149, v149, v149
	v_lshlrev_b32_e32 v180, 16, v250
	v_add_f32_e32 v150, v150, v180
	v_lshlrev_b32_e32 v134, 16, v134
	v_mul_f32_e32 v150, v150, v134
	v_cvt_pk_bf16_f32 v150, v150, v150
	v_and_b32_e32 v181, 0xffff0000, v250
	v_add_f32_e32 v151, v151, v181
	v_lshlrev_b32_e32 v135, 16, v135
	v_mul_f32_e32 v151, v151, v135
	v_cvt_pk_bf16_f32 v151, v151, v151
	v_lshlrev_b32_e32 v178, 16, v251
	v_add_f32_e32 v152, v152, v178
	v_lshlrev_b32_e32 v136, 16, v136
	v_mul_f32_e32 v152, v152, v136
	v_cvt_pk_bf16_f32 v152, v152, v152
	v_and_b32_e32 v179, 0xffff0000, v251
	v_add_f32_e32 v153, v153, v179
	v_lshlrev_b32_e32 v137, 16, v137
	v_mul_f32_e32 v153, v153, v137
	v_cvt_pk_bf16_f32 v153, v153, v153
	v_lshlrev_b32_e32 v180, 16, v252
	v_add_f32_e32 v154, v154, v180
	v_lshlrev_b32_e32 v138, 16, v138
	v_mul_f32_e32 v154, v154, v138
	v_cvt_pk_bf16_f32 v154, v154, v154
	v_and_b32_e32 v181, 0xffff0000, v252
	v_add_f32_e32 v155, v155, v181
	v_lshlrev_b32_e32 v139, 16, v139
	v_mul_f32_e32 v155, v155, v139
	v_cvt_pk_bf16_f32 v155, v155, v155
	v_lshlrev_b32_e32 v178, 16, v253
	v_add_f32_e32 v156, v156, v178
	v_lshlrev_b32_e32 v140, 16, v140
	v_mul_f32_e32 v156, v156, v140
	v_cvt_pk_bf16_f32 v156, v156, v156
	v_and_b32_e32 v179, 0xffff0000, v253
	v_add_f32_e32 v157, v157, v179
	v_lshlrev_b32_e32 v141, 16, v141
	v_mul_f32_e32 v157, v157, v141
	v_cvt_pk_bf16_f32 v157, v157, v157
	v_lshlrev_b32_e32 v180, 16, v254
	v_add_f32_e32 v158, v158, v180
	v_lshlrev_b32_e32 v142, 16, v142
	v_mul_f32_e32 v158, v158, v142
	v_cvt_pk_bf16_f32 v158, v158, v158
	v_and_b32_e32 v181, 0xffff0000, v254
	v_add_f32_e32 v159, v159, v181
	v_lshlrev_b32_e32 v143, 16, v143
	v_mul_f32_e32 v159, v159, v143
	v_cvt_pk_bf16_f32 v159, v159, v159
	v_add_u32_e32 v182, 0x0, v210
	v_add_u32_e32 v183, 0x1000, v182
	global_store_short v182, v144, s[42:43]
	global_store_short v182, v145, s[42:43] offset:2048
	global_store_short v183, v146, s[42:43]
	global_store_short v183, v147, s[42:43] offset:2048
	v_add_u32_e32 v182, 0x8000, v210
	v_add_u32_e32 v183, 0x1000, v182
	global_store_short v182, v148, s[42:43]
	global_store_short v182, v149, s[42:43] offset:2048
	global_store_short v183, v150, s[42:43]
	global_store_short v183, v151, s[42:43] offset:2048
	v_add_u32_e32 v182, 0x10000, v210
	v_add_u32_e32 v183, 0x1000, v182
	global_store_short v182, v152, s[42:43]
	global_store_short v182, v153, s[42:43] offset:2048
	global_store_short v183, v154, s[42:43]
	global_store_short v183, v155, s[42:43] offset:2048
	v_add_u32_e32 v182, 0x18000, v210
	v_add_u32_e32 v183, 0x1000, v182
	global_store_short v182, v156, s[42:43]
	global_store_short v182, v157, s[42:43] offset:2048
	global_store_short v183, v158, s[42:43]
	global_store_short v183, v159, s[42:43] offset:2048
	s_add_i32 s13, s13, 1
	s_sub_i32 s54, 17, s13
	s_lshl_b32 s55, s54, 14
	s_lshl_b32 s56, s6, 11
	s_add_i32 s55, s55, s56
	s_add_u32 s44, s22, s55
	s_addc_u32 s45, s23, 0
	s_cmp_lt_u32 s13, 2
	s_sub_i32 s50, 1, s13
	s_lshl_b32 s50, s50, 7
	s_lshl_b32 s51, s9, 8
	s_add_i32 s51, s51, 0x8000
	s_add_i32 s51, s51, s50
	s_sub_i32 s50, 17, s13
	s_lshl_b32 s50, s50, 7
	s_lshl_b32 s57, s9, 11
	s_add_i32 s57, s57, s50
	s_cmp_lt_u32 s13, 2
	s_cselect_b32 s57, s51, s57
	s_lshl_b32 s57, s57, 11
	s_add_u32 s40, s18, s57
	s_addc_u32 s41, s19, 0
	s_add_u32 s42, s20, s57
	s_addc_u32 s43, s21, 0
	global_load_dword v247, v209, s[44:45]
	global_load_dword v248, v209, s[44:45] offset:256
	global_load_dword v249, v209, s[44:45] offset:512
	global_load_dword v250, v209, s[44:45] offset:768
	global_load_dword v251, v209, s[44:45] offset:1024
	global_load_dword v252, v209, s[44:45] offset:1280
	global_load_dword v253, v209, s[44:45] offset:1536
	global_load_dword v254, v209, s[44:45] offset:1792
	v_add_u32_e32 v182, 0x0, v210
	v_add_u32_e32 v183, 0x1000, v182
	global_load_ushort v128, v182, s[40:41]
	global_load_ushort v129, v182, s[40:41] offset:2048
	global_load_ushort v130, v183, s[40:41]
	global_load_ushort v131, v183, s[40:41] offset:2048
	v_add_u32_e32 v182, 0x8000, v210
	v_add_u32_e32 v183, 0x1000, v182
	global_load_ushort v132, v182, s[40:41]
	global_load_ushort v133, v182, s[40:41] offset:2048
	global_load_ushort v134, v183, s[40:41]
	global_load_ushort v135, v183, s[40:41] offset:2048
	v_add_u32_e32 v182, 0x10000, v210
	v_add_u32_e32 v183, 0x1000, v182
	global_load_ushort v136, v182, s[40:41]
	global_load_ushort v137, v182, s[40:41] offset:2048
	global_load_ushort v138, v183, s[40:41]
	global_load_ushort v139, v183, s[40:41] offset:2048
	v_add_u32_e32 v182, 0x18000, v210
	v_add_u32_e32 v183, 0x1000, v182
	global_load_ushort v140, v182, s[40:41]
	global_load_ushort v141, v182, s[40:41] offset:2048
	global_load_ushort v142, v183, s[40:41]
	global_load_ushort v143, v183, s[40:41] offset:2048
	s_cmp_eq_u32 s7, 0
	s_cbranch_scc0 .Lmylru_nm_8
	v_or_b32_e32 v163, 0x10000, v162
	ds_read_b128 v[96:99], v163
	ds_read_b128 v[100:103], v163 offset:8192
	ds_read_b128 v[104:107], v163 offset:16384
	ds_read_b128 v[108:111], v163 offset:24576
	v_xor_b32_e32 v164, 0x40, v163
	ds_read_b128 v[112:115], v164
	ds_read_b128 v[116:119], v164 offset:8192
	ds_read_b128 v[120:123], v164 offset:16384
	ds_read_b128 v[124:127], v164 offset:24576
	s_waitcnt lgkmcnt(7)
	v_mfma_f32_16x16x32_bf16 v[64:67], v[96:99], v[0:3], 0
	v_mfma_f32_16x16x32_bf16 v[68:71], v[96:99], v[32:35], 0
	v_xor_b32_e32 v164, 0x80, v163
	ds_read_b128 v[96:99], v164
	s_waitcnt lgkmcnt(7)
	v_mfma_f32_16x16x32_bf16 v[72:75], v[100:103], v[0:3], 0
	v_mfma_f32_16x16x32_bf16 v[76:79], v[100:103], v[32:35], 0
	ds_read_b128 v[100:103], v164 offset:8192
	s_waitcnt lgkmcnt(7)
	v_mfma_f32_16x16x32_bf16 v[80:83], v[104:107], v[0:3], 0
	v_mfma_f32_16x16x32_bf16 v[84:87], v[104:107], v[32:35], 0
	ds_read_b128 v[104:107], v164 offset:16384
	s_waitcnt lgkmcnt(7)
	v_mfma_f32_16x16x32_bf16 v[88:91], v[108:111], v[0:3], 0
	v_mfma_f32_16x16x32_bf16 v[92:95], v[108:111], v[32:35], 0
	ds_read_b128 v[108:111], v164 offset:24576
	s_waitcnt lgkmcnt(7)
	v_mfma_f32_16x16x32_bf16 v[64:67], v[112:115], v[4:7], v[64:67]
	v_mfma_f32_16x16x32_bf16 v[68:71], v[112:115], v[36:39], v[68:71]
	v_xor_b32_e32 v164, 0xc0, v163
	ds_read_b128 v[112:115], v164
	s_waitcnt lgkmcnt(7)
	v_mfma_f32_16x16x32_bf16 v[72:75], v[116:119], v[4:7], v[72:75]
	v_mfma_f32_16x16x32_bf16 v[76:79], v[116:119], v[36:39], v[76:79]
	ds_read_b128 v[116:119], v164 offset:8192
	s_waitcnt lgkmcnt(7)
	v_mfma_f32_16x16x32_bf16 v[80:83], v[120:123], v[4:7], v[80:83]
	v_mfma_f32_16x16x32_bf16 v[84:87], v[120:123], v[36:39], v[84:87]
	ds_read_b128 v[120:123], v164 offset:16384
	s_waitcnt lgkmcnt(7)
	v_mfma_f32_16x16x32_bf16 v[88:91], v[124:127], v[4:7], v[88:91]
	v_mfma_f32_16x16x32_bf16 v[92:95], v[124:127], v[36:39], v[92:95]
	ds_read_b128 v[124:127], v164 offset:24576
	s_waitcnt lgkmcnt(7)
	v_mfma_f32_16x16x32_bf16 v[64:67], v[96:99], v[8:11], v[64:67]
	v_mfma_f32_16x16x32_bf16 v[68:71], v[96:99], v[40:43], v[68:71]
	v_xor_b32_e32 v164, 0x100, v163
	ds_read_b128 v[96:99], v164
	s_waitcnt lgkmcnt(7)
	v_mfma_f32_16x16x32_bf16 v[72:75], v[100:103], v[8:11], v[72:75]
	v_mfma_f32_16x16x32_bf16 v[76:79], v[100:103], v[40:43], v[76:79]
	ds_read_b128 v[100:103], v164 offset:8192
	s_waitcnt lgkmcnt(7)
	v_mfma_f32_16x16x32_bf16 v[80:83], v[104:107], v[8:11], v[80:83]
	v_mfma_f32_16x16x32_bf16 v[84:87], v[104:107], v[40:43], v[84:87]
	ds_read_b128 v[104:107], v164 offset:16384
	s_waitcnt lgkmcnt(7)
	v_mfma_f32_16x16x32_bf16 v[88:91], v[108:111], v[8:11], v[88:91]
	v_mfma_f32_16x16x32_bf16 v[92:95], v[108:111], v[40:43], v[92:95]
	ds_read_b128 v[108:111], v164 offset:24576
	s_waitcnt lgkmcnt(7)
	v_mfma_f32_16x16x32_bf16 v[64:67], v[112:115], v[12:15], v[64:67]
	v_mfma_f32_16x16x32_bf16 v[68:71], v[112:115], v[44:47], v[68:71]
	v_xor_b32_e32 v164, 0x140, v163
	ds_read_b128 v[112:115], v164
	s_waitcnt lgkmcnt(7)
	v_mfma_f32_16x16x32_bf16 v[72:75], v[116:119], v[12:15], v[72:75]
	v_mfma_f32_16x16x32_bf16 v[76:79], v[116:119], v[44:47], v[76:79]
	ds_read_b128 v[116:119], v164 offset:8192
	s_waitcnt lgkmcnt(7)
	v_mfma_f32_16x16x32_bf16 v[80:83], v[120:123], v[12:15], v[80:83]
	v_mfma_f32_16x16x32_bf16 v[84:87], v[120:123], v[44:47], v[84:87]
	ds_read_b128 v[120:123], v164 offset:16384
	s_waitcnt lgkmcnt(7)
	v_mfma_f32_16x16x32_bf16 v[88:91], v[124:127], v[12:15], v[88:91]
	v_mfma_f32_16x16x32_bf16 v[92:95], v[124:127], v[44:47], v[92:95]
	ds_read_b128 v[124:127], v164 offset:24576
	s_waitcnt lgkmcnt(7)
	v_mfma_f32_16x16x32_bf16 v[64:67], v[96:99], v[16:19], v[64:67]
	v_mfma_f32_16x16x32_bf16 v[68:71], v[96:99], v[48:51], v[68:71]
	v_xor_b32_e32 v164, 0x180, v163
	ds_read_b128 v[96:99], v164
	s_waitcnt lgkmcnt(7)
	v_mfma_f32_16x16x32_bf16 v[72:75], v[100:103], v[16:19], v[72:75]
	v_mfma_f32_16x16x32_bf16 v[76:79], v[100:103], v[48:51], v[76:79]
	ds_read_b128 v[100:103], v164 offset:8192
	s_waitcnt lgkmcnt(7)
	v_mfma_f32_16x16x32_bf16 v[80:83], v[104:107], v[16:19], v[80:83]
	v_mfma_f32_16x16x32_bf16 v[84:87], v[104:107], v[48:51], v[84:87]
	ds_read_b128 v[104:107], v164 offset:16384
	s_waitcnt lgkmcnt(7)
	v_mfma_f32_16x16x32_bf16 v[88:91], v[108:111], v[16:19], v[88:91]
	v_mfma_f32_16x16x32_bf16 v[92:95], v[108:111], v[48:51], v[92:95]
	ds_read_b128 v[108:111], v164 offset:24576
	s_waitcnt lgkmcnt(7)
	v_mfma_f32_16x16x32_bf16 v[64:67], v[112:115], v[20:23], v[64:67]
	v_mfma_f32_16x16x32_bf16 v[68:71], v[112:115], v[52:55], v[68:71]
	v_xor_b32_e32 v164, 0x1c0, v163
	ds_read_b128 v[112:115], v164
	s_waitcnt lgkmcnt(7)
	v_mfma_f32_16x16x32_bf16 v[72:75], v[116:119], v[20:23], v[72:75]
	v_mfma_f32_16x16x32_bf16 v[76:79], v[116:119], v[52:55], v[76:79]
	ds_read_b128 v[116:119], v164 offset:8192
	s_waitcnt lgkmcnt(7)
	v_mfma_f32_16x16x32_bf16 v[80:83], v[120:123], v[20:23], v[80:83]
	v_mfma_f32_16x16x32_bf16 v[84:87], v[120:123], v[52:55], v[84:87]
	ds_read_b128 v[120:123], v164 offset:16384
	s_waitcnt lgkmcnt(7)
	v_mfma_f32_16x16x32_bf16 v[88:91], v[124:127], v[20:23], v[88:91]
	v_mfma_f32_16x16x32_bf16 v[92:95], v[124:127], v[52:55], v[92:95]
	ds_read_b128 v[124:127], v164 offset:24576
	s_waitcnt lgkmcnt(7)
	v_mfma_f32_16x16x32_bf16 v[64:67], v[96:99], v[24:27], v[64:67]
	v_mfma_f32_16x16x32_bf16 v[68:71], v[96:99], v[56:59], v[68:71]
	s_waitcnt lgkmcnt(6)
	v_mfma_f32_16x16x32_bf16 v[72:75], v[100:103], v[24:27], v[72:75]
	v_mfma_f32_16x16x32_bf16 v[76:79], v[100:103], v[56:59], v[76:79]
	s_waitcnt lgkmcnt(5)
	v_mfma_f32_16x16x32_bf16 v[80:83], v[104:107], v[24:27], v[80:83]
	v_mfma_f32_16x16x32_bf16 v[84:87], v[104:107], v[56:59], v[84:87]
	s_waitcnt lgkmcnt(4)
	v_mfma_f32_16x16x32_bf16 v[88:91], v[108:111], v[24:27], v[88:91]
	v_mfma_f32_16x16x32_bf16 v[92:95], v[108:111], v[56:59], v[92:95]
	s_waitcnt lgkmcnt(3)
	v_mfma_f32_16x16x32_bf16 v[64:67], v[112:115], v[28:31], v[64:67]
	v_mfma_f32_16x16x32_bf16 v[68:71], v[112:115], v[60:63], v[68:71]
	s_waitcnt lgkmcnt(2)
	v_mfma_f32_16x16x32_bf16 v[72:75], v[116:119], v[28:31], v[72:75]
	v_mfma_f32_16x16x32_bf16 v[76:79], v[116:119], v[60:63], v[76:79]
	s_waitcnt lgkmcnt(1)
	v_mfma_f32_16x16x32_bf16 v[80:83], v[120:123], v[28:31], v[80:83]
	v_mfma_f32_16x16x32_bf16 v[84:87], v[120:123], v[60:63], v[84:87]
	s_waitcnt lgkmcnt(0)
	v_mfma_f32_16x16x32_bf16 v[88:91], v[124:127], v[28:31], v[88:91]
	v_mfma_f32_16x16x32_bf16 v[92:95], v[124:127], v[60:63], v[92:95]
.Lmylru_nm_8:
	v_or_b32_e32 v169, 0x10000, v165
	v_or_b32_e32 v170, 0x10000, v166
	v_or_b32_e32 v171, 0x10000, v167
	v_or_b32_e32 v172, 0x10000, v168
	ds_read_u16 v144, v169
	ds_read_u16 v145, v170
	ds_read_u16 v146, v171
	ds_read_u16 v147, v172
	ds_read_u16 v148, v169 offset:8192
	ds_read_u16 v149, v170 offset:8192
	ds_read_u16 v150, v171 offset:8192
	ds_read_u16 v151, v172 offset:8192
	ds_read_u16 v152, v169 offset:16384
	ds_read_u16 v153, v170 offset:16384
	ds_read_u16 v154, v171 offset:16384
	ds_read_u16 v155, v172 offset:16384
	ds_read_u16 v156, v169 offset:24576
	ds_read_u16 v157, v170 offset:24576
	ds_read_u16 v158, v171 offset:24576
	ds_read_u16 v159, v172 offset:24576
	s_nop 7
	v_fma_f32 v178, v64, s53, v173
	v_fma_f32 v179, v65, s53, v173
	v_fma_f32 v180, v66, s53, v173
	v_fma_f32 v181, v67, s53, v173
	v_fma_f32 v182, v72, s53, v173
	v_fma_f32 v183, v73, s53, v173
	v_fma_f32 v184, v74, s53, v173
	v_fma_f32 v185, v75, s53, v173
	v_fma_f32 v186, v68, s53, v174
	v_fma_f32 v187, v69, s53, v174
	v_fma_f32 v188, v70, s53, v174
	v_fma_f32 v189, v71, s53, v174
	v_fma_f32 v190, v76, s53, v174
	v_fma_f32 v191, v77, s53, v174
	v_fma_f32 v192, v78, s53, v174
	v_fma_f32 v193, v79, s53, v174
	v_exp_f32_e32 v178, v178
	v_exp_f32_e32 v179, v179
	v_exp_f32_e32 v180, v180
	v_exp_f32_e32 v181, v181
	v_exp_f32_e32 v182, v182
	v_exp_f32_e32 v183, v183
	v_exp_f32_e32 v184, v184
	v_exp_f32_e32 v185, v185
	v_exp_f32_e32 v186, v186
	v_exp_f32_e32 v187, v187
	v_exp_f32_e32 v188, v188
	v_exp_f32_e32 v189, v189
	v_exp_f32_e32 v190, v190
	v_exp_f32_e32 v191, v191
	v_exp_f32_e32 v192, v192
	v_exp_f32_e32 v193, v193
	v_add_f32_e32 v178, 1.0, v178
	v_add_f32_e32 v179, 1.0, v179
	v_add_f32_e32 v180, 1.0, v180
	v_add_f32_e32 v181, 1.0, v181
	v_add_f32_e32 v182, 1.0, v182
	v_add_f32_e32 v183, 1.0, v183
	v_add_f32_e32 v184, 1.0, v184
	v_add_f32_e32 v185, 1.0, v185
	v_add_f32_e32 v186, 1.0, v186
	v_add_f32_e32 v187, 1.0, v187
	v_add_f32_e32 v188, 1.0, v188
	v_add_f32_e32 v189, 1.0, v189
	v_add_f32_e32 v190, 1.0, v190
	v_add_f32_e32 v191, 1.0, v191
	v_add_f32_e32 v192, 1.0, v192
	v_add_f32_e32 v193, 1.0, v193
	v_rcp_f32_e32 v178, v178
	v_rcp_f32_e32 v179, v179
	v_rcp_f32_e32 v180, v180
	v_rcp_f32_e32 v181, v181
	v_rcp_f32_e32 v182, v182
	v_rcp_f32_e32 v183, v183
	v_rcp_f32_e32 v184, v184
	v_rcp_f32_e32 v185, v185
	v_rcp_f32_e32 v186, v186
	v_rcp_f32_e32 v187, v187
	v_rcp_f32_e32 v188, v188
	v_rcp_f32_e32 v189, v189
	v_rcp_f32_e32 v190, v190
	v_rcp_f32_e32 v191, v191
	v_rcp_f32_e32 v192, v192
	v_rcp_f32_e32 v193, v193
	v_mul_f32_e32 v178, v175, v178
	v_mul_f32_e32 v179, v175, v179
	v_mul_f32_e32 v180, v175, v180
	v_mul_f32_e32 v181, v175, v181
	v_mul_f32_e32 v182, v175, v182
	v_mul_f32_e32 v183, v175, v183
	v_mul_f32_e32 v184, v175, v184
	v_mul_f32_e32 v185, v175, v185
	v_exp_f32_e32 v96, v178
	v_exp_f32_e32 v97, v179
	v_exp_f32_e32 v98, v180
	v_exp_f32_e32 v99, v181
	v_exp_f32_e32 v100, v182
	v_exp_f32_e32 v101, v183
	v_exp_f32_e32 v102, v184
	v_exp_f32_e32 v103, v185
	s_nop 0
	v_fma_f32 v194, -v96, v96, 1.0
	v_fma_f32 v195, -v97, v97, 1.0
	v_fma_f32 v196, -v98, v98, 1.0
	v_fma_f32 v197, -v99, v99, 1.0
	v_fma_f32 v198, -v100, v100, 1.0
	v_fma_f32 v199, -v101, v101, 1.0
	v_fma_f32 v200, -v102, v102, 1.0
	v_fma_f32 v201, -v103, v103, 1.0
	v_max_f32_e32 v194, 0, v194
	v_max_f32_e32 v195, 0, v195
	v_max_f32_e32 v196, 0, v196
	v_max_f32_e32 v197, 0, v197
	v_max_f32_e32 v198, 0, v198
	v_max_f32_e32 v199, 0, v199
	v_max_f32_e32 v200, 0, v200
	v_max_f32_e32 v201, 0, v201
	v_sqrt_f32_e32 v194, v194
	v_sqrt_f32_e32 v195, v195
	v_sqrt_f32_e32 v196, v196
	v_sqrt_f32_e32 v197, v197
	v_sqrt_f32_e32 v198, v198
	v_sqrt_f32_e32 v199, v199
	v_sqrt_f32_e32 v200, v200
	v_sqrt_f32_e32 v201, v201
	s_waitcnt lgkmcnt(8)
	v_lshlrev_b32_e32 v144, 16, v144
	v_lshlrev_b32_e32 v145, 16, v145
	v_lshlrev_b32_e32 v146, 16, v146
	v_lshlrev_b32_e32 v147, 16, v147
	v_lshlrev_b32_e32 v148, 16, v148
	v_lshlrev_b32_e32 v149, 16, v149
	v_lshlrev_b32_e32 v150, 16, v150
	v_lshlrev_b32_e32 v151, 16, v151
	v_mul_f32_e32 v194, v194, v186
	v_mul_f32_e32 v195, v195, v187
	v_mul_f32_e32 v196, v196, v188
	v_mul_f32_e32 v197, v197, v189
	v_mul_f32_e32 v198, v198, v190
	v_mul_f32_e32 v199, v199, v191
	v_mul_f32_e32 v200, v200, v192
	v_mul_f32_e32 v201, v201, v193
	v_mul_f32_e32 v144, v194, v144
	v_mul_f32_e32 v145, v195, v145
	v_mul_f32_e32 v146, v196, v146
	v_mul_f32_e32 v147, v197, v147
	v_mul_f32_e32 v148, v198, v148
	v_mul_f32_e32 v149, v199, v149
	v_mul_f32_e32 v150, v200, v150
	v_mul_f32_e32 v151, v201, v151
	v_fma_f32 v178, v80, s53, v173
	v_fma_f32 v179, v81, s53, v173
	v_fma_f32 v180, v82, s53, v173
	v_fma_f32 v181, v83, s53, v173
	v_fma_f32 v182, v88, s53, v173
	v_fma_f32 v183, v89, s53, v173
	v_fma_f32 v184, v90, s53, v173
	v_fma_f32 v185, v91, s53, v173
	v_fma_f32 v186, v84, s53, v174
	v_fma_f32 v187, v85, s53, v174
	v_fma_f32 v188, v86, s53, v174
	v_fma_f32 v189, v87, s53, v174
	v_fma_f32 v190, v92, s53, v174
	v_fma_f32 v191, v93, s53, v174
	v_fma_f32 v192, v94, s53, v174
	v_fma_f32 v193, v95, s53, v174
	v_exp_f32_e32 v178, v178
	v_exp_f32_e32 v179, v179
	v_exp_f32_e32 v180, v180
	v_exp_f32_e32 v181, v181
	v_exp_f32_e32 v182, v182
	v_exp_f32_e32 v183, v183
	v_exp_f32_e32 v184, v184
	v_exp_f32_e32 v185, v185
	v_exp_f32_e32 v186, v186
	v_exp_f32_e32 v187, v187
	v_exp_f32_e32 v188, v188
	v_exp_f32_e32 v189, v189
	v_exp_f32_e32 v190, v190
	v_exp_f32_e32 v191, v191
	v_exp_f32_e32 v192, v192
	v_exp_f32_e32 v193, v193
	v_add_f32_e32 v178, 1.0, v178
	v_add_f32_e32 v179, 1.0, v179
	v_add_f32_e32 v180, 1.0, v180
	v_add_f32_e32 v181, 1.0, v181
	v_add_f32_e32 v182, 1.0, v182
	v_add_f32_e32 v183, 1.0, v183
	v_add_f32_e32 v184, 1.0, v184
	v_add_f32_e32 v185, 1.0, v185
	v_add_f32_e32 v186, 1.0, v186
	v_add_f32_e32 v187, 1.0, v187
	v_add_f32_e32 v188, 1.0, v188
	v_add_f32_e32 v189, 1.0, v189
	v_add_f32_e32 v190, 1.0, v190
	v_add_f32_e32 v191, 1.0, v191
	v_add_f32_e32 v192, 1.0, v192
	v_add_f32_e32 v193, 1.0, v193
	v_rcp_f32_e32 v178, v178
	v_rcp_f32_e32 v179, v179
	v_rcp_f32_e32 v180, v180
	v_rcp_f32_e32 v181, v181
	v_rcp_f32_e32 v182, v182
	v_rcp_f32_e32 v183, v183
	v_rcp_f32_e32 v184, v184
	v_rcp_f32_e32 v185, v185
	v_rcp_f32_e32 v186, v186
	v_rcp_f32_e32 v187, v187
	v_rcp_f32_e32 v188, v188
	v_rcp_f32_e32 v189, v189
	v_rcp_f32_e32 v190, v190
	v_rcp_f32_e32 v191, v191
	v_rcp_f32_e32 v192, v192
	v_rcp_f32_e32 v193, v193
	v_mul_f32_e32 v178, v175, v178
	v_mul_f32_e32 v179, v175, v179
	v_mul_f32_e32 v180, v175, v180
	v_mul_f32_e32 v181, v175, v181
	v_mul_f32_e32 v182, v175, v182
	v_mul_f32_e32 v183, v175, v183
	v_mul_f32_e32 v184, v175, v184
	v_mul_f32_e32 v185, v175, v185
	v_exp_f32_e32 v104, v178
	v_exp_f32_e32 v105, v179
	v_exp_f32_e32 v106, v180
	v_exp_f32_e32 v107, v181
	v_exp_f32_e32 v108, v182
	v_exp_f32_e32 v109, v183
	v_exp_f32_e32 v110, v184
	v_exp_f32_e32 v111, v185
	s_nop 0
	v_fma_f32 v194, -v104, v104, 1.0
	v_fma_f32 v195, -v105, v105, 1.0
	v_fma_f32 v196, -v106, v106, 1.0
	v_fma_f32 v197, -v107, v107, 1.0
	v_fma_f32 v198, -v108, v108, 1.0
	v_fma_f32 v199, -v109, v109, 1.0
	v_fma_f32 v200, -v110, v110, 1.0
	v_fma_f32 v201, -v111, v111, 1.0
	v_max_f32_e32 v194, 0, v194
	v_max_f32_e32 v195, 0, v195
	v_max_f32_e32 v196, 0, v196
	v_max_f32_e32 v197, 0, v197
	v_max_f32_e32 v198, 0, v198
	v_max_f32_e32 v199, 0, v199
	v_max_f32_e32 v200, 0, v200
	v_max_f32_e32 v201, 0, v201
	v_sqrt_f32_e32 v194, v194
	v_sqrt_f32_e32 v195, v195
	v_sqrt_f32_e32 v196, v196
	v_sqrt_f32_e32 v197, v197
	v_sqrt_f32_e32 v198, v198
	v_sqrt_f32_e32 v199, v199
	v_sqrt_f32_e32 v200, v200
	v_sqrt_f32_e32 v201, v201
	s_waitcnt lgkmcnt(0)
	v_lshlrev_b32_e32 v152, 16, v152
	v_lshlrev_b32_e32 v153, 16, v153
	v_lshlrev_b32_e32 v154, 16, v154
	v_lshlrev_b32_e32 v155, 16, v155
	v_lshlrev_b32_e32 v156, 16, v156
	v_lshlrev_b32_e32 v157, 16, v157
	v_lshlrev_b32_e32 v158, 16, v158
	v_lshlrev_b32_e32 v159, 16, v159
	v_mul_f32_e32 v194, v194, v186
	v_mul_f32_e32 v195, v195, v187
	v_mul_f32_e32 v196, v196, v188
	v_mul_f32_e32 v197, v197, v189
	v_mul_f32_e32 v198, v198, v190
	v_mul_f32_e32 v199, v199, v191
	v_mul_f32_e32 v200, v200, v192
	v_mul_f32_e32 v201, v201, v193
	v_mul_f32_e32 v152, v194, v152
	v_mul_f32_e32 v153, v195, v153
	v_mul_f32_e32 v154, v196, v154
	v_mul_f32_e32 v155, v197, v155
	v_mul_f32_e32 v156, v198, v156
	v_mul_f32_e32 v157, v199, v157
	v_mul_f32_e32 v158, v200, v158
	v_mul_f32_e32 v159, v201, v159
	v_fma_f32 v146, v98, v147, v146
	v_fma_f32 v150, v102, v151, v150
	v_fma_f32 v154, v106, v155, v154
	v_fma_f32 v158, v110, v159, v158
	v_mul_f32_e32 v98, v98, v99
	v_mul_f32_e32 v102, v102, v103
	v_mul_f32_e32 v106, v106, v107
	v_mul_f32_e32 v110, v110, v111
	v_fma_f32 v145, v97, v146, v145
	v_fma_f32 v149, v101, v150, v149
	v_fma_f32 v153, v105, v154, v153
	v_fma_f32 v157, v109, v158, v157
	v_mul_f32_e32 v97, v97, v98
	v_mul_f32_e32 v101, v101, v102
	v_mul_f32_e32 v105, v105, v106
	v_mul_f32_e32 v109, v109, v110
	v_fma_f32 v144, v96, v145, v144
	v_fma_f32 v148, v100, v149, v148
	v_fma_f32 v152, v104, v153, v152
	v_fma_f32 v156, v108, v157, v156
	v_mul_f32_e32 v96, v96, v97
	v_mul_f32_e32 v100, v100, v101
	v_mul_f32_e32 v104, v104, v105
	v_mul_f32_e32 v108, v108, v109
	ds_bpermute_b32 v178, v204, v96
	ds_bpermute_b32 v182, v204, v144
	ds_bpermute_b32 v179, v204, v100
	ds_bpermute_b32 v183, v204, v148
	ds_bpermute_b32 v180, v204, v104
	ds_bpermute_b32 v184, v204, v152
	ds_bpermute_b32 v181, v204, v108
	ds_bpermute_b32 v185, v204, v156
	s_waitcnt lgkmcnt(0)
	v_fma_f32 v186, v182, v96, v144
	v_cndmask_b32_e64 v178, 1.0, v178, s[34:35]
	v_fma_f32 v187, v183, v100, v148
	v_cndmask_b32_e64 v179, 1.0, v179, s[34:35]
	v_fma_f32 v188, v184, v104, v152
	v_cndmask_b32_e64 v180, 1.0, v180, s[34:35]
	v_fma_f32 v189, v185, v108, v156
	v_cndmask_b32_e64 v181, 1.0, v181, s[34:35]
	v_cndmask_b32_e64 v223, v144, v186, s[34:35]
	v_mul_f32_e32 v219, v96, v178
	v_cndmask_b32_e64 v224, v148, v187, s[34:35]
	v_mul_f32_e32 v220, v100, v179
	v_cndmask_b32_e64 v225, v152, v188, s[34:35]
	v_mul_f32_e32 v221, v104, v180
	v_cndmask_b32_e64 v226, v156, v189, s[34:35]
	v_mul_f32_e32 v222, v108, v181
	ds_bpermute_b32 v178, v205, v219
	ds_bpermute_b32 v182, v205, v223
	ds_bpermute_b32 v179, v205, v220
	ds_bpermute_b32 v183, v205, v224
	ds_bpermute_b32 v180, v205, v221
	ds_bpermute_b32 v184, v205, v225
	ds_bpermute_b32 v181, v205, v222
	ds_bpermute_b32 v185, v205, v226
	s_waitcnt lgkmcnt(0)
	v_fma_f32 v186, v182, v219, v223
	v_cndmask_b32_e64 v178, 1.0, v178, s[36:37]
	v_fma_f32 v187, v183, v220, v224
	v_cndmask_b32_e64 v179, 1.0, v179, s[36:37]
	v_fma_f32 v188, v184, v221, v225
	v_cndmask_b32_e64 v180, 1.0, v180, s[36:37]
	v_fma_f32 v189, v185, v222, v226
	v_cndmask_b32_e64 v181, 1.0, v181, s[36:37]
	v_cndmask_b32_e64 v223, v223, v186, s[36:37]
	v_mul_f32_e32 v219, v219, v178
	v_cndmask_b32_e64 v224, v224, v187, s[36:37]
	v_mul_f32_e32 v220, v220, v179
	v_cndmask_b32_e64 v225, v225, v188, s[36:37]
	v_mul_f32_e32 v221, v221, v180
	v_cndmask_b32_e64 v226, v226, v189, s[36:37]
	v_mul_f32_e32 v222, v222, v181
	ds_bpermute_b32 v227, v204, v219
	ds_bpermute_b32 v231, v204, v223
	ds_bpermute_b32 v235, v206, v219
	ds_bpermute_b32 v239, v206, v223
	ds_bpermute_b32 v228, v204, v220
	ds_bpermute_b32 v232, v204, v224
	ds_bpermute_b32 v236, v206, v220
	ds_bpermute_b32 v244, v206, v224
	ds_bpermute_b32 v229, v204, v221
	ds_bpermute_b32 v233, v204, v225
	ds_bpermute_b32 v237, v206, v221
	ds_bpermute_b32 v245, v206, v225
	ds_bpermute_b32 v230, v204, v222
	ds_bpermute_b32 v234, v204, v226
	ds_bpermute_b32 v238, v206, v222
	ds_bpermute_b32 v246, v206, v226
	s_waitcnt lgkmcnt(0)
	v_cndmask_b32_e64 v227, 1.0, v227, s[34:35]
	v_cndmask_b32_e64 v231, 0, v231, s[34:35]
	v_cndmask_b32_e64 v228, 1.0, v228, s[34:35]
	v_cndmask_b32_e64 v232, 0, v232, s[34:35]
	v_cndmask_b32_e64 v229, 1.0, v229, s[34:35]
	v_cndmask_b32_e64 v233, 0, v233, s[34:35]
	v_cndmask_b32_e64 v230, 1.0, v230, s[34:35]
	v_cndmask_b32_e64 v234, 0, v234, s[34:35]
	v_mov_b32_e32 v190, v238
	v_mov_b32_e32 v194, v246
	v_mov_b32_e32 v198, v190
	v_mov_b32_e32 v201, v194
	v_fma_f32 v194, v194, v237, v245
	v_mul_f32_e32 v190, v190, v237
	v_mov_b32_e32 v199, v190
	v_mov_b32_e32 v177, v194
	v_fma_f32 v194, v194, v236, v244
	v_mul_f32_e32 v190, v190, v236
	v_mov_b32_e32 v200, v190
	v_mov_b32_e32 v203, v194
	v_fma_f32 v194, v194, v235, v239
	v_mul_f32_e32 v190, v190, v235
	v_mov_b32_e32 v191, v194
	ds_write_b64 v207, v[190:191] offset:1024
	s_cmp_eq_u32 s13, 2
	s_cbranch_scc1 .Lmylru_t0_8
	s_waitcnt vmcnt(40)
	s_branch .Lmylru_t1_8
